# v27 + runs of adjacent s_waitcnt vmcnt(N) (left by the deleted accumulator zeroing) collapsed to the strongest one (86 removed)
# baseline (speedup 1.0000x reference)
; #define PG8_STAGE(bufoff, rs_, soff_, voff) do { _Pragma("unroll") for (int _i = 0; _i < 2; ++_i) \
;         __builtin_amdgcn_raw_ptr_buffer_load_lds(rs_, (LAS void*)(lds + (bufoff) + ldsw + _i * 8192), 16, (int)(voff)[_i], (int)(soff_), 0, 0); } while (0)
; #define PG8_LDA(dst, b, h) do { _Pragma("unroll") for (int m = 0; m < 4; ++m) dst[m] = PG8_LD2(lds + PG8_SA(b, h) + aoff + m * 2048); } while (0)
; #define PG8_LDB(dst, b, h) do { _Pragma("unroll") for (int n = 0; n < 2; ++n) dst[n] = PG8_LD2(lds + PG8_SB(b, h) + boff + n * 2048); } while (0)
; #define PG8_WAIT_V(n) asm volatile("s_waitcnt vmcnt(" #n ")" ::: "memory")
; #define PG8_WAIT_L(n) asm volatile("s_waitcnt lgkmcnt(" #n ")" ::: "memory")
; #define PG8_BAR __builtin_amdgcn_s_barrier()
; #define PG8_SCHED __builtin_amdgcn_sched_barrier(0)
; template <class Epi, class Sched, bool ALIGN_EPI = false, bool SP2 = false, bool FP8 = false>
; __device__ __forceinline__ void gemm_phase(LAS unsigned char* lds, const Gemm g, const Sched& S, const Epi& E, int wbase) {
;     ...
;             PG8_LDB(B0, 0, 0); PG8_LDB(B1, 0, 1); PG8_SCHED; PG8_LDA(At, 0, 0); PG8_STAGE(PG8_SA(1, 1), rAc, a1 + hstep, voffA);
;             PG8_WAIT_V(8); PG8_WAIT_L(0); PG8_BAR; PG8_MMA(0, 0, At, B0); PG8_MMA(0, 1, At, B1); PG8_BAR; PG8_SCHED;
;             PG8_LDA(At, 0, 1); PG8_STAGE(PG8_SB(0, 0), rB2, b2, voffB); PG8_STAGE(PG8_SB(0, 1), rB2, b2 + hstep, voffB); PG8_STAGE(PG8_SA(0, 0), rA2, a2, voffA);
;             PG8_WAIT_V(8); PG8_WAIT_L(0); PG8_BAR; PG8_MMA(1, 0, At, B0); PG8_MMA(1, 1, At, B1); PG8_BAR; PG8_SCHED;
.LBB0_256:
	s_lshl_b32 s82, s1, 18
	s_andn2_b64 vcc, exec, s[66:67]
	s_lshl_b32 s83, s21, 18
	s_cbranch_vccnz .LBB0_260
	s_and_b64 s[2:3], s[26:27], exec
	s_waitcnt vmcnt(22)
	v_mov_b32_e32 v231, v164
	v_mov_b32_e32 v230, 0xff61b1e6
	v_mov_b32_e32 v175, v233
	s_cselect_b32 s2, s82, s29
	s_cselect_b32 s3, s83, s28
	s_add_i32 s16, s29, 0x80
	s_addk_i32 s28, 0x100
	s_mov_b32 s29, 0
	ds_read_b128 v[128:131], v252
	ds_read_b128 v[132:135], v252 offset:1024
	ds_read_b128 v[136:139], v252 offset:2048
	ds_read_b128 v[140:143], v252 offset:3072
	ds_read_b128 v[144:147], v225
	ds_read_b128 v[148:151], v225 offset:1024
	ds_read_b128 v[152:155], v225 offset:2048
	ds_read_b128 v[156:159], v225 offset:3072
	s_add_i32 s6, s16, 0x80
	s_cmp_eq_u32 s18, s29
	s_cselect_b32 s46, s2, s6
	s_cselect_b32 s31, s3, s28
	s_or_b32 s30, s46, 0x80
	s_add_i32 s6, s41, s16
	s_mov_b32 m0, s19
	ds_read_b128 v[176:179], v172
	ds_read_b128 v[180:183], v172 offset:1024
	ds_read_b128 v[184:187], v172 offset:2048
	ds_read_b128 v[188:191], v172 offset:3072
	ds_read_b128 v[194:197], v172 offset:4096
	ds_read_b128 v[198:201], v172 offset:5120
	ds_read_b128 v[202:205], v172 offset:6144
	ds_read_b128 v[206:209], v172 offset:7168
	buffer_load_dwordx4 v192, s[36:39], s6 offen lds
	s_mov_b32 m0, s20
	s_nop 0
	buffer_load_dwordx4 v223, s[36:39], s6 offen lds
	s_waitcnt vmcnt(8)
	s_waitcnt lgkmcnt(0)
	s_barrier
	s_setprio 1
	v_mfma_f32_16x16x128_f8f6f4 v[124:127], v[128:135], v[176:183], 0
	v_mfma_f32_16x16x128_f8f6f4 v[120:123], v[136:143], v[176:183], 0
	v_mfma_f32_16x16x128_f8f6f4 v[108:111], v[128:135], v[184:191], 0
	v_mfma_f32_16x16x128_f8f6f4 v[104:107], v[136:143], v[184:191], 0
	v_mfma_f32_16x16x128_f8f6f4 v[160:163], v[128:135], v[194:201], 0
	v_mfma_f32_16x16x128_f8f6f4 v[210:213], v[136:143], v[194:201], 0
	v_mfma_f32_16x16x128_f8f6f4 v[214:217], v[128:135], v[202:209], 0
	v_mfma_f32_16x16x128_f8f6f4 v[218:221], v[136:143], v[202:209], 0
	v_mfma_f32_16x16x128_f8f6f4 v[116:119], v[144:151], v[176:183], 0
	v_mfma_f32_16x16x128_f8f6f4 v[112:115], v[152:159], v[176:183], 0
	v_mfma_f32_16x16x128_f8f6f4 v[100:103], v[144:151], v[184:191], 0
	v_mfma_f32_16x16x128_f8f6f4 v[96:99], v[152:159], v[184:191], 0
	v_mfma_f32_16x16x128_f8f6f4 v[176:179], v[144:151], v[194:201], 0
	v_mfma_f32_16x16x128_f8f6f4 v[180:183], v[152:159], v[194:201], 0
	v_mfma_f32_16x16x128_f8f6f4 v[184:187], v[144:151], v[202:209], 0
	v_mfma_f32_16x16x128_f8f6f4 v[188:191], v[152:159], v[202:209], 0
	s_setprio 0
	s_barrier
	s_mov_b32 m0, s43
	s_mov_b32 s6, s38
	s_mov_b32 s7, s39
	s_nop 1
	buffer_load_dwordx4 v222, s[4:7], s31 offen lds
	s_mov_b32 m0, s44
	ds_read_b128 v[64:67], v172 offset:16384
	s_add_i32 s47, s31, s41
	buffer_load_dwordx4 v193, s[4:7], s31 offen lds
	s_mov_b32 m0, s45
	ds_read_b128 v[68:71], v172 offset:17408
	buffer_load_dwordx4 v222, s[4:7], s47 offen lds
	s_mov_b32 m0, s42
	ds_read_b128 v[72:75], v172 offset:18432
	buffer_load_dwordx4 v192, s[36:39], s46 offen lds
	s_mov_b32 m0, s53
	ds_read_b128 v[76:79], v172 offset:19456
	buffer_load_dwordx4 v223, s[36:39], s46 offen lds
	ds_read_b128 v[80:83], v172 offset:20480
	ds_read_b128 v[84:87], v172 offset:21504
	ds_read_b128 v[88:91], v172 offset:22528
	ds_read_b128 v[92:95], v172 offset:23552
	s_waitcnt vmcnt(7)
	s_waitcnt lgkmcnt(0)
	s_barrier
	s_setprio 1
	v_mfma_f32_16x16x128_f8f6f4 v[60:63], v[128:135], v[64:71], 0
	v_mfma_f32_16x16x128_f8f6f4 v[56:59], v[136:143], v[64:71], 0
	v_mfma_f32_16x16x128_f8f6f4 v[194:197], v[128:135], v[72:79], 0
	v_mfma_f32_16x16x128_f8f6f4 v[198:201], v[136:143], v[72:79], 0
	v_mfma_f32_16x16x128_f8f6f4 v[202:205], v[128:135], v[80:87], 0
	v_mfma_f32_16x16x128_f8f6f4 v[206:209], v[136:143], v[80:87], 0
	v_mfma_f32_16x16x128_f8f6f4 v[236:239], v[128:135], v[88:95], 0
	v_mfma_f32_16x16x128_f8f6f4 v[240:243], v[136:143], v[88:95], 0
	v_mfma_f32_16x16x128_f8f6f4 v[52:55], v[144:151], v[64:71], 0
	v_mfma_f32_16x16x128_f8f6f4 v[48:51], v[152:159], v[64:71], 0
	v_mfma_f32_16x16x128_f8f6f4 v[244:247], v[144:151], v[72:79], 0
	v_mfma_f32_16x16x128_f8f6f4 v[248:251], v[152:159], v[72:79], 0
	v_mfma_f32_16x16x128_f8f6f4 v[226:229], v[144:151], v[80:87], 0
	v_mfma_f32_16x16x128_f8f6f4 v[232:235], v[152:159], v[80:87], 0
	v_mfma_f32_16x16x128_f8f6f4 v[164:167], v[144:151], v[88:95], 0
	v_mfma_f32_16x16x128_f8f6f4 v[168:171], v[152:159], v[88:95], 0
	s_setprio 0
	s_barrier
; #define PG8_STAGE(bufoff, rs_, soff_, voff) do { _Pragma("unroll") for (int _i = 0; _i < 2; ++_i) \
;         __builtin_amdgcn_raw_ptr_buffer_load_lds(rs_, (LAS void*)(lds + (bufoff) + ldsw + _i * 8192), 16, (int)(voff)[_i], (int)(soff_), 0, 0); } while (0)
; #define PG8_LDA(dst, b, h) do { _Pragma("unroll") for (int m = 0; m < 4; ++m) dst[m] = PG8_LD2(lds + PG8_SA(b, h) + aoff + m * 2048); } while (0)
; #define PG8_LDB(dst, b, h) do { _Pragma("unroll") for (int n = 0; n < 2; ++n) dst[n] = PG8_LD2(lds + PG8_SB(b, h) + boff + n * 2048); } while (0)
; #define PG8_WAIT_V(n) asm volatile("s_waitcnt vmcnt(" #n ")" ::: "memory")
; #define PG8_WAIT_L(n) asm volatile("s_waitcnt lgkmcnt(" #n ")" ::: "memory")
; #define PG8_BAR __builtin_amdgcn_s_barrier()
; #define PG8_SCHED __builtin_amdgcn_sched_barrier(0)
; template <class Epi, class Sched, bool ALIGN_EPI = false, bool SP2 = false, bool FP8 = false>
; __device__ __forceinline__ void gemm_phase(LAS unsigned char* lds, const Gemm g, const Sched& S, const Epi& E, int wbase) {
;     ...
;             PG8_WAIT_V(8); PG8_WAIT_L(0); PG8_BAR; PG8_MMA(1, 0, At, B0); PG8_MMA(1, 1, At, B1); PG8_BAR; PG8_SCHED;
;             PG8_LDB(B0, 1, 0); PG8_LDB(B1, 1, 1); PG8_SCHED; PG8_LDA(At, 1, 0); PG8_STAGE(PG8_SA(0, 1), rA2, a2 + hstep, voffA);
;             PG8_WAIT_V(8); PG8_WAIT_L(0); PG8_BAR; PG8_MMA(0, 0, At, B0); PG8_MMA(0, 1, At, B1); PG8_BAR; PG8_SCHED;
;             PG8_LDA(At, 1, 1); PG8_STAGE(PG8_SB(1, 0), rB2, b3, voffB); PG8_STAGE(PG8_SB(1, 1), rB2, b3 + hstep, voffB); PG8_STAGE(PG8_SA(1, 0), rA2, a3, voffA);
;             PG8_WAIT_V(8); PG8_WAIT_L(0); PG8_BAR; PG8_MMA(1, 0, At, B0); PG8_MMA(1, 1, At, B1); PG8_BAR; PG8_SCHED;
	s_mov_b32 m0, s52
	s_nop 0
	buffer_load_dwordx4 v193, s[4:7], s47 offen lds
	s_nop 4
	ds_read_b128 v[0:3], v173
	ds_read_b128 v[4:7], v173 offset:1024
	ds_read_b128 v[16:19], v173 offset:2048
	ds_read_b128 v[20:23], v173 offset:3072
	ds_read_b128 v[128:131], v174
	ds_read_b128 v[132:135], v174 offset:1024
	ds_read_b128 v[136:139], v174 offset:2048
	ds_read_b128 v[140:143], v174 offset:3072
	s_add_i32 s46, s46, s41
	s_mov_b32 m0, s56
	ds_read_b128 v[8:11], v172 offset:32768
	ds_read_b128 v[12:15], v172 offset:33792
	ds_read_b128 v[24:27], v172 offset:34816
	ds_read_b128 v[28:31], v172 offset:35840
	ds_read_b128 v[32:35], v172 offset:36864
	ds_read_b128 v[36:39], v172 offset:37888
	ds_read_b128 v[40:43], v172 offset:38912
	ds_read_b128 v[44:47], v172 offset:39936
	buffer_load_dwordx4 v192, s[36:39], s46 offen lds
	s_mov_b32 m0, s57
	s_nop 0
	buffer_load_dwordx4 v223, s[36:39], s46 offen lds
	s_waitcnt vmcnt(8)
	s_waitcnt lgkmcnt(0)
	s_barrier
	s_setprio 1
	v_mfma_f32_16x16x128_f8f6f4 v[124:127], v[0:7], v[8:15], v[124:127]
	v_mfma_f32_16x16x128_f8f6f4 v[120:123], v[16:23], v[8:15], v[120:123]
	v_mfma_f32_16x16x128_f8f6f4 v[108:111], v[0:7], v[24:31], v[108:111]
	v_mfma_f32_16x16x128_f8f6f4 v[104:107], v[16:23], v[24:31], v[104:107]
	v_mfma_f32_16x16x128_f8f6f4 v[92:95], v[0:7], v[32:39], v[160:163]
	v_mfma_f32_16x16x128_f8f6f4 v[88:91], v[16:23], v[32:39], v[210:213]
	v_mfma_f32_16x16x128_f8f6f4 v[76:79], v[0:7], v[40:47], v[214:217]
	v_mfma_f32_16x16x128_f8f6f4 v[72:75], v[16:23], v[40:47], v[218:221]
	v_mfma_f32_16x16x128_f8f6f4 v[116:119], v[128:135], v[8:15], v[116:119]
	v_mfma_f32_16x16x128_f8f6f4 v[112:115], v[136:143], v[8:15], v[112:115]
	v_mfma_f32_16x16x128_f8f6f4 v[100:103], v[128:135], v[24:31], v[100:103]
	v_mfma_f32_16x16x128_f8f6f4 v[96:99], v[136:143], v[24:31], v[96:99]
	v_mfma_f32_16x16x128_f8f6f4 v[84:87], v[128:135], v[32:39], v[176:179]
	v_mfma_f32_16x16x128_f8f6f4 v[80:83], v[136:143], v[32:39], v[180:183]
	v_mfma_f32_16x16x128_f8f6f4 v[68:71], v[128:135], v[40:47], v[184:187]
	v_mfma_f32_16x16x128_f8f6f4 v[64:67], v[136:143], v[40:47], v[188:191]
	s_setprio 0
	s_barrier
	s_mov_b32 m0, s58
	s_bitset1_b32 s31, 7
	buffer_load_dwordx4 v222, s[4:7], s31 offen lds
	s_mov_b32 m0, s59
	ds_read_b128 v[32:35], v172 offset:49152
	buffer_load_dwordx4 v193, s[4:7], s31 offen lds
	s_add_i32 s31, s31, s41
	s_mov_b32 m0, s65
	ds_read_b128 v[36:39], v172 offset:50176
	buffer_load_dwordx4 v222, s[4:7], s31 offen lds
	s_mov_b32 m0, s33
	ds_read_b128 v[144:147], v172 offset:51200
	buffer_load_dwordx4 v193, s[4:7], s31 offen lds
	s_mov_b32 m0, s12
	ds_read_b128 v[148:151], v172 offset:52224
	buffer_load_dwordx4 v192, s[36:39], s30 offen lds
	s_mov_b32 m0, s13
	ds_read_b128 v[152:155], v172 offset:53248
	buffer_load_dwordx4 v223, s[36:39], s30 offen lds
	ds_read_b128 v[156:159], v172 offset:54272
	ds_read_b128 v[176:179], v172 offset:55296
	ds_read_b128 v[180:183], v172 offset:56320
	s_waitcnt vmcnt(8)
	s_waitcnt lgkmcnt(0)
	s_barrier
	s_setprio 1
	v_mfma_f32_16x16x128_f8f6f4 v[60:63], v[0:7], v[32:39], v[60:63]
	v_mfma_f32_16x16x128_f8f6f4 v[56:59], v[16:23], v[32:39], v[56:59]
	v_mfma_f32_16x16x128_f8f6f4 v[44:47], v[0:7], v[144:151], v[194:197]
	v_mfma_f32_16x16x128_f8f6f4 v[40:43], v[16:23], v[144:151], v[198:201]
	v_mfma_f32_16x16x128_f8f6f4 v[28:31], v[0:7], v[152:159], v[202:205]
	v_mfma_f32_16x16x128_f8f6f4 v[24:27], v[16:23], v[152:159], v[206:209]
	v_mfma_f32_16x16x128_f8f6f4 v[12:15], v[0:7], v[176:183], v[236:239]
	v_mfma_f32_16x16x128_f8f6f4 v[8:11], v[16:23], v[176:183], v[240:243]
	v_mfma_f32_16x16x128_f8f6f4 v[52:55], v[128:135], v[32:39], v[52:55]
	v_mfma_f32_16x16x128_f8f6f4 v[48:51], v[136:143], v[32:39], v[48:51]
	v_mfma_f32_16x16x128_f8f6f4 v[36:39], v[128:135], v[144:151], v[244:247]
	v_mfma_f32_16x16x128_f8f6f4 v[32:35], v[136:143], v[144:151], v[248:251]
	v_mfma_f32_16x16x128_f8f6f4 v[20:23], v[128:135], v[152:159], v[226:229]
	v_mfma_f32_16x16x128_f8f6f4 v[16:19], v[136:143], v[152:159], v[232:235]
	v_mfma_f32_16x16x128_f8f6f4 v[4:7], v[128:135], v[176:183], v[164:167]
	v_mfma_f32_16x16x128_f8f6f4 v[0:3], v[136:143], v[176:183], v[168:171]
	s_setprio 0
	s_barrier
	s_add_i32 s29, s29, 2
	s_addk_i32 s16, 0x100
	s_addk_i32 s28, 0x100
	s_cmp_ge_i32 s29, s77
	s_cbranch_scc0 .LBB0_258
	s_branch .Lzp_after_258

;     __device__ __forceinline__ unsigned a_off(const Unit& u, const Gemm& g) const { return (unsigned)u.pm * (unsigned)(BM * 2) * (unsigned)g.K; }
;     __device__ __forceinline__ unsigned b_off(const Unit& u, const Gemm& g) const { return (unsigned)u.pn * (unsigned)(BM * 2) * (unsigned)g.K; }
;     __device__ __forceinline__ bool next(int i, Unit& u) const { return so.next(i, u); }
;     __device__ __forceinline__ unsigned a_off(const Unit& u, const Gemm& g) const { return (unsigned)u.pm * (unsigned)(BM * 2) * (unsigned)g.K; }
;     __device__ __forceinline__ bool next(int i, Unit& u) const { const bool ok = so.next(i >> 1, u); u.part = i & 1; return ok; }
; template <class Epi, class Sched, bool ALIGN_EPI = false, bool SP2 = false, bool FP8 = false>
; __device__ __forceinline__ void gemm_phase(LAS unsigned char* lds, const Gemm g, const Sched& S, const Epi& E, int wbase) {
;     ...
;         const bool has_next = S.next(ui + 1, nxt);
;         const unsigned nA = has_next ? S.a_off(nxt, g) : cA, nB = has_next ? S.b_off(nxt, g) : cB;
;         const rsrc_t rAn = (Sched::TWO && has_next) ? (nxt.part ? rA1 : rA0) : rAc, rBn = (Sched::TWO && has_next) ? (nxt.part ? rB1 : rB0) : rBc;
;         float pre_[8] = {0.f, 0.f, 0.f, 0.f, 0.f, 0.f, 0.f, 0.f};
;         if constexpr (Epi::HAS_PRE) E.pre_load(pre_, cur, wr);
;         for (int t = 0; t < nt; t += 2) {
;             const bool last = (t == nt - 2);
;             const unsigned a1 = cA + (unsigned)(t + 1) * kstep;
;             const unsigned a2 = last ? nA : cA + (unsigned)(t + 2) * kstep, b2 = last ? nB : cB + (unsigned)(t + 2) * kstep; const rsrc_t rA2 = (Sched::TWO && last) ? rAn : rAc, rB2 = (Sched::TWO && last) ? rBn : rBc;
;             const unsigned a3 = a2 + kstep, b3 = b2 + kstep;
;             if (last && has_next) S.a_ready(nxt);
;             if constexpr (SP2) {
;             PG8_LDB(B0, 0, 0); PG8_LDB(B1, 0, 1); PG8_SCHED; PG8_LDA(At, 0, 0); PG8_STAGE(PG8_SA(1, 1), rAc, a1 + hstep, voffA);
;             PG8_WAIT_V(8); PG8_WAIT_L(0); PG8_BAR; PG8_MMA(0, 0, At, B0); PG8_MMA(0, 1, At, B1); PG8_BAR; PG8_SCHED;
;             PG8_LDA(At, 0, 1); PG8_STAGE(PG8_SB(0, 0), rB2, b2, voffB); PG8_STAGE(PG8_SB(0, 1), rB2, b2 + hstep, voffB); PG8_STAGE(PG8_SA(0, 0), rA2, a2, voffA);
;             PG8_WAIT_V(8); PG8_WAIT_L(0); PG8_BAR; PG8_MMA(1, 0, At, B0); PG8_MMA(1, 1, At, B1); PG8_BAR; PG8_SCHED;
.LBB0_350:
	s_lshl_b32 s20, s19, 19
	s_andn2_b64 vcc, exec, s[66:67]
	s_lshl_b32 s21, s18, 19
	s_cbranch_vccnz .LBB0_430
	s_and_b64 s[2:3], s[26:27], exec
	s_waitcnt vmcnt(22)
	s_cselect_b32 s2, s20, s29
	s_cselect_b32 s3, s21, s28
	s_add_i32 s16, s29, 0x80
	s_addk_i32 s28, 0x100
	s_mov_b32 s29, 0
	v_add_u32_e32 v140, 0x10000, v170
	v_add_u32_e32 v156, 0x14000, v170
	ds_read_b128 v[128:131], v140
	ds_read_b128 v[132:135], v140 offset:1024
	ds_read_b128 v[136:139], v140 offset:2048
	ds_read_b128 v[140:143], v140 offset:3072
	ds_read_b128 v[144:147], v156
	ds_read_b128 v[148:151], v156 offset:1024
	ds_read_b128 v[152:155], v156 offset:2048
	ds_read_b128 v[156:159], v156 offset:3072
	s_add_i32 s6, s16, 0x80
	s_cmp_eq_u32 s12, s29
	s_cselect_b32 s46, s2, s6
	s_cselect_b32 s31, s3, s28
	s_or_b32 s30, s46, 0x80
	s_add_i32 s6, s33, s16
	s_mov_b32 m0, s13
	ds_read_b128 v[160:163], v171
	ds_read_b128 v[172:175], v171 offset:1024
	ds_read_b128 v[176:179], v171 offset:2048
	ds_read_b128 v[180:183], v171 offset:3072
	ds_read_b128 v[184:187], v171 offset:4096
	ds_read_b128 v[188:191], v171 offset:5120
	ds_read_b128 v[194:197], v171 offset:6144
	ds_read_b128 v[198:201], v171 offset:7168
	buffer_load_dwordx4 v164, s[36:39], s6 offen lds
	s_mov_b32 m0, s83
	s_nop 0
	buffer_load_dwordx4 v166, s[36:39], s6 offen lds
	s_waitcnt vmcnt(8)
	s_waitcnt lgkmcnt(0)
	s_barrier
	s_setprio 1
	v_mfma_f32_16x16x32_bf16 v[124:127], v[128:131], v[160:163], 0
	v_mfma_f32_16x16x32_bf16 v[120:123], v[136:139], v[160:163], 0
	v_mfma_f32_16x16x32_bf16 v[108:111], v[128:131], v[176:179], 0
	v_mfma_f32_16x16x32_bf16 v[104:107], v[136:139], v[176:179], 0
	v_mfma_f32_16x16x32_bf16 v[92:95], v[128:131], v[184:187], 0
	v_mfma_f32_16x16x32_bf16 v[88:91], v[136:139], v[184:187], 0
	v_mfma_f32_16x16x32_bf16 v[76:79], v[128:131], v[194:197], 0
	v_mfma_f32_16x16x32_bf16 v[72:75], v[136:139], v[194:197], 0
	v_mfma_f32_16x16x32_bf16 v[124:127], v[132:135], v[172:175], v[124:127]
	v_mfma_f32_16x16x32_bf16 v[120:123], v[140:143], v[172:175], v[120:123]
	v_mfma_f32_16x16x32_bf16 v[108:111], v[132:135], v[180:183], v[108:111]
	v_mfma_f32_16x16x32_bf16 v[104:107], v[140:143], v[180:183], v[104:107]
	v_mfma_f32_16x16x32_bf16 v[92:95], v[132:135], v[188:191], v[92:95]
	v_mfma_f32_16x16x32_bf16 v[88:91], v[140:143], v[188:191], v[88:91]
	v_mfma_f32_16x16x32_bf16 v[76:79], v[132:135], v[198:201], v[76:79]
	v_mfma_f32_16x16x32_bf16 v[72:75], v[140:143], v[198:201], v[72:75]
	v_mfma_f32_16x16x32_bf16 v[116:119], v[144:147], v[160:163], 0
	v_mfma_f32_16x16x32_bf16 v[112:115], v[152:155], v[160:163], 0
	v_mfma_f32_16x16x32_bf16 v[100:103], v[144:147], v[176:179], 0
	v_mfma_f32_16x16x32_bf16 v[96:99], v[152:155], v[176:179], 0
	v_mfma_f32_16x16x32_bf16 v[84:87], v[144:147], v[184:187], 0
	v_mfma_f32_16x16x32_bf16 v[80:83], v[152:155], v[184:187], 0
	v_mfma_f32_16x16x32_bf16 v[68:71], v[144:147], v[194:197], 0
	v_mfma_f32_16x16x32_bf16 v[64:67], v[152:155], v[194:197], 0
	v_mfma_f32_16x16x32_bf16 v[116:119], v[148:151], v[172:175], v[116:119]
	v_mfma_f32_16x16x32_bf16 v[112:115], v[156:159], v[172:175], v[112:115]
	v_mfma_f32_16x16x32_bf16 v[100:103], v[148:151], v[180:183], v[100:103]
	v_mfma_f32_16x16x32_bf16 v[96:99], v[156:159], v[180:183], v[96:99]
	v_mfma_f32_16x16x32_bf16 v[84:87], v[148:151], v[188:191], v[84:87]
	v_mfma_f32_16x16x32_bf16 v[80:83], v[156:159], v[188:191], v[80:83]
	v_mfma_f32_16x16x32_bf16 v[68:71], v[148:151], v[198:201], v[68:71]
	v_mfma_f32_16x16x32_bf16 v[64:67], v[156:159], v[198:201], v[64:67]
	s_setprio 0
	s_barrier
	s_mov_b32 m0, s42
	s_mov_b32 s6, s38
	s_mov_b32 s7, s39
	buffer_load_dwordx4 v165, s[4:7], s31 offen lds
	s_mov_b32 m0, s43
	ds_read_b128 v[160:163], v171 offset:16384
	s_add_i32 s47, s31, s33
	buffer_load_dwordx4 v167, s[4:7], s31 offen lds
	s_mov_b32 m0, s44
	ds_read_b128 v[172:175], v171 offset:17408
	buffer_load_dwordx4 v165, s[4:7], s47 offen lds
	s_mov_b32 m0, s41
	ds_read_b128 v[176:179], v171 offset:18432
	buffer_load_dwordx4 v164, s[36:39], s46 offen lds
	s_mov_b32 m0, s52
	ds_read_b128 v[180:183], v171 offset:19456
	buffer_load_dwordx4 v166, s[36:39], s46 offen lds
	ds_read_b128 v[184:187], v171 offset:20480
	ds_read_b128 v[188:191], v171 offset:21504
	ds_read_b128 v[194:197], v171 offset:22528
	ds_read_b128 v[198:201], v171 offset:23552
	s_waitcnt vmcnt(7)
	s_waitcnt lgkmcnt(0)
	s_barrier
	s_setprio 1
	v_mfma_f32_16x16x32_bf16 v[60:63], v[128:131], v[160:163], 0
	v_mfma_f32_16x16x32_bf16 v[56:59], v[136:139], v[160:163], 0
	v_mfma_f32_16x16x32_bf16 v[44:47], v[128:131], v[176:179], 0
	v_mfma_f32_16x16x32_bf16 v[40:43], v[136:139], v[176:179], 0
	v_mfma_f32_16x16x32_bf16 v[28:31], v[128:131], v[184:187], 0
	v_mfma_f32_16x16x32_bf16 v[24:27], v[136:139], v[184:187], 0
	v_mfma_f32_16x16x32_bf16 v[12:15], v[128:131], v[194:197], 0
	v_mfma_f32_16x16x32_bf16 v[8:11], v[136:139], v[194:197], 0
	v_mfma_f32_16x16x32_bf16 v[60:63], v[132:135], v[172:175], v[60:63]
	v_mfma_f32_16x16x32_bf16 v[56:59], v[140:143], v[172:175], v[56:59]
	v_mfma_f32_16x16x32_bf16 v[44:47], v[132:135], v[180:183], v[44:47]
	v_mfma_f32_16x16x32_bf16 v[40:43], v[140:143], v[180:183], v[40:43]
	v_mfma_f32_16x16x32_bf16 v[28:31], v[132:135], v[188:191], v[28:31]
	v_mfma_f32_16x16x32_bf16 v[24:27], v[140:143], v[188:191], v[24:27]
	v_mfma_f32_16x16x32_bf16 v[12:15], v[132:135], v[198:201], v[12:15]
	v_mfma_f32_16x16x32_bf16 v[8:11], v[140:143], v[198:201], v[8:11]
	v_mfma_f32_16x16x32_bf16 v[52:55], v[144:147], v[160:163], 0
	v_mfma_f32_16x16x32_bf16 v[48:51], v[152:155], v[160:163], 0
	v_mfma_f32_16x16x32_bf16 v[36:39], v[144:147], v[176:179], 0
	v_mfma_f32_16x16x32_bf16 v[32:35], v[152:155], v[176:179], 0
	v_mfma_f32_16x16x32_bf16 v[20:23], v[144:147], v[184:187], 0
	v_mfma_f32_16x16x32_bf16 v[16:19], v[152:155], v[184:187], 0
	v_mfma_f32_16x16x32_bf16 v[4:7], v[144:147], v[194:197], 0
	v_mfma_f32_16x16x32_bf16 v[0:3], v[152:155], v[194:197], 0
	v_mfma_f32_16x16x32_bf16 v[52:55], v[148:151], v[172:175], v[52:55]
	v_mfma_f32_16x16x32_bf16 v[48:51], v[156:159], v[172:175], v[48:51]
	v_mfma_f32_16x16x32_bf16 v[36:39], v[148:151], v[180:183], v[36:39]
	v_mfma_f32_16x16x32_bf16 v[32:35], v[156:159], v[180:183], v[32:35]
	v_mfma_f32_16x16x32_bf16 v[20:23], v[148:151], v[188:191], v[20:23]
	v_mfma_f32_16x16x32_bf16 v[16:19], v[156:159], v[188:191], v[16:19]
	v_mfma_f32_16x16x32_bf16 v[4:7], v[148:151], v[198:201], v[4:7]
	v_mfma_f32_16x16x32_bf16 v[0:3], v[156:159], v[198:201], v[0:3]
	s_setprio 0
	s_barrier
; #define PG8_STAGE(bufoff, rs_, soff_, voff) do { _Pragma("unroll") for (int _i = 0; _i < 2; ++_i) \
;         __builtin_amdgcn_raw_ptr_buffer_load_lds(rs_, (LAS void*)(lds + (bufoff) + ldsw + _i * 8192), 16, (int)(voff)[_i], (int)(soff_), 0, 0); } while (0)
; #define PG8_LDA(dst, b, h) do { _Pragma("unroll") for (int m = 0; m < 4; ++m) dst[m] = PG8_LD2(lds + PG8_SA(b, h) + aoff + m * 2048); } while (0)
; #define PG8_LDB(dst, b, h) do { _Pragma("unroll") for (int n = 0; n < 2; ++n) dst[n] = PG8_LD2(lds + PG8_SB(b, h) + boff + n * 2048); } while (0)
; #define PG8_WAIT_V(n) asm volatile("s_waitcnt vmcnt(" #n ")" ::: "memory")
; #define PG8_WAIT_L(n) asm volatile("s_waitcnt lgkmcnt(" #n ")" ::: "memory")
; #define PG8_BAR __builtin_amdgcn_s_barrier()
; #define PG8_SCHED __builtin_amdgcn_sched_barrier(0)
; template <class Epi, class Sched, bool ALIGN_EPI = false, bool SP2 = false, bool FP8 = false>
; __device__ __forceinline__ void gemm_phase(LAS unsigned char* lds, const Gemm g, const Sched& S, const Epi& E, int wbase) {
;     ...
;             PG8_LDB(B0, 1, 0); PG8_LDB(B1, 1, 1); PG8_SCHED; PG8_LDA(At, 1, 0); PG8_STAGE(PG8_SA(0, 1), rA2, a2 + hstep, voffA);
;             PG8_WAIT_V(8); PG8_WAIT_L(0); PG8_BAR; PG8_MMA(0, 0, At, B0); PG8_MMA(0, 1, At, B1); PG8_BAR; PG8_SCHED;
;             PG8_LDA(At, 1, 1); PG8_STAGE(PG8_SB(1, 0), rB2, b3, voffB); PG8_STAGE(PG8_SB(1, 1), rB2, b3 + hstep, voffB); PG8_STAGE(PG8_SA(1, 0), rA2, a3, voffA);
;             PG8_WAIT_V(8); PG8_WAIT_L(0); PG8_BAR; PG8_MMA(1, 0, At, B0); PG8_MMA(1, 1, At, B1); PG8_BAR; PG8_SCHED;
	s_mov_b32 m0, s45
	s_nop 0
	buffer_load_dwordx4 v167, s[4:7], s47 offen lds
	v_add_u32_e32 v140, 0x18000, v170
	v_add_u32_e32 v156, 0x1c000, v170
	ds_read_b128 v[128:131], v140
	ds_read_b128 v[132:135], v140 offset:1024
	ds_read_b128 v[136:139], v140 offset:2048
	ds_read_b128 v[140:143], v140 offset:3072
	ds_read_b128 v[144:147], v156
	ds_read_b128 v[148:151], v156 offset:1024
	ds_read_b128 v[152:155], v156 offset:2048
	ds_read_b128 v[156:159], v156 offset:3072
	s_add_i32 s46, s46, s33
	s_mov_b32 m0, s53
	ds_read_b128 v[160:163], v171 offset:32768
	ds_read_b128 v[172:175], v171 offset:33792
	ds_read_b128 v[176:179], v171 offset:34816
	ds_read_b128 v[180:183], v171 offset:35840
	ds_read_b128 v[184:187], v171 offset:36864
	ds_read_b128 v[188:191], v171 offset:37888
	ds_read_b128 v[194:197], v171 offset:38912
	ds_read_b128 v[198:201], v171 offset:39936
	buffer_load_dwordx4 v164, s[36:39], s46 offen lds
	s_mov_b32 m0, s1
	s_nop 0
	buffer_load_dwordx4 v166, s[36:39], s46 offen lds
	s_waitcnt vmcnt(8)
	s_waitcnt lgkmcnt(0)
	s_barrier
	s_setprio 1
	v_mfma_f32_16x16x32_bf16 v[124:127], v[128:131], v[160:163], v[124:127]
	v_mfma_f32_16x16x32_bf16 v[120:123], v[136:139], v[160:163], v[120:123]
	v_mfma_f32_16x16x32_bf16 v[108:111], v[128:131], v[176:179], v[108:111]
	v_mfma_f32_16x16x32_bf16 v[104:107], v[136:139], v[176:179], v[104:107]
	v_mfma_f32_16x16x32_bf16 v[92:95], v[128:131], v[184:187], v[92:95]
	v_mfma_f32_16x16x32_bf16 v[88:91], v[136:139], v[184:187], v[88:91]
	v_mfma_f32_16x16x32_bf16 v[76:79], v[128:131], v[194:197], v[76:79]
	v_mfma_f32_16x16x32_bf16 v[72:75], v[136:139], v[194:197], v[72:75]
	v_mfma_f32_16x16x32_bf16 v[124:127], v[132:135], v[172:175], v[124:127]
	v_mfma_f32_16x16x32_bf16 v[120:123], v[140:143], v[172:175], v[120:123]
	v_mfma_f32_16x16x32_bf16 v[108:111], v[132:135], v[180:183], v[108:111]
	v_mfma_f32_16x16x32_bf16 v[104:107], v[140:143], v[180:183], v[104:107]
	v_mfma_f32_16x16x32_bf16 v[92:95], v[132:135], v[188:191], v[92:95]
	v_mfma_f32_16x16x32_bf16 v[88:91], v[140:143], v[188:191], v[88:91]
	v_mfma_f32_16x16x32_bf16 v[76:79], v[132:135], v[198:201], v[76:79]
	v_mfma_f32_16x16x32_bf16 v[72:75], v[140:143], v[198:201], v[72:75]
	v_mfma_f32_16x16x32_bf16 v[116:119], v[144:147], v[160:163], v[116:119]
	v_mfma_f32_16x16x32_bf16 v[112:115], v[152:155], v[160:163], v[112:115]
	v_mfma_f32_16x16x32_bf16 v[100:103], v[144:147], v[176:179], v[100:103]
	v_mfma_f32_16x16x32_bf16 v[96:99], v[152:155], v[176:179], v[96:99]
	v_mfma_f32_16x16x32_bf16 v[84:87], v[144:147], v[184:187], v[84:87]
	v_mfma_f32_16x16x32_bf16 v[80:83], v[152:155], v[184:187], v[80:83]
	v_mfma_f32_16x16x32_bf16 v[68:71], v[144:147], v[194:197], v[68:71]
	v_mfma_f32_16x16x32_bf16 v[64:67], v[152:155], v[194:197], v[64:67]
	v_mfma_f32_16x16x32_bf16 v[116:119], v[148:151], v[172:175], v[116:119]
	v_mfma_f32_16x16x32_bf16 v[112:115], v[156:159], v[172:175], v[112:115]
	v_mfma_f32_16x16x32_bf16 v[100:103], v[148:151], v[180:183], v[100:103]
	v_mfma_f32_16x16x32_bf16 v[96:99], v[156:159], v[180:183], v[96:99]
	v_mfma_f32_16x16x32_bf16 v[84:87], v[148:151], v[188:191], v[84:87]
	v_mfma_f32_16x16x32_bf16 v[80:83], v[156:159], v[188:191], v[80:83]
	v_mfma_f32_16x16x32_bf16 v[68:71], v[148:151], v[198:201], v[68:71]
	v_mfma_f32_16x16x32_bf16 v[64:67], v[156:159], v[198:201], v[64:67]
	s_setprio 0
	s_barrier
	s_mov_b32 m0, s56
	s_bitset1_b32 s31, 7
	buffer_load_dwordx4 v165, s[4:7], s31 offen lds
	s_mov_b32 m0, s57
	ds_read_b128 v[160:163], v171 offset:49152
	buffer_load_dwordx4 v167, s[4:7], s31 offen lds
	s_add_i32 s31, s31, s33
	s_mov_b32 m0, s65
	ds_read_b128 v[172:175], v171 offset:50176
	buffer_load_dwordx4 v165, s[4:7], s31 offen lds
	s_mov_b32 m0, s76
	ds_read_b128 v[176:179], v171 offset:51200
	buffer_load_dwordx4 v167, s[4:7], s31 offen lds
	s_mov_b32 m0, s58
	ds_read_b128 v[180:183], v171 offset:52224
	buffer_load_dwordx4 v164, s[36:39], s30 offen lds
	s_mov_b32 m0, s59
	ds_read_b128 v[184:187], v171 offset:53248
	buffer_load_dwordx4 v166, s[36:39], s30 offen lds
	ds_read_b128 v[188:191], v171 offset:54272
	ds_read_b128 v[194:197], v171 offset:55296
	ds_read_b128 v[198:201], v171 offset:56320
	s_waitcnt vmcnt(8)
	s_waitcnt lgkmcnt(0)
	s_barrier
	s_setprio 1
	v_mfma_f32_16x16x32_bf16 v[60:63], v[128:131], v[160:163], v[60:63]
	v_mfma_f32_16x16x32_bf16 v[56:59], v[136:139], v[160:163], v[56:59]
	v_mfma_f32_16x16x32_bf16 v[44:47], v[128:131], v[176:179], v[44:47]
	v_mfma_f32_16x16x32_bf16 v[40:43], v[136:139], v[176:179], v[40:43]
	v_mfma_f32_16x16x32_bf16 v[28:31], v[128:131], v[184:187], v[28:31]
	v_mfma_f32_16x16x32_bf16 v[24:27], v[136:139], v[184:187], v[24:27]
	v_mfma_f32_16x16x32_bf16 v[12:15], v[128:131], v[194:197], v[12:15]
	v_mfma_f32_16x16x32_bf16 v[8:11], v[136:139], v[194:197], v[8:11]
	v_mfma_f32_16x16x32_bf16 v[60:63], v[132:135], v[172:175], v[60:63]
	v_mfma_f32_16x16x32_bf16 v[56:59], v[140:143], v[172:175], v[56:59]
	v_mfma_f32_16x16x32_bf16 v[44:47], v[132:135], v[180:183], v[44:47]
	v_mfma_f32_16x16x32_bf16 v[40:43], v[140:143], v[180:183], v[40:43]
	v_mfma_f32_16x16x32_bf16 v[28:31], v[132:135], v[188:191], v[28:31]
	v_mfma_f32_16x16x32_bf16 v[24:27], v[140:143], v[188:191], v[24:27]
	v_mfma_f32_16x16x32_bf16 v[12:15], v[132:135], v[198:201], v[12:15]
	v_mfma_f32_16x16x32_bf16 v[8:11], v[140:143], v[198:201], v[8:11]
	v_mfma_f32_16x16x32_bf16 v[52:55], v[144:147], v[160:163], v[52:55]
	v_mfma_f32_16x16x32_bf16 v[48:51], v[152:155], v[160:163], v[48:51]
	v_mfma_f32_16x16x32_bf16 v[36:39], v[144:147], v[176:179], v[36:39]
	v_mfma_f32_16x16x32_bf16 v[32:35], v[152:155], v[176:179], v[32:35]
	v_mfma_f32_16x16x32_bf16 v[20:23], v[144:147], v[184:187], v[20:23]
	v_mfma_f32_16x16x32_bf16 v[16:19], v[152:155], v[184:187], v[16:19]
	v_mfma_f32_16x16x32_bf16 v[4:7], v[144:147], v[194:197], v[4:7]
	v_mfma_f32_16x16x32_bf16 v[0:3], v[152:155], v[194:197], v[0:3]
	v_mfma_f32_16x16x32_bf16 v[52:55], v[148:151], v[172:175], v[52:55]
	v_mfma_f32_16x16x32_bf16 v[48:51], v[156:159], v[172:175], v[48:51]
	v_mfma_f32_16x16x32_bf16 v[36:39], v[148:151], v[180:183], v[36:39]
	v_mfma_f32_16x16x32_bf16 v[32:35], v[156:159], v[180:183], v[32:35]
	v_mfma_f32_16x16x32_bf16 v[20:23], v[148:151], v[188:191], v[20:23]
	v_mfma_f32_16x16x32_bf16 v[16:19], v[156:159], v[188:191], v[16:19]
	v_mfma_f32_16x16x32_bf16 v[4:7], v[148:151], v[198:201], v[4:7]
	v_mfma_f32_16x16x32_bf16 v[0:3], v[156:159], v[198:201], v[0:3]
	s_setprio 0
	s_barrier
	s_add_i32 s29, s29, 2
	s_addk_i32 s16, 0x100
	s_addk_i32 s28, 0x100
	s_cmp_ge_i32 s29, s82
	s_cbranch_scc0 .LBB0_352
	s_branch .Lzp_after_352

;     __device__ __forceinline__ unsigned a_off(const Unit& u, const Gemm& g) const { return (unsigned)u.pm * (unsigned)(BM * 2) * (unsigned)g.K; }
;     __device__ __forceinline__ unsigned b_off(const Unit& u, const Gemm& g) const { return (unsigned)u.pn * (unsigned)(BM * 2) * (unsigned)g.K; }
;     __device__ __forceinline__ bool next(int i, Unit& u) const { return so.next(i, u); }
;     __device__ __forceinline__ unsigned a_off(const Unit& u, const Gemm& g) const { return (unsigned)u.pm * (unsigned)(BM * 2) * (unsigned)g.K; }
;     __device__ __forceinline__ bool next(int i, Unit& u) const { const bool ok = so.next(i >> 1, u); u.part = i & 1; return ok; }
; template <class Epi, class Sched, bool ALIGN_EPI = false, bool SP2 = false, bool FP8 = false>
; __device__ __forceinline__ void gemm_phase(LAS unsigned char* lds, const Gemm g, const Sched& S, const Epi& E, int wbase) {
;     ...
;         const bool has_next = S.next(ui + 1, nxt);
;         const unsigned nA = has_next ? S.a_off(nxt, g) : cA, nB = has_next ? S.b_off(nxt, g) : cB;
;         const rsrc_t rAn = (Sched::TWO && has_next) ? (nxt.part ? rA1 : rA0) : rAc, rBn = (Sched::TWO && has_next) ? (nxt.part ? rB1 : rB0) : rBc;
;         float pre_[8] = {0.f, 0.f, 0.f, 0.f, 0.f, 0.f, 0.f, 0.f};
;         if constexpr (Epi::HAS_PRE) E.pre_load(pre_, cur, wr);
;         for (int t = 0; t < nt; t += 2) {
;             const bool last = (t == nt - 2);
;             const unsigned a1 = cA + (unsigned)(t + 1) * kstep;
;             const unsigned a2 = last ? nA : cA + (unsigned)(t + 2) * kstep, b2 = last ? nB : cB + (unsigned)(t + 2) * kstep; const rsrc_t rA2 = (Sched::TWO && last) ? rAn : rAc, rB2 = (Sched::TWO && last) ? rBn : rBc;
;             const unsigned a3 = a2 + kstep, b3 = b2 + kstep;
;             if (last && has_next) S.a_ready(nxt);
;             if constexpr (SP2) {
;             PG8_LDB(B0, 0, 0); PG8_LDB(B1, 0, 1); PG8_SCHED; PG8_LDA(At, 0, 0); PG8_STAGE(PG8_SA(1, 1), rAc, a1 + hstep, voffA);
;             PG8_WAIT_V(8); PG8_WAIT_L(0); PG8_BAR; PG8_MMA(0, 0, At, B0); PG8_MMA(0, 1, At, B1); PG8_BAR; PG8_SCHED;
;             PG8_LDA(At, 0, 1); PG8_STAGE(PG8_SB(0, 0), rB2, b2, voffB); PG8_STAGE(PG8_SB(0, 1), rB2, b2 + hstep, voffB); PG8_STAGE(PG8_SA(0, 0), rA2, a2, voffA);
;             PG8_WAIT_V(8); PG8_WAIT_L(0); PG8_BAR; PG8_MMA(1, 0, At, B0); PG8_MMA(1, 1, At, B1); PG8_BAR; PG8_SCHED;
.LBB0_448:
	s_lshl_b32 s48, s47, 17
	s_andn2_b64 vcc, exec, s[10:11]
	s_lshl_b32 s52, s46, 17
	s_cbranch_vccnz .LBB0_456
	s_and_b64 s[6:7], s[16:17], exec
	s_waitcnt vmcnt(22)
	s_cselect_b32 s56, s48, s55
	s_cselect_b32 s57, s52, s54
	s_add_i32 s58, s55, 0x80
	s_add_i32 s59, s54, 0x100
	s_mov_b32 s60, 0
	v_add_u32_e32 v148, 0x10000, v138
	v_add_u32_e32 v164, 0x14000, v138
	ds_read_b128 v[128:131], v148
	ds_read_b128 v[140:143], v148 offset:1024
	ds_read_b128 v[144:147], v148 offset:2048
	ds_read_b128 v[148:151], v148 offset:3072
	ds_read_b128 v[152:155], v164
	ds_read_b128 v[156:159], v164 offset:1024
	ds_read_b128 v[160:163], v164 offset:2048
	ds_read_b128 v[164:167], v164 offset:3072
	s_add_i32 s6, s58, 0x80
	s_cmp_eq_u32 s42, s60
	s_cselect_b32 s61, s56, s6
	s_cselect_b32 s55, s57, s59
	s_or_b32 s54, s61, 0x80
	s_add_i32 s6, s19, s58
	s_mov_b32 m0, s43
	ds_read_b128 v[168:171], v139
	ds_read_b128 v[172:175], v139 offset:1024
	ds_read_b128 v[176:179], v139 offset:2048
	ds_read_b128 v[180:183], v139 offset:3072
	ds_read_b128 v[184:187], v139 offset:4096
	ds_read_b128 v[188:191], v139 offset:5120
	ds_read_b128 v[194:197], v139 offset:6144
	ds_read_b128 v[198:201], v139 offset:7168
	buffer_load_dwordx4 v132, s[36:39], s6 offen lds
	s_mov_b32 m0, s44
	s_nop 0
	buffer_load_dwordx4 v134, s[36:39], s6 offen lds
	s_waitcnt vmcnt(8)
	s_waitcnt lgkmcnt(0)
	s_barrier
	s_setprio 1
	v_mfma_f32_16x16x32_bf16 v[124:127], v[128:131], v[168:171], 0
	v_mfma_f32_16x16x32_bf16 v[120:123], v[144:147], v[168:171], 0
	v_mfma_f32_16x16x32_bf16 v[108:111], v[128:131], v[176:179], 0
	v_mfma_f32_16x16x32_bf16 v[104:107], v[144:147], v[176:179], 0
	v_mfma_f32_16x16x32_bf16 v[92:95], v[128:131], v[184:187], 0
	v_mfma_f32_16x16x32_bf16 v[88:91], v[144:147], v[184:187], 0
	v_mfma_f32_16x16x32_bf16 v[76:79], v[128:131], v[194:197], 0
	v_mfma_f32_16x16x32_bf16 v[72:75], v[144:147], v[194:197], 0
	v_mfma_f32_16x16x32_bf16 v[124:127], v[140:143], v[172:175], v[124:127]
	v_mfma_f32_16x16x32_bf16 v[120:123], v[148:151], v[172:175], v[120:123]
	v_mfma_f32_16x16x32_bf16 v[108:111], v[140:143], v[180:183], v[108:111]
	v_mfma_f32_16x16x32_bf16 v[104:107], v[148:151], v[180:183], v[104:107]
	v_mfma_f32_16x16x32_bf16 v[92:95], v[140:143], v[188:191], v[92:95]
	v_mfma_f32_16x16x32_bf16 v[88:91], v[148:151], v[188:191], v[88:91]
	v_mfma_f32_16x16x32_bf16 v[76:79], v[140:143], v[198:201], v[76:79]
	v_mfma_f32_16x16x32_bf16 v[72:75], v[148:151], v[198:201], v[72:75]
	v_mfma_f32_16x16x32_bf16 v[116:119], v[152:155], v[168:171], 0
	v_mfma_f32_16x16x32_bf16 v[112:115], v[160:163], v[168:171], 0
	v_mfma_f32_16x16x32_bf16 v[100:103], v[152:155], v[176:179], 0
	v_mfma_f32_16x16x32_bf16 v[96:99], v[160:163], v[176:179], 0
	v_mfma_f32_16x16x32_bf16 v[84:87], v[152:155], v[184:187], 0
	v_mfma_f32_16x16x32_bf16 v[80:83], v[160:163], v[184:187], 0
	v_mfma_f32_16x16x32_bf16 v[68:71], v[152:155], v[194:197], 0
	v_mfma_f32_16x16x32_bf16 v[64:67], v[160:163], v[194:197], 0
	v_mfma_f32_16x16x32_bf16 v[116:119], v[156:159], v[172:175], v[116:119]
	v_mfma_f32_16x16x32_bf16 v[112:115], v[164:167], v[172:175], v[112:115]
	v_mfma_f32_16x16x32_bf16 v[100:103], v[156:159], v[180:183], v[100:103]
	v_mfma_f32_16x16x32_bf16 v[96:99], v[164:167], v[180:183], v[96:99]
	v_mfma_f32_16x16x32_bf16 v[84:87], v[156:159], v[188:191], v[84:87]
	v_mfma_f32_16x16x32_bf16 v[80:83], v[164:167], v[188:191], v[80:83]
	v_mfma_f32_16x16x32_bf16 v[68:71], v[156:159], v[198:201], v[68:71]
	v_mfma_f32_16x16x32_bf16 v[64:67], v[164:167], v[198:201], v[64:67]
	s_setprio 0
	s_barrier
	s_mov_b32 m0, s21
	s_mov_b32 s6, s38
	s_mov_b32 s7, s39
	buffer_load_dwordx4 v133, s[4:7], s55 offen lds
	s_mov_b32 m0, s22
	ds_read_b128 v[168:171], v139 offset:16384
	s_add_i32 s62, s55, s19
	buffer_load_dwordx4 v135, s[4:7], s55 offen lds
	s_mov_b32 m0, s23
	ds_read_b128 v[172:175], v139 offset:17408
	buffer_load_dwordx4 v133, s[4:7], s62 offen lds
	s_mov_b32 m0, s20
	ds_read_b128 v[176:179], v139 offset:18432
	buffer_load_dwordx4 v132, s[36:39], s61 offen lds
	s_mov_b32 m0, s25
	ds_read_b128 v[180:183], v139 offset:19456
	buffer_load_dwordx4 v134, s[36:39], s61 offen lds
	ds_read_b128 v[184:187], v139 offset:20480
	ds_read_b128 v[188:191], v139 offset:21504
	ds_read_b128 v[194:197], v139 offset:22528
	ds_read_b128 v[198:201], v139 offset:23552
	s_waitcnt vmcnt(7)
	s_waitcnt lgkmcnt(0)
	s_barrier
	s_setprio 1
	v_mfma_f32_16x16x32_bf16 v[60:63], v[128:131], v[168:171], 0
	v_mfma_f32_16x16x32_bf16 v[56:59], v[144:147], v[168:171], 0
	v_mfma_f32_16x16x32_bf16 v[44:47], v[128:131], v[176:179], 0
	v_mfma_f32_16x16x32_bf16 v[40:43], v[144:147], v[176:179], 0
	v_mfma_f32_16x16x32_bf16 v[28:31], v[128:131], v[184:187], 0
	v_mfma_f32_16x16x32_bf16 v[24:27], v[144:147], v[184:187], 0
	v_mfma_f32_16x16x32_bf16 v[12:15], v[128:131], v[194:197], 0
	v_mfma_f32_16x16x32_bf16 v[8:11], v[144:147], v[194:197], 0
	v_mfma_f32_16x16x32_bf16 v[60:63], v[140:143], v[172:175], v[60:63]
	v_mfma_f32_16x16x32_bf16 v[56:59], v[148:151], v[172:175], v[56:59]
	v_mfma_f32_16x16x32_bf16 v[44:47], v[140:143], v[180:183], v[44:47]
	v_mfma_f32_16x16x32_bf16 v[40:43], v[148:151], v[180:183], v[40:43]
	v_mfma_f32_16x16x32_bf16 v[28:31], v[140:143], v[188:191], v[28:31]
	v_mfma_f32_16x16x32_bf16 v[24:27], v[148:151], v[188:191], v[24:27]
	v_mfma_f32_16x16x32_bf16 v[12:15], v[140:143], v[198:201], v[12:15]
	v_mfma_f32_16x16x32_bf16 v[8:11], v[148:151], v[198:201], v[8:11]
	v_mfma_f32_16x16x32_bf16 v[52:55], v[152:155], v[168:171], 0
	v_mfma_f32_16x16x32_bf16 v[48:51], v[160:163], v[168:171], 0
	v_mfma_f32_16x16x32_bf16 v[36:39], v[152:155], v[176:179], 0
	v_mfma_f32_16x16x32_bf16 v[32:35], v[160:163], v[176:179], 0
	v_mfma_f32_16x16x32_bf16 v[20:23], v[152:155], v[184:187], 0
	v_mfma_f32_16x16x32_bf16 v[16:19], v[160:163], v[184:187], 0
	v_mfma_f32_16x16x32_bf16 v[4:7], v[152:155], v[194:197], 0
	v_mfma_f32_16x16x32_bf16 v[0:3], v[160:163], v[194:197], 0
	v_mfma_f32_16x16x32_bf16 v[52:55], v[156:159], v[172:175], v[52:55]
	v_mfma_f32_16x16x32_bf16 v[48:51], v[164:167], v[172:175], v[48:51]
	v_mfma_f32_16x16x32_bf16 v[36:39], v[156:159], v[180:183], v[36:39]
	v_mfma_f32_16x16x32_bf16 v[32:35], v[164:167], v[180:183], v[32:35]
	v_mfma_f32_16x16x32_bf16 v[20:23], v[156:159], v[188:191], v[20:23]
	v_mfma_f32_16x16x32_bf16 v[16:19], v[164:167], v[188:191], v[16:19]
	v_mfma_f32_16x16x32_bf16 v[4:7], v[156:159], v[198:201], v[4:7]
	v_mfma_f32_16x16x32_bf16 v[0:3], v[164:167], v[198:201], v[0:3]
	s_setprio 0
	s_barrier
; #define PG8_STAGE(bufoff, rs_, soff_, voff) do { _Pragma("unroll") for (int _i = 0; _i < 2; ++_i) \
;         __builtin_amdgcn_raw_ptr_buffer_load_lds(rs_, (LAS void*)(lds + (bufoff) + ldsw + _i * 8192), 16, (int)(voff)[_i], (int)(soff_), 0, 0); } while (0)
; #define PG8_LDA(dst, b, h) do { _Pragma("unroll") for (int m = 0; m < 4; ++m) dst[m] = PG8_LD2(lds + PG8_SA(b, h) + aoff + m * 2048); } while (0)
; #define PG8_LDB(dst, b, h) do { _Pragma("unroll") for (int n = 0; n < 2; ++n) dst[n] = PG8_LD2(lds + PG8_SB(b, h) + boff + n * 2048); } while (0)
; #define PG8_WAIT_V(n) asm volatile("s_waitcnt vmcnt(" #n ")" ::: "memory")
; #define PG8_WAIT_L(n) asm volatile("s_waitcnt lgkmcnt(" #n ")" ::: "memory")
; #define PG8_BAR __builtin_amdgcn_s_barrier()
; #define PG8_SCHED __builtin_amdgcn_sched_barrier(0)
; template <class Epi, class Sched, bool ALIGN_EPI = false, bool SP2 = false, bool FP8 = false>
; __device__ __forceinline__ void gemm_phase(LAS unsigned char* lds, const Gemm g, const Sched& S, const Epi& E, int wbase) {
;     ...
;             PG8_LDB(B0, 1, 0); PG8_LDB(B1, 1, 1); PG8_SCHED; PG8_LDA(At, 1, 0); PG8_STAGE(PG8_SA(0, 1), rA2, a2 + hstep, voffA);
;             PG8_WAIT_V(8); PG8_WAIT_L(0); PG8_BAR; PG8_MMA(0, 0, At, B0); PG8_MMA(0, 1, At, B1); PG8_BAR; PG8_SCHED;
;             PG8_LDA(At, 1, 1); PG8_STAGE(PG8_SB(1, 0), rB2, b3, voffB); PG8_STAGE(PG8_SB(1, 1), rB2, b3 + hstep, voffB); PG8_STAGE(PG8_SA(1, 0), rA2, a3, voffA);
;             PG8_WAIT_V(8); PG8_WAIT_L(0); PG8_BAR; PG8_MMA(1, 0, At, B0); PG8_MMA(1, 1, At, B1); PG8_BAR; PG8_SCHED;
	s_mov_b32 m0, s24
	s_nop 0
	buffer_load_dwordx4 v135, s[4:7], s62 offen lds
	v_add_u32_e32 v148, 0x18000, v138
	v_add_u32_e32 v164, 0x1c000, v138
	ds_read_b128 v[128:131], v148
	ds_read_b128 v[140:143], v148 offset:1024
	ds_read_b128 v[144:147], v148 offset:2048
	ds_read_b128 v[148:151], v148 offset:3072
	ds_read_b128 v[152:155], v164
	ds_read_b128 v[156:159], v164 offset:1024
	ds_read_b128 v[160:163], v164 offset:2048
	ds_read_b128 v[164:167], v164 offset:3072
	s_add_i32 s61, s61, s19
	s_mov_b32 m0, s26
	ds_read_b128 v[168:171], v139 offset:32768
	ds_read_b128 v[172:175], v139 offset:33792
	ds_read_b128 v[176:179], v139 offset:34816
	ds_read_b128 v[180:183], v139 offset:35840
	ds_read_b128 v[184:187], v139 offset:36864
	ds_read_b128 v[188:191], v139 offset:37888
	ds_read_b128 v[194:197], v139 offset:38912
	ds_read_b128 v[198:201], v139 offset:39936
	buffer_load_dwordx4 v132, s[36:39], s61 offen lds
	s_mov_b32 m0, s27
	s_nop 0
	buffer_load_dwordx4 v134, s[36:39], s61 offen lds
	s_waitcnt vmcnt(8)
	s_waitcnt lgkmcnt(0)
	s_barrier
	s_setprio 1
	v_mfma_f32_16x16x32_bf16 v[124:127], v[128:131], v[168:171], v[124:127]
	v_mfma_f32_16x16x32_bf16 v[120:123], v[144:147], v[168:171], v[120:123]
	v_mfma_f32_16x16x32_bf16 v[108:111], v[128:131], v[176:179], v[108:111]
	v_mfma_f32_16x16x32_bf16 v[104:107], v[144:147], v[176:179], v[104:107]
	v_mfma_f32_16x16x32_bf16 v[92:95], v[128:131], v[184:187], v[92:95]
	v_mfma_f32_16x16x32_bf16 v[88:91], v[144:147], v[184:187], v[88:91]
	v_mfma_f32_16x16x32_bf16 v[76:79], v[128:131], v[194:197], v[76:79]
	v_mfma_f32_16x16x32_bf16 v[72:75], v[144:147], v[194:197], v[72:75]
	v_mfma_f32_16x16x32_bf16 v[124:127], v[140:143], v[172:175], v[124:127]
	v_mfma_f32_16x16x32_bf16 v[120:123], v[148:151], v[172:175], v[120:123]
	v_mfma_f32_16x16x32_bf16 v[108:111], v[140:143], v[180:183], v[108:111]
	v_mfma_f32_16x16x32_bf16 v[104:107], v[148:151], v[180:183], v[104:107]
	v_mfma_f32_16x16x32_bf16 v[92:95], v[140:143], v[188:191], v[92:95]
	v_mfma_f32_16x16x32_bf16 v[88:91], v[148:151], v[188:191], v[88:91]
	v_mfma_f32_16x16x32_bf16 v[76:79], v[140:143], v[198:201], v[76:79]
	v_mfma_f32_16x16x32_bf16 v[72:75], v[148:151], v[198:201], v[72:75]
	v_mfma_f32_16x16x32_bf16 v[116:119], v[152:155], v[168:171], v[116:119]
	v_mfma_f32_16x16x32_bf16 v[112:115], v[160:163], v[168:171], v[112:115]
	v_mfma_f32_16x16x32_bf16 v[100:103], v[152:155], v[176:179], v[100:103]
	v_mfma_f32_16x16x32_bf16 v[96:99], v[160:163], v[176:179], v[96:99]
	v_mfma_f32_16x16x32_bf16 v[84:87], v[152:155], v[184:187], v[84:87]
	v_mfma_f32_16x16x32_bf16 v[80:83], v[160:163], v[184:187], v[80:83]
	v_mfma_f32_16x16x32_bf16 v[68:71], v[152:155], v[194:197], v[68:71]
	v_mfma_f32_16x16x32_bf16 v[64:67], v[160:163], v[194:197], v[64:67]
	v_mfma_f32_16x16x32_bf16 v[116:119], v[156:159], v[172:175], v[116:119]
	v_mfma_f32_16x16x32_bf16 v[112:115], v[164:167], v[172:175], v[112:115]
	v_mfma_f32_16x16x32_bf16 v[100:103], v[156:159], v[180:183], v[100:103]
	v_mfma_f32_16x16x32_bf16 v[96:99], v[164:167], v[180:183], v[96:99]
	v_mfma_f32_16x16x32_bf16 v[84:87], v[156:159], v[188:191], v[84:87]
	v_mfma_f32_16x16x32_bf16 v[80:83], v[164:167], v[188:191], v[80:83]
	v_mfma_f32_16x16x32_bf16 v[68:71], v[156:159], v[198:201], v[68:71]
	v_mfma_f32_16x16x32_bf16 v[64:67], v[164:167], v[198:201], v[64:67]
	s_setprio 0
	s_barrier
	s_mov_b32 m0, s28
	s_bitset1_b32 s55, 7
	buffer_load_dwordx4 v133, s[4:7], s55 offen lds
	s_mov_b32 m0, s29
	ds_read_b128 v[168:171], v139 offset:49152
	buffer_load_dwordx4 v135, s[4:7], s55 offen lds
	s_add_i32 s55, s55, s19
	s_mov_b32 m0, s33
	ds_read_b128 v[172:175], v139 offset:50176
	buffer_load_dwordx4 v133, s[4:7], s55 offen lds
	s_mov_b32 m0, s34
	ds_read_b128 v[176:179], v139 offset:51200
	buffer_load_dwordx4 v135, s[4:7], s55 offen lds
	s_mov_b32 m0, s30
	ds_read_b128 v[180:183], v139 offset:52224
	buffer_load_dwordx4 v132, s[36:39], s54 offen lds
	s_mov_b32 m0, s31
	ds_read_b128 v[184:187], v139 offset:53248
	buffer_load_dwordx4 v134, s[36:39], s54 offen lds
	ds_read_b128 v[188:191], v139 offset:54272
	ds_read_b128 v[194:197], v139 offset:55296
	ds_read_b128 v[198:201], v139 offset:56320
	s_waitcnt vmcnt(8)
	s_waitcnt lgkmcnt(0)
	s_barrier
	s_setprio 1
	v_mfma_f32_16x16x32_bf16 v[60:63], v[128:131], v[168:171], v[60:63]
	v_mfma_f32_16x16x32_bf16 v[56:59], v[144:147], v[168:171], v[56:59]
	v_mfma_f32_16x16x32_bf16 v[44:47], v[128:131], v[176:179], v[44:47]
	v_mfma_f32_16x16x32_bf16 v[40:43], v[144:147], v[176:179], v[40:43]
	v_mfma_f32_16x16x32_bf16 v[28:31], v[128:131], v[184:187], v[28:31]
	v_mfma_f32_16x16x32_bf16 v[24:27], v[144:147], v[184:187], v[24:27]
	v_mfma_f32_16x16x32_bf16 v[12:15], v[128:131], v[194:197], v[12:15]
	v_mfma_f32_16x16x32_bf16 v[8:11], v[144:147], v[194:197], v[8:11]
	v_mfma_f32_16x16x32_bf16 v[60:63], v[140:143], v[172:175], v[60:63]
	v_mfma_f32_16x16x32_bf16 v[56:59], v[148:151], v[172:175], v[56:59]
	v_mfma_f32_16x16x32_bf16 v[44:47], v[140:143], v[180:183], v[44:47]
	v_mfma_f32_16x16x32_bf16 v[40:43], v[148:151], v[180:183], v[40:43]
	v_mfma_f32_16x16x32_bf16 v[28:31], v[140:143], v[188:191], v[28:31]
	v_mfma_f32_16x16x32_bf16 v[24:27], v[148:151], v[188:191], v[24:27]
	v_mfma_f32_16x16x32_bf16 v[12:15], v[140:143], v[198:201], v[12:15]
	v_mfma_f32_16x16x32_bf16 v[8:11], v[148:151], v[198:201], v[8:11]
	v_mfma_f32_16x16x32_bf16 v[52:55], v[152:155], v[168:171], v[52:55]
	v_mfma_f32_16x16x32_bf16 v[48:51], v[160:163], v[168:171], v[48:51]
	v_mfma_f32_16x16x32_bf16 v[36:39], v[152:155], v[176:179], v[36:39]
	v_mfma_f32_16x16x32_bf16 v[32:35], v[160:163], v[176:179], v[32:35]
	v_mfma_f32_16x16x32_bf16 v[20:23], v[152:155], v[184:187], v[20:23]
	v_mfma_f32_16x16x32_bf16 v[16:19], v[160:163], v[184:187], v[16:19]
	v_mfma_f32_16x16x32_bf16 v[4:7], v[152:155], v[194:197], v[4:7]
	v_mfma_f32_16x16x32_bf16 v[0:3], v[160:163], v[194:197], v[0:3]
	v_mfma_f32_16x16x32_bf16 v[52:55], v[156:159], v[172:175], v[52:55]
	v_mfma_f32_16x16x32_bf16 v[48:51], v[164:167], v[172:175], v[48:51]
	v_mfma_f32_16x16x32_bf16 v[36:39], v[156:159], v[180:183], v[36:39]
	v_mfma_f32_16x16x32_bf16 v[32:35], v[164:167], v[180:183], v[32:35]
	v_mfma_f32_16x16x32_bf16 v[20:23], v[156:159], v[188:191], v[20:23]
	v_mfma_f32_16x16x32_bf16 v[16:19], v[164:167], v[188:191], v[16:19]
	v_mfma_f32_16x16x32_bf16 v[4:7], v[156:159], v[198:201], v[4:7]
	v_mfma_f32_16x16x32_bf16 v[0:3], v[164:167], v[198:201], v[0:3]
	s_setprio 0
	s_barrier
	s_add_i32 s60, s60, 2
	s_addk_i32 s58, 0x100
	s_addk_i32 s59, 0x100
	s_cmp_ge_i32 s60, s35
	s_cbranch_scc0 .LBB0_450
	s_branch .Lzp_after_450

;     __device__ __forceinline__ unsigned a_off(const Unit& u, const Gemm& g) const { return (unsigned)u.pm * (unsigned)(BM * 2) * (unsigned)g.K; }
;     __device__ __forceinline__ unsigned b_off(const Unit& u, const Gemm& g) const { return (unsigned)u.pn * (unsigned)(BM * 2) * (unsigned)g.K; }
;     __device__ __forceinline__ bool next(int i, Unit& u) const { return so.next(i, u); }
;     __device__ __forceinline__ unsigned a_off(const Unit& u, const Gemm& g) const { return (unsigned)u.pm * (unsigned)(BM * 2) * (unsigned)g.K; }
;     __device__ __forceinline__ bool next(int i, Unit& u) const { const bool ok = so.next(i >> 1, u); u.part = i & 1; return ok; }
; template <class Epi, class Sched, bool ALIGN_EPI = false, bool SP2 = false, bool FP8 = false>
; __device__ __forceinline__ void gemm_phase(LAS unsigned char* lds, const Gemm g, const Sched& S, const Epi& E, int wbase) {
;     ...
;         const bool has_next = S.next(ui + 1, nxt);
;         const unsigned nA = has_next ? S.a_off(nxt, g) : cA, nB = has_next ? S.b_off(nxt, g) : cB;
;         const rsrc_t rAn = (Sched::TWO && has_next) ? (nxt.part ? rA1 : rA0) : rAc, rBn = (Sched::TWO && has_next) ? (nxt.part ? rB1 : rB0) : rBc;
;         float pre_[8] = {0.f, 0.f, 0.f, 0.f, 0.f, 0.f, 0.f, 0.f};
;         if constexpr (Epi::HAS_PRE) E.pre_load(pre_, cur, wr);
;         for (int t = 0; t < nt; t += 2) {
;             const bool last = (t == nt - 2);
;             const unsigned a1 = cA + (unsigned)(t + 1) * kstep;
;             const unsigned a2 = last ? nA : cA + (unsigned)(t + 2) * kstep, b2 = last ? nB : cB + (unsigned)(t + 2) * kstep; const rsrc_t rA2 = (Sched::TWO && last) ? rAn : rAc, rB2 = (Sched::TWO && last) ? rBn : rBc;
;             const unsigned a3 = a2 + kstep, b3 = b2 + kstep;
;             if (last && has_next) S.a_ready(nxt);
;             if constexpr (SP2) {
;             PG8_LDB(B0, 0, 0); PG8_LDB(B1, 0, 1); PG8_SCHED; PG8_LDA(At, 0, 0); PG8_STAGE(PG8_SA(1, 1), rAc, a1 + hstep, voffA);
;             PG8_WAIT_V(8); PG8_WAIT_L(0); PG8_BAR; PG8_MMA(0, 0, At, B0); PG8_MMA(0, 1, At, B1); PG8_BAR; PG8_SCHED;
;             PG8_LDA(At, 0, 1); PG8_STAGE(PG8_SB(0, 0), rB2, b2, voffB); PG8_STAGE(PG8_SB(0, 1), rB2, b2 + hstep, voffB); PG8_STAGE(PG8_SA(0, 0), rA2, a2, voffA);
;             PG8_WAIT_V(8); PG8_WAIT_L(0); PG8_BAR; PG8_MMA(1, 0, At, B0); PG8_MMA(1, 1, At, B1); PG8_BAR; PG8_SCHED;
.LBB0_924:
	s_lshl_b32 s79, s77, 18
	s_andn2_b64 vcc, exec, s[22:23]
	s_lshl_b32 s80, s76, 18
	s_cbranch_vccnz .LBB0_928
	s_and_b64 s[2:3], s[26:27], exec
	s_waitcnt vmcnt(23)
	v_mov_b32_e32 v159, v233
	s_cselect_b32 s2, s79, s4
	s_cselect_b32 s3, s80, s5
	s_addk_i32 s4, 0x80
	s_addk_i32 s5, 0x100
	s_mov_b32 s11, 0
	s_waitcnt vmcnt(0)
	v_add_u32_e32 v120, 0x10000, v160
	ds_read_b128 v[132:135], v120
	ds_read_b128 v[136:139], v120 offset:1024
	ds_read_b128 v[140:143], v120 offset:2048
	ds_read_b128 v[144:147], v120 offset:3072
	v_add_u32_e32 v120, 0x14000, v160
	ds_read_b128 v[162:165], v120
	ds_read_b128 v[166:169], v120 offset:1024
	ds_read_b128 v[170:173], v120 offset:2048
	ds_read_b128 v[174:177], v120 offset:3072
	s_add_i32 s14, s4, 0x80
	s_cmp_eq_u32 s60, s11
	s_cselect_b32 s66, s2, s14
	s_cselect_b32 s55, s3, s5
	s_or_b32 s54, s66, 0x80
	s_add_i32 s14, s30, s4
	s_mov_b32 m0, s61
	ds_read_b128 v[178:181], v161
	ds_read_b128 v[182:185], v161 offset:1024
	ds_read_b128 v[194:197], v161 offset:2048
	ds_read_b128 v[198:201], v161 offset:3072
	ds_read_b128 v[202:205], v161 offset:4096
	ds_read_b128 v[206:209], v161 offset:5120
	ds_read_b128 v[210:213], v161 offset:6144
	ds_read_b128 v[214:217], v161 offset:7168
	buffer_load_dwordx4 v222, s[36:39], s14 offen lds
	s_mov_b32 m0, s62
	s_nop 0
	buffer_load_dwordx4 v156, s[36:39], s14 offen lds
	s_waitcnt vmcnt(8)
	s_waitcnt lgkmcnt(0)
	s_barrier
	s_setprio 1
	v_mfma_f32_16x16x128_f8f6f4 v[124:127], v[140:147], v[178:185], 0
	v_mfma_f32_16x16x128_f8f6f4 v[108:111], v[132:139], v[194:201], 0
	v_mfma_f32_16x16x128_f8f6f4 v[104:107], v[140:147], v[194:201], 0
	v_mfma_f32_16x16x128_f8f6f4 v[120:123], v[132:139], v[178:185], 0
	v_mfma_f32_16x16x128_f8f6f4 v[148:151], v[132:139], v[202:209], 0
	v_mfma_f32_16x16x128_f8f6f4 v[186:189], v[140:147], v[202:209], 0
	v_mfma_f32_16x16x128_f8f6f4 v[218:221], v[132:139], v[210:217], 0
	v_mfma_f32_16x16x128_f8f6f4 v[226:229], v[140:147], v[210:217], 0
	v_mfma_f32_16x16x128_f8f6f4 v[116:119], v[162:169], v[178:185], 0
	v_mfma_f32_16x16x128_f8f6f4 v[112:115], v[170:177], v[178:185], 0
	v_mfma_f32_16x16x128_f8f6f4 v[100:103], v[162:169], v[194:201], 0
	v_mfma_f32_16x16x128_f8f6f4 v[96:99], v[170:177], v[194:201], 0
	v_mfma_f32_16x16x128_f8f6f4 v[178:181], v[162:169], v[202:209], 0
	v_mfma_f32_16x16x128_f8f6f4 v[182:185], v[170:177], v[202:209], 0
	v_mfma_f32_16x16x128_f8f6f4 v[194:197], v[162:169], v[210:217], 0
	v_mfma_f32_16x16x128_f8f6f4 v[198:201], v[170:177], v[210:217], 0
	s_setprio 0
	s_barrier
	s_mov_b32 m0, s33
	s_mov_b32 s14, s38
	s_mov_b32 s15, s39
	s_nop 1
	buffer_load_dwordx4 v223, s[12:15], s55 offen lds
	s_mov_b32 m0, s34
	ds_read_b128 v[64:67], v161 offset:16384
	s_add_i32 s67, s55, s30
	buffer_load_dwordx4 v157, s[12:15], s55 offen lds
	s_mov_b32 m0, s35
	ds_read_b128 v[68:71], v161 offset:17408
	buffer_load_dwordx4 v223, s[12:15], s67 offen lds
	s_mov_b32 m0, s31
	ds_read_b128 v[72:75], v161 offset:18432
	buffer_load_dwordx4 v222, s[36:39], s66 offen lds
	s_mov_b32 m0, s42
	ds_read_b128 v[76:79], v161 offset:19456
	buffer_load_dwordx4 v156, s[36:39], s66 offen lds
	ds_read_b128 v[80:83], v161 offset:20480
	ds_read_b128 v[84:87], v161 offset:21504
	ds_read_b128 v[88:91], v161 offset:22528
	ds_read_b128 v[92:95], v161 offset:23552
	s_waitcnt vmcnt(7)
	s_waitcnt lgkmcnt(0)
	s_barrier
	s_setprio 1
	v_mfma_f32_16x16x128_f8f6f4 v[60:63], v[132:139], v[64:71], 0
	v_mfma_f32_16x16x128_f8f6f4 v[56:59], v[140:147], v[64:71], 0
	v_mfma_f32_16x16x128_f8f6f4 v[202:205], v[132:139], v[72:79], 0
	v_mfma_f32_16x16x128_f8f6f4 v[206:209], v[140:147], v[72:79], 0
	v_mfma_f32_16x16x128_f8f6f4 v[210:213], v[132:139], v[80:87], 0
	v_mfma_f32_16x16x128_f8f6f4 v[214:217], v[140:147], v[80:87], 0
	v_mfma_f32_16x16x128_f8f6f4 v[230:233], v[132:139], v[88:95], 0
	v_mfma_f32_16x16x128_f8f6f4 v[234:237], v[140:147], v[88:95], 0
	v_mfma_f32_16x16x128_f8f6f4 v[52:55], v[162:169], v[64:71], 0
	v_mfma_f32_16x16x128_f8f6f4 v[48:51], v[170:177], v[64:71], 0
	v_mfma_f32_16x16x128_f8f6f4 v[238:241], v[162:169], v[72:79], 0
	v_mfma_f32_16x16x128_f8f6f4 v[242:245], v[170:177], v[72:79], 0
	v_mfma_f32_16x16x128_f8f6f4 v[246:249], v[162:169], v[80:87], 0
	v_mfma_f32_16x16x128_f8f6f4 v[250:253], v[170:177], v[80:87], 0
	v_mfma_f32_16x16x128_f8f6f4 v[190:193], v[162:169], v[88:95], 0
	v_mfma_f32_16x16x128_f8f6f4 v[152:155], v[170:177], v[88:95], 0
	s_setprio 0
	s_barrier
; #define PG8_STAGE(bufoff, rs_, soff_, voff) do { _Pragma("unroll") for (int _i = 0; _i < 2; ++_i) \
;         __builtin_amdgcn_raw_ptr_buffer_load_lds(rs_, (LAS void*)(lds + (bufoff) + ldsw + _i * 8192), 16, (int)(voff)[_i], (int)(soff_), 0, 0); } while (0)
; #define PG8_LDA(dst, b, h) do { _Pragma("unroll") for (int m = 0; m < 4; ++m) dst[m] = PG8_LD2(lds + PG8_SA(b, h) + aoff + m * 2048); } while (0)
; #define PG8_LDB(dst, b, h) do { _Pragma("unroll") for (int n = 0; n < 2; ++n) dst[n] = PG8_LD2(lds + PG8_SB(b, h) + boff + n * 2048); } while (0)
; #define PG8_WAIT_V(n) asm volatile("s_waitcnt vmcnt(" #n ")" ::: "memory")
; #define PG8_WAIT_L(n) asm volatile("s_waitcnt lgkmcnt(" #n ")" ::: "memory")
; #define PG8_BAR __builtin_amdgcn_s_barrier()
; #define PG8_SCHED __builtin_amdgcn_sched_barrier(0)
; template <class Epi, class Sched, bool ALIGN_EPI = false, bool SP2 = false, bool FP8 = false>
; __device__ __forceinline__ void gemm_phase(LAS unsigned char* lds, const Gemm g, const Sched& S, const Epi& E, int wbase) {
;     ...
;             PG8_LDB(B0, 1, 0); PG8_LDB(B1, 1, 1); PG8_SCHED; PG8_LDA(At, 1, 0); PG8_STAGE(PG8_SA(0, 1), rA2, a2 + hstep, voffA);
;             PG8_WAIT_V(8); PG8_WAIT_L(0); PG8_BAR; PG8_MMA(0, 0, At, B0); PG8_MMA(0, 1, At, B1); PG8_BAR; PG8_SCHED;
;             PG8_LDA(At, 1, 1); PG8_STAGE(PG8_SB(1, 0), rB2, b3, voffB); PG8_STAGE(PG8_SB(1, 1), rB2, b3 + hstep, voffB); PG8_STAGE(PG8_SA(1, 0), rA2, a3, voffA);
;             PG8_WAIT_V(8); PG8_WAIT_L(0); PG8_BAR; PG8_MMA(1, 0, At, B0); PG8_MMA(1, 1, At, B1); PG8_BAR; PG8_SCHED;
	s_mov_b32 m0, s41
	s_nop 0
	buffer_load_dwordx4 v157, s[12:15], s67 offen lds
	v_add_u32_e32 v8, 0x18000, v160
	s_nop 3
	ds_read_b128 v[0:3], v8
	ds_read_b128 v[4:7], v8 offset:1024
	ds_read_b128 v[16:19], v8 offset:2048
	ds_read_b128 v[20:23], v8 offset:3072
	v_add_u32_e32 v8, 0x1c000, v160
	ds_read_b128 v[132:135], v8
	ds_read_b128 v[136:139], v8 offset:1024
	ds_read_b128 v[140:143], v8 offset:2048
	ds_read_b128 v[144:147], v8 offset:3072
	s_add_i32 s66, s66, s30
	s_mov_b32 m0, s43
	ds_read_b128 v[8:11], v161 offset:32768
	ds_read_b128 v[12:15], v161 offset:33792
	ds_read_b128 v[24:27], v161 offset:34816
	ds_read_b128 v[28:31], v161 offset:35840
	ds_read_b128 v[32:35], v161 offset:36864
	ds_read_b128 v[36:39], v161 offset:37888
	ds_read_b128 v[40:43], v161 offset:38912
	ds_read_b128 v[44:47], v161 offset:39936
	buffer_load_dwordx4 v222, s[36:39], s66 offen lds
	s_mov_b32 m0, s44
	s_nop 0
	buffer_load_dwordx4 v156, s[36:39], s66 offen lds
	s_waitcnt vmcnt(8)
	s_waitcnt lgkmcnt(0)
	s_barrier
	s_setprio 1
	v_mfma_f32_16x16x128_f8f6f4 v[128:131], v[0:7], v[8:15], v[120:123]
	v_mfma_f32_16x16x128_f8f6f4 v[124:127], v[16:23], v[8:15], v[124:127]
	v_mfma_f32_16x16x128_f8f6f4 v[108:111], v[0:7], v[24:31], v[108:111]
	v_mfma_f32_16x16x128_f8f6f4 v[104:107], v[16:23], v[24:31], v[104:107]
	v_mfma_f32_16x16x128_f8f6f4 v[92:95], v[0:7], v[32:39], v[148:151]
	v_mfma_f32_16x16x128_f8f6f4 v[88:91], v[16:23], v[32:39], v[186:189]
	v_mfma_f32_16x16x128_f8f6f4 v[76:79], v[0:7], v[40:47], v[218:221]
	v_mfma_f32_16x16x128_f8f6f4 v[72:75], v[16:23], v[40:47], v[226:229]
	v_mfma_f32_16x16x128_f8f6f4 v[116:119], v[132:139], v[8:15], v[116:119]
	v_mfma_f32_16x16x128_f8f6f4 v[112:115], v[140:147], v[8:15], v[112:115]
	v_mfma_f32_16x16x128_f8f6f4 v[100:103], v[132:139], v[24:31], v[100:103]
	v_mfma_f32_16x16x128_f8f6f4 v[96:99], v[140:147], v[24:31], v[96:99]
	v_mfma_f32_16x16x128_f8f6f4 v[84:87], v[132:139], v[32:39], v[178:181]
	v_mfma_f32_16x16x128_f8f6f4 v[80:83], v[140:147], v[32:39], v[182:185]
	v_mfma_f32_16x16x128_f8f6f4 v[68:71], v[132:139], v[40:47], v[194:197]
	v_mfma_f32_16x16x128_f8f6f4 v[64:67], v[140:147], v[40:47], v[198:201]
	s_setprio 0
	s_barrier
	s_mov_b32 m0, s45
	s_bitset1_b32 s55, 7
	buffer_load_dwordx4 v223, s[12:15], s55 offen lds
	s_mov_b32 m0, s46
	ds_read_b128 v[32:35], v161 offset:49152
	buffer_load_dwordx4 v157, s[12:15], s55 offen lds
	s_add_i32 s55, s55, s30
	s_mov_b32 m0, s52
	ds_read_b128 v[36:39], v161 offset:50176
	buffer_load_dwordx4 v223, s[12:15], s55 offen lds
	s_mov_b32 m0, s53
	ds_read_b128 v[162:165], v161 offset:51200
	buffer_load_dwordx4 v157, s[12:15], s55 offen lds
	s_mov_b32 m0, s47
	ds_read_b128 v[166:169], v161 offset:52224
	buffer_load_dwordx4 v222, s[36:39], s54 offen lds
	s_mov_b32 m0, s48
	ds_read_b128 v[170:173], v161 offset:53248
	buffer_load_dwordx4 v156, s[36:39], s54 offen lds
	ds_read_b128 v[174:177], v161 offset:54272
	ds_read_b128 v[178:181], v161 offset:55296
	ds_read_b128 v[182:185], v161 offset:56320
	s_waitcnt vmcnt(8)
	s_waitcnt lgkmcnt(0)
	s_barrier
	s_setprio 1
	v_mfma_f32_16x16x128_f8f6f4 v[60:63], v[0:7], v[32:39], v[60:63]
	v_mfma_f32_16x16x128_f8f6f4 v[56:59], v[16:23], v[32:39], v[56:59]
	v_mfma_f32_16x16x128_f8f6f4 v[44:47], v[0:7], v[162:169], v[202:205]
	v_mfma_f32_16x16x128_f8f6f4 v[40:43], v[16:23], v[162:169], v[206:209]
	v_mfma_f32_16x16x128_f8f6f4 v[28:31], v[0:7], v[170:177], v[210:213]
	v_mfma_f32_16x16x128_f8f6f4 v[24:27], v[16:23], v[170:177], v[214:217]
	v_mfma_f32_16x16x128_f8f6f4 v[12:15], v[0:7], v[178:185], v[230:233]
	v_mfma_f32_16x16x128_f8f6f4 v[8:11], v[16:23], v[178:185], v[234:237]
	v_mfma_f32_16x16x128_f8f6f4 v[52:55], v[132:139], v[32:39], v[52:55]
	v_mfma_f32_16x16x128_f8f6f4 v[48:51], v[140:147], v[32:39], v[48:51]
	v_mfma_f32_16x16x128_f8f6f4 v[36:39], v[132:139], v[162:169], v[238:241]
	v_mfma_f32_16x16x128_f8f6f4 v[32:35], v[140:147], v[162:169], v[242:245]
	v_mfma_f32_16x16x128_f8f6f4 v[20:23], v[132:139], v[170:177], v[246:249]
	v_mfma_f32_16x16x128_f8f6f4 v[16:19], v[140:147], v[170:177], v[250:253]
	v_mfma_f32_16x16x128_f8f6f4 v[4:7], v[132:139], v[178:185], v[190:193]
	v_mfma_f32_16x16x128_f8f6f4 v[0:3], v[140:147], v[178:185], v[152:155]
	s_setprio 0
	s_barrier
	s_add_i32 s11, s11, 2
	s_addk_i32 s4, 0x100
	s_addk_i32 s5, 0x100
	s_cmp_ge_i32 s11, s58
	s_cbranch_scc0 .LBB0_926
	s_branch .Lzp_after_926

;     __device__ __forceinline__ unsigned a_off(const Unit& u, const Gemm& g) const { return (unsigned)u.pm * (unsigned)(BM * 2) * (unsigned)g.K; }
;     __device__ __forceinline__ unsigned b_off(const Unit& u, const Gemm& g) const { return (unsigned)u.pn * (unsigned)(BM * 2) * (unsigned)g.K; }
;     __device__ __forceinline__ bool next(int i, Unit& u) const { return so.next(i, u); }
;     __device__ __forceinline__ unsigned a_off(const Unit& u, const Gemm& g) const { return (unsigned)u.pm * (unsigned)(BM * 2) * (unsigned)g.K; }
;     __device__ __forceinline__ bool next(int i, Unit& u) const { const bool ok = so.next(i >> 1, u); u.part = i & 1; return ok; }
; template <class Epi, class Sched, bool ALIGN_EPI = false, bool SP2 = false, bool FP8 = false>
; __device__ __forceinline__ void gemm_phase(LAS unsigned char* lds, const Gemm g, const Sched& S, const Epi& E, int wbase) {
;     ...
;         const bool has_next = S.next(ui + 1, nxt);
;         const unsigned nA = has_next ? S.a_off(nxt, g) : cA, nB = has_next ? S.b_off(nxt, g) : cB;
;         const rsrc_t rAn = (Sched::TWO && has_next) ? (nxt.part ? rA1 : rA0) : rAc, rBn = (Sched::TWO && has_next) ? (nxt.part ? rB1 : rB0) : rBc;
;         float pre_[8] = {0.f, 0.f, 0.f, 0.f, 0.f, 0.f, 0.f, 0.f};
;         if constexpr (Epi::HAS_PRE) E.pre_load(pre_, cur, wr);
;         for (int t = 0; t < nt; t += 2) {
;             const bool last = (t == nt - 2);
;             const unsigned a1 = cA + (unsigned)(t + 1) * kstep;
;             const unsigned a2 = last ? nA : cA + (unsigned)(t + 2) * kstep, b2 = last ? nB : cB + (unsigned)(t + 2) * kstep; const rsrc_t rA2 = (Sched::TWO && last) ? rAn : rAc, rB2 = (Sched::TWO && last) ? rBn : rBc;
;             const unsigned a3 = a2 + kstep, b3 = b2 + kstep;
;             if (last && has_next) S.a_ready(nxt);
;             if constexpr (SP2) {
;             PG8_LDB(B0, 0, 0); PG8_LDB(B1, 0, 1); PG8_SCHED; PG8_LDA(At, 0, 0); PG8_STAGE(PG8_SA(1, 1), rAc, a1 + hstep, voffA);
;             PG8_WAIT_V(8); PG8_WAIT_L(0); PG8_BAR; PG8_MMA(0, 0, At, B0); PG8_MMA(0, 1, At, B1); PG8_BAR; PG8_SCHED;
;             PG8_LDA(At, 0, 1); PG8_STAGE(PG8_SB(0, 0), rB2, b2, voffB); PG8_STAGE(PG8_SB(0, 1), rB2, b2 + hstep, voffB); PG8_STAGE(PG8_SA(0, 0), rA2, a2, voffA);
;             PG8_WAIT_V(8); PG8_WAIT_L(0); PG8_BAR; PG8_MMA(1, 0, At, B0); PG8_MMA(1, 1, At, B1); PG8_BAR; PG8_SCHED;
.LBB0_1002:
	s_lshl_b32 s81, s80, 19
	s_andn2_b64 vcc, exec, s[24:25]
	s_lshl_b32 s82, s79, 19
	s_cbranch_vccnz .LBB0_1058
	s_and_b64 s[2:3], s[28:29], exec
	s_waitcnt vmcnt(23)
	s_cselect_b32 s2, s81, s4
	s_cselect_b32 s3, s82, s5
	s_addk_i32 s4, 0x80
	s_addk_i32 s5, 0x100
	s_mov_b32 s11, 0
	s_waitcnt vmcnt(0)
	v_add_u32_e32 v132, 0x10000, v180
	v_add_u32_e32 v156, 0x14000, v180
	ds_read_b128 v[96:99], v132
	ds_read_b128 v[108:111], v132 offset:1024
	ds_read_b128 v[120:123], v132 offset:2048
	ds_read_b128 v[132:135], v132 offset:3072
	ds_read_b128 v[136:139], v156
	ds_read_b128 v[144:147], v156 offset:1024
	ds_read_b128 v[152:155], v156 offset:2048
	ds_read_b128 v[156:159], v156 offset:3072
	s_add_i32 s14, s4, 0x80
	s_cmp_eq_u32 s62, s11
	s_cselect_b32 s66, s2, s14
	s_cselect_b32 s55, s3, s5
	s_or_b32 s54, s66, 0x80
	s_add_i32 s14, s33, s4
	s_mov_b32 m0, s63
	ds_read_b128 v[160:163], v181
	ds_read_b128 v[164:167], v181 offset:1024
	ds_read_b128 v[168:171], v181 offset:2048
	ds_read_b128 v[182:185], v181 offset:3072
	ds_read_b128 v[186:189], v181 offset:4096
	ds_read_b128 v[190:193], v181 offset:5120
	ds_read_b128 v[194:197], v181 offset:6144
	ds_read_b128 v[198:201], v181 offset:7168
	buffer_load_dwordx4 v174, s[36:39], s14 offen lds
	s_mov_b32 m0, s65
	s_nop 0
	buffer_load_dwordx4 v176, s[36:39], s14 offen lds
	s_waitcnt vmcnt(8)
	s_waitcnt lgkmcnt(0)
	s_barrier
	s_setprio 1
	v_mfma_f32_16x16x32_bf16 v[148:151], v[96:99], v[160:163], 0
	v_mfma_f32_16x16x32_bf16 v[140:143], v[120:123], v[160:163], 0
	v_mfma_f32_16x16x32_bf16 v[116:119], v[96:99], v[168:171], 0
	v_mfma_f32_16x16x32_bf16 v[112:115], v[120:123], v[168:171], 0
	v_mfma_f32_16x16x32_bf16 v[92:95], v[96:99], v[186:189], 0
	v_mfma_f32_16x16x32_bf16 v[88:91], v[120:123], v[186:189], 0
	v_mfma_f32_16x16x32_bf16 v[76:79], v[96:99], v[194:197], 0
	v_mfma_f32_16x16x32_bf16 v[72:75], v[120:123], v[194:197], 0
	v_mfma_f32_16x16x32_bf16 v[148:151], v[108:111], v[164:167], v[148:151]
	v_mfma_f32_16x16x32_bf16 v[140:143], v[132:135], v[164:167], v[140:143]
	v_mfma_f32_16x16x32_bf16 v[116:119], v[108:111], v[182:185], v[116:119]
	v_mfma_f32_16x16x32_bf16 v[112:115], v[132:135], v[182:185], v[112:115]
	v_mfma_f32_16x16x32_bf16 v[92:95], v[108:111], v[190:193], v[92:95]
	v_mfma_f32_16x16x32_bf16 v[88:91], v[132:135], v[190:193], v[88:91]
	v_mfma_f32_16x16x32_bf16 v[76:79], v[108:111], v[198:201], v[76:79]
	v_mfma_f32_16x16x32_bf16 v[72:75], v[132:135], v[198:201], v[72:75]
	v_mfma_f32_16x16x32_bf16 v[128:131], v[136:139], v[160:163], 0
	v_mfma_f32_16x16x32_bf16 v[124:127], v[152:155], v[160:163], 0
	v_mfma_f32_16x16x32_bf16 v[104:107], v[136:139], v[168:171], 0
	v_mfma_f32_16x16x32_bf16 v[100:103], v[152:155], v[168:171], 0
	v_mfma_f32_16x16x32_bf16 v[84:87], v[136:139], v[186:189], 0
	v_mfma_f32_16x16x32_bf16 v[80:83], v[152:155], v[186:189], 0
	v_mfma_f32_16x16x32_bf16 v[68:71], v[136:139], v[194:197], 0
	v_mfma_f32_16x16x32_bf16 v[64:67], v[152:155], v[194:197], 0
	v_mfma_f32_16x16x32_bf16 v[128:131], v[144:147], v[164:167], v[128:131]
	v_mfma_f32_16x16x32_bf16 v[124:127], v[156:159], v[164:167], v[124:127]
	v_mfma_f32_16x16x32_bf16 v[104:107], v[144:147], v[182:185], v[104:107]
	v_mfma_f32_16x16x32_bf16 v[100:103], v[156:159], v[182:185], v[100:103]
	v_mfma_f32_16x16x32_bf16 v[84:87], v[144:147], v[190:193], v[84:87]
	v_mfma_f32_16x16x32_bf16 v[80:83], v[156:159], v[190:193], v[80:83]
	v_mfma_f32_16x16x32_bf16 v[68:71], v[144:147], v[198:201], v[68:71]
	v_mfma_f32_16x16x32_bf16 v[64:67], v[156:159], v[198:201], v[64:67]
	s_setprio 0
	s_barrier
	s_mov_b32 m0, s35
	s_mov_b32 s14, s38
	s_mov_b32 s15, s39
	buffer_load_dwordx4 v175, s[12:15], s55 offen lds
	s_mov_b32 m0, s41
	ds_read_b128 v[160:163], v181 offset:16384
	s_add_i32 s67, s55, s33
	buffer_load_dwordx4 v177, s[12:15], s55 offen lds
	s_mov_b32 m0, s42
	ds_read_b128 v[164:167], v181 offset:17408
	buffer_load_dwordx4 v175, s[12:15], s67 offen lds
	s_mov_b32 m0, s34
	ds_read_b128 v[168:171], v181 offset:18432
	buffer_load_dwordx4 v174, s[36:39], s66 offen lds
	s_mov_b32 m0, s44
	ds_read_b128 v[182:185], v181 offset:19456
	buffer_load_dwordx4 v176, s[36:39], s66 offen lds
	ds_read_b128 v[186:189], v181 offset:20480
	ds_read_b128 v[190:193], v181 offset:21504
	ds_read_b128 v[194:197], v181 offset:22528
	ds_read_b128 v[198:201], v181 offset:23552
	s_waitcnt vmcnt(7)
	s_waitcnt lgkmcnt(0)
	s_barrier
	s_setprio 1
	v_mfma_f32_16x16x32_bf16 v[60:63], v[96:99], v[160:163], 0
	v_mfma_f32_16x16x32_bf16 v[56:59], v[120:123], v[160:163], 0
	v_mfma_f32_16x16x32_bf16 v[44:47], v[96:99], v[168:171], 0
	v_mfma_f32_16x16x32_bf16 v[40:43], v[120:123], v[168:171], 0
	v_mfma_f32_16x16x32_bf16 v[28:31], v[96:99], v[186:189], 0
	v_mfma_f32_16x16x32_bf16 v[24:27], v[120:123], v[186:189], 0
	v_mfma_f32_16x16x32_bf16 v[12:15], v[96:99], v[194:197], 0
	v_mfma_f32_16x16x32_bf16 v[8:11], v[120:123], v[194:197], 0
	v_mfma_f32_16x16x32_bf16 v[60:63], v[108:111], v[164:167], v[60:63]
	v_mfma_f32_16x16x32_bf16 v[56:59], v[132:135], v[164:167], v[56:59]
	v_mfma_f32_16x16x32_bf16 v[44:47], v[108:111], v[182:185], v[44:47]
	v_mfma_f32_16x16x32_bf16 v[40:43], v[132:135], v[182:185], v[40:43]
	v_mfma_f32_16x16x32_bf16 v[28:31], v[108:111], v[190:193], v[28:31]
	v_mfma_f32_16x16x32_bf16 v[24:27], v[132:135], v[190:193], v[24:27]
	v_mfma_f32_16x16x32_bf16 v[12:15], v[108:111], v[198:201], v[12:15]
	v_mfma_f32_16x16x32_bf16 v[8:11], v[132:135], v[198:201], v[8:11]
	v_mfma_f32_16x16x32_bf16 v[52:55], v[136:139], v[160:163], 0
	v_mfma_f32_16x16x32_bf16 v[48:51], v[152:155], v[160:163], 0
	v_mfma_f32_16x16x32_bf16 v[36:39], v[136:139], v[168:171], 0
	v_mfma_f32_16x16x32_bf16 v[32:35], v[152:155], v[168:171], 0
	v_mfma_f32_16x16x32_bf16 v[20:23], v[136:139], v[186:189], 0
	v_mfma_f32_16x16x32_bf16 v[16:19], v[152:155], v[186:189], 0
	v_mfma_f32_16x16x32_bf16 v[4:7], v[136:139], v[194:197], 0
	v_mfma_f32_16x16x32_bf16 v[0:3], v[152:155], v[194:197], 0
	v_mfma_f32_16x16x32_bf16 v[52:55], v[144:147], v[164:167], v[52:55]
	v_mfma_f32_16x16x32_bf16 v[48:51], v[156:159], v[164:167], v[48:51]
	v_mfma_f32_16x16x32_bf16 v[36:39], v[144:147], v[182:185], v[36:39]
	v_mfma_f32_16x16x32_bf16 v[32:35], v[156:159], v[182:185], v[32:35]
	v_mfma_f32_16x16x32_bf16 v[20:23], v[144:147], v[190:193], v[20:23]
	v_mfma_f32_16x16x32_bf16 v[16:19], v[156:159], v[190:193], v[16:19]
	v_mfma_f32_16x16x32_bf16 v[4:7], v[144:147], v[198:201], v[4:7]
	v_mfma_f32_16x16x32_bf16 v[0:3], v[156:159], v[198:201], v[0:3]
	s_setprio 0
	s_barrier
; #define PG8_STAGE(bufoff, rs_, soff_, voff) do { _Pragma("unroll") for (int _i = 0; _i < 2; ++_i) \
;         __builtin_amdgcn_raw_ptr_buffer_load_lds(rs_, (LAS void*)(lds + (bufoff) + ldsw + _i * 8192), 16, (int)(voff)[_i], (int)(soff_), 0, 0); } while (0)
; #define PG8_LDA(dst, b, h) do { _Pragma("unroll") for (int m = 0; m < 4; ++m) dst[m] = PG8_LD2(lds + PG8_SA(b, h) + aoff + m * 2048); } while (0)
; #define PG8_LDB(dst, b, h) do { _Pragma("unroll") for (int n = 0; n < 2; ++n) dst[n] = PG8_LD2(lds + PG8_SB(b, h) + boff + n * 2048); } while (0)
; #define PG8_WAIT_V(n) asm volatile("s_waitcnt vmcnt(" #n ")" ::: "memory")
; #define PG8_WAIT_L(n) asm volatile("s_waitcnt lgkmcnt(" #n ")" ::: "memory")
; #define PG8_BAR __builtin_amdgcn_s_barrier()
; #define PG8_SCHED __builtin_amdgcn_sched_barrier(0)
; template <class Epi, class Sched, bool ALIGN_EPI = false, bool SP2 = false, bool FP8 = false>
; __device__ __forceinline__ void gemm_phase(LAS unsigned char* lds, const Gemm g, const Sched& S, const Epi& E, int wbase) {
;     ...
;             PG8_LDB(B0, 1, 0); PG8_LDB(B1, 1, 1); PG8_SCHED; PG8_LDA(At, 1, 0); PG8_STAGE(PG8_SA(0, 1), rA2, a2 + hstep, voffA);
;             PG8_WAIT_V(8); PG8_WAIT_L(0); PG8_BAR; PG8_MMA(0, 0, At, B0); PG8_MMA(0, 1, At, B1); PG8_BAR; PG8_SCHED;
;             PG8_LDA(At, 1, 1); PG8_STAGE(PG8_SB(1, 0), rB2, b3, voffB); PG8_STAGE(PG8_SB(1, 1), rB2, b3 + hstep, voffB); PG8_STAGE(PG8_SA(1, 0), rA2, a3, voffA);
;             PG8_WAIT_V(8); PG8_WAIT_L(0); PG8_BAR; PG8_MMA(1, 0, At, B0); PG8_MMA(1, 1, At, B1); PG8_BAR; PG8_SCHED;
	s_mov_b32 m0, s43
	s_nop 0
	buffer_load_dwordx4 v177, s[12:15], s67 offen lds
	v_add_u32_e32 v132, 0x18000, v180
	v_add_u32_e32 v156, 0x1c000, v180
	ds_read_b128 v[96:99], v132
	ds_read_b128 v[108:111], v132 offset:1024
	ds_read_b128 v[120:123], v132 offset:2048
	ds_read_b128 v[132:135], v132 offset:3072
	ds_read_b128 v[136:139], v156
	ds_read_b128 v[144:147], v156 offset:1024
	ds_read_b128 v[152:155], v156 offset:2048
	ds_read_b128 v[156:159], v156 offset:3072
	s_add_i32 s66, s66, s33
	s_mov_b32 m0, s45
	ds_read_b128 v[160:163], v181 offset:32768
	ds_read_b128 v[164:167], v181 offset:33792
	ds_read_b128 v[168:171], v181 offset:34816
	ds_read_b128 v[182:185], v181 offset:35840
	ds_read_b128 v[186:189], v181 offset:36864
	ds_read_b128 v[190:193], v181 offset:37888
	ds_read_b128 v[194:197], v181 offset:38912
	ds_read_b128 v[198:201], v181 offset:39936
	buffer_load_dwordx4 v174, s[36:39], s66 offen lds
	s_mov_b32 m0, s46
	s_nop 0
	buffer_load_dwordx4 v176, s[36:39], s66 offen lds
	s_waitcnt vmcnt(8)
	s_waitcnt lgkmcnt(0)
	s_barrier
	s_setprio 1
	v_mfma_f32_16x16x32_bf16 v[148:151], v[96:99], v[160:163], v[148:151]
	v_mfma_f32_16x16x32_bf16 v[140:143], v[120:123], v[160:163], v[140:143]
	v_mfma_f32_16x16x32_bf16 v[116:119], v[96:99], v[168:171], v[116:119]
	v_mfma_f32_16x16x32_bf16 v[112:115], v[120:123], v[168:171], v[112:115]
	v_mfma_f32_16x16x32_bf16 v[92:95], v[96:99], v[186:189], v[92:95]
	v_mfma_f32_16x16x32_bf16 v[88:91], v[120:123], v[186:189], v[88:91]
	v_mfma_f32_16x16x32_bf16 v[76:79], v[96:99], v[194:197], v[76:79]
	v_mfma_f32_16x16x32_bf16 v[72:75], v[120:123], v[194:197], v[72:75]
	v_mfma_f32_16x16x32_bf16 v[148:151], v[108:111], v[164:167], v[148:151]
	v_mfma_f32_16x16x32_bf16 v[140:143], v[132:135], v[164:167], v[140:143]
	v_mfma_f32_16x16x32_bf16 v[116:119], v[108:111], v[182:185], v[116:119]
	v_mfma_f32_16x16x32_bf16 v[112:115], v[132:135], v[182:185], v[112:115]
	v_mfma_f32_16x16x32_bf16 v[92:95], v[108:111], v[190:193], v[92:95]
	v_mfma_f32_16x16x32_bf16 v[88:91], v[132:135], v[190:193], v[88:91]
	v_mfma_f32_16x16x32_bf16 v[76:79], v[108:111], v[198:201], v[76:79]
	v_mfma_f32_16x16x32_bf16 v[72:75], v[132:135], v[198:201], v[72:75]
	v_mfma_f32_16x16x32_bf16 v[128:131], v[136:139], v[160:163], v[128:131]
	v_mfma_f32_16x16x32_bf16 v[124:127], v[152:155], v[160:163], v[124:127]
	v_mfma_f32_16x16x32_bf16 v[104:107], v[136:139], v[168:171], v[104:107]
	v_mfma_f32_16x16x32_bf16 v[100:103], v[152:155], v[168:171], v[100:103]
	v_mfma_f32_16x16x32_bf16 v[84:87], v[136:139], v[186:189], v[84:87]
	v_mfma_f32_16x16x32_bf16 v[80:83], v[152:155], v[186:189], v[80:83]
	v_mfma_f32_16x16x32_bf16 v[68:71], v[136:139], v[194:197], v[68:71]
	v_mfma_f32_16x16x32_bf16 v[64:67], v[152:155], v[194:197], v[64:67]
	v_mfma_f32_16x16x32_bf16 v[128:131], v[144:147], v[164:167], v[128:131]
	v_mfma_f32_16x16x32_bf16 v[124:127], v[156:159], v[164:167], v[124:127]
	v_mfma_f32_16x16x32_bf16 v[104:107], v[144:147], v[182:185], v[104:107]
	v_mfma_f32_16x16x32_bf16 v[100:103], v[156:159], v[182:185], v[100:103]
	v_mfma_f32_16x16x32_bf16 v[84:87], v[144:147], v[190:193], v[84:87]
	v_mfma_f32_16x16x32_bf16 v[80:83], v[156:159], v[190:193], v[80:83]
	v_mfma_f32_16x16x32_bf16 v[68:71], v[144:147], v[198:201], v[68:71]
	v_mfma_f32_16x16x32_bf16 v[64:67], v[156:159], v[198:201], v[64:67]
	s_setprio 0
	s_barrier
	s_mov_b32 m0, s47
	s_bitset1_b32 s55, 7
	buffer_load_dwordx4 v175, s[12:15], s55 offen lds
	s_mov_b32 m0, s48
	ds_read_b128 v[160:163], v181 offset:49152
	buffer_load_dwordx4 v177, s[12:15], s55 offen lds
	s_add_i32 s55, s55, s33
	s_mov_b32 m0, s56
	ds_read_b128 v[164:167], v181 offset:50176
	buffer_load_dwordx4 v175, s[12:15], s55 offen lds
	s_mov_b32 m0, s57
	ds_read_b128 v[168:171], v181 offset:51200
	buffer_load_dwordx4 v177, s[12:15], s55 offen lds
	s_mov_b32 m0, s52
	ds_read_b128 v[182:185], v181 offset:52224
	buffer_load_dwordx4 v174, s[36:39], s54 offen lds
	s_mov_b32 m0, s53
	ds_read_b128 v[186:189], v181 offset:53248
	buffer_load_dwordx4 v176, s[36:39], s54 offen lds
	ds_read_b128 v[190:193], v181 offset:54272
	ds_read_b128 v[194:197], v181 offset:55296
	ds_read_b128 v[198:201], v181 offset:56320
	s_waitcnt vmcnt(8)
	s_waitcnt lgkmcnt(0)
	s_barrier
	s_setprio 1
	v_mfma_f32_16x16x32_bf16 v[60:63], v[96:99], v[160:163], v[60:63]
	v_mfma_f32_16x16x32_bf16 v[56:59], v[120:123], v[160:163], v[56:59]
	v_mfma_f32_16x16x32_bf16 v[44:47], v[96:99], v[168:171], v[44:47]
	v_mfma_f32_16x16x32_bf16 v[40:43], v[120:123], v[168:171], v[40:43]
	v_mfma_f32_16x16x32_bf16 v[28:31], v[96:99], v[186:189], v[28:31]
	v_mfma_f32_16x16x32_bf16 v[24:27], v[120:123], v[186:189], v[24:27]
	v_mfma_f32_16x16x32_bf16 v[12:15], v[96:99], v[194:197], v[12:15]
	v_mfma_f32_16x16x32_bf16 v[8:11], v[120:123], v[194:197], v[8:11]
	v_mfma_f32_16x16x32_bf16 v[60:63], v[108:111], v[164:167], v[60:63]
	v_mfma_f32_16x16x32_bf16 v[56:59], v[132:135], v[164:167], v[56:59]
	v_mfma_f32_16x16x32_bf16 v[44:47], v[108:111], v[182:185], v[44:47]
	v_mfma_f32_16x16x32_bf16 v[40:43], v[132:135], v[182:185], v[40:43]
	v_mfma_f32_16x16x32_bf16 v[28:31], v[108:111], v[190:193], v[28:31]
	v_mfma_f32_16x16x32_bf16 v[24:27], v[132:135], v[190:193], v[24:27]
	v_mfma_f32_16x16x32_bf16 v[12:15], v[108:111], v[198:201], v[12:15]
	v_mfma_f32_16x16x32_bf16 v[8:11], v[132:135], v[198:201], v[8:11]
	v_mfma_f32_16x16x32_bf16 v[52:55], v[136:139], v[160:163], v[52:55]
	v_mfma_f32_16x16x32_bf16 v[48:51], v[152:155], v[160:163], v[48:51]
	v_mfma_f32_16x16x32_bf16 v[36:39], v[136:139], v[168:171], v[36:39]
	v_mfma_f32_16x16x32_bf16 v[32:35], v[152:155], v[168:171], v[32:35]
	v_mfma_f32_16x16x32_bf16 v[20:23], v[136:139], v[186:189], v[20:23]
	v_mfma_f32_16x16x32_bf16 v[16:19], v[152:155], v[186:189], v[16:19]
	v_mfma_f32_16x16x32_bf16 v[4:7], v[136:139], v[194:197], v[4:7]
	v_mfma_f32_16x16x32_bf16 v[0:3], v[152:155], v[194:197], v[0:3]
	v_mfma_f32_16x16x32_bf16 v[52:55], v[144:147], v[164:167], v[52:55]
	v_mfma_f32_16x16x32_bf16 v[48:51], v[156:159], v[164:167], v[48:51]
	v_mfma_f32_16x16x32_bf16 v[36:39], v[144:147], v[182:185], v[36:39]
	v_mfma_f32_16x16x32_bf16 v[32:35], v[156:159], v[182:185], v[32:35]
	v_mfma_f32_16x16x32_bf16 v[20:23], v[144:147], v[190:193], v[20:23]
	v_mfma_f32_16x16x32_bf16 v[16:19], v[156:159], v[190:193], v[16:19]
	v_mfma_f32_16x16x32_bf16 v[4:7], v[144:147], v[198:201], v[4:7]
	v_mfma_f32_16x16x32_bf16 v[0:3], v[156:159], v[198:201], v[0:3]
	s_setprio 0
	s_barrier
	s_add_i32 s11, s11, 2
	s_addk_i32 s4, 0x100
	s_addk_i32 s5, 0x100
	s_cmp_ge_i32 s11, s60
	s_cbranch_scc0 .LBB0_1004
	s_branch .Lzp_after_1004

;     __device__ __forceinline__ unsigned a_off(const Unit& u, const Gemm& g) const { return (unsigned)u.pm * (unsigned)(BM * 2) * (unsigned)g.K; }
;     __device__ __forceinline__ unsigned b_off(const Unit& u, const Gemm& g) const { return (unsigned)u.pn * (unsigned)(BM * 2) * (unsigned)g.K; }
;     __device__ __forceinline__ bool next(int i, Unit& u) const { return so.next(i, u); }
;     __device__ __forceinline__ unsigned a_off(const Unit& u, const Gemm& g) const { return (unsigned)u.pm * (unsigned)(BM * 2) * (unsigned)g.K; }
;     __device__ __forceinline__ bool next(int i, Unit& u) const { const bool ok = so.next(i >> 1, u); u.part = i & 1; return ok; }
; template <class Epi, class Sched, bool ALIGN_EPI = false, bool SP2 = false, bool FP8 = false>
; __device__ __forceinline__ void gemm_phase(LAS unsigned char* lds, const Gemm g, const Sched& S, const Epi& E, int wbase) {
;     ...
;         const bool has_next = S.next(ui + 1, nxt);
;         const unsigned nA = has_next ? S.a_off(nxt, g) : cA, nB = has_next ? S.b_off(nxt, g) : cB;
;         const rsrc_t rAn = (Sched::TWO && has_next) ? (nxt.part ? rA1 : rA0) : rAc, rBn = (Sched::TWO && has_next) ? (nxt.part ? rB1 : rB0) : rBc;
;         float pre_[8] = {0.f, 0.f, 0.f, 0.f, 0.f, 0.f, 0.f, 0.f};
;         if constexpr (Epi::HAS_PRE) E.pre_load(pre_, cur, wr);
;         for (int t = 0; t < nt; t += 2) {
;             const bool last = (t == nt - 2);
;             const unsigned a1 = cA + (unsigned)(t + 1) * kstep;
;             const unsigned a2 = last ? nA : cA + (unsigned)(t + 2) * kstep, b2 = last ? nB : cB + (unsigned)(t + 2) * kstep; const rsrc_t rA2 = (Sched::TWO && last) ? rAn : rAc, rB2 = (Sched::TWO && last) ? rBn : rBc;
;             const unsigned a3 = a2 + kstep, b3 = b2 + kstep;
;             if (last && has_next) S.a_ready(nxt);
;             if constexpr (SP2) {
;             PG8_LDB(B0, 0, 0); PG8_LDB(B1, 0, 1); PG8_SCHED; PG8_LDA(At, 0, 0); PG8_STAGE(PG8_SA(1, 1), rAc, a1 + hstep, voffA);
;             PG8_WAIT_V(8); PG8_WAIT_L(0); PG8_BAR; PG8_MMA(0, 0, At, B0); PG8_MMA(0, 1, At, B1); PG8_BAR; PG8_SCHED;
;             PG8_LDA(At, 0, 1); PG8_STAGE(PG8_SB(0, 0), rB2, b2, voffB); PG8_STAGE(PG8_SB(0, 1), rB2, b2 + hstep, voffB); PG8_STAGE(PG8_SA(0, 0), rA2, a2, voffA);
;             PG8_WAIT_V(8); PG8_WAIT_L(0); PG8_BAR; PG8_MMA(1, 0, At, B0); PG8_MMA(1, 1, At, B1); PG8_BAR; PG8_SCHED;
.LBB0_1626:
	s_lshl_b32 s56, s53, 19
	s_andn2_b64 vcc, exec, s[12:13]
	s_lshl_b32 s57, s52, 19
	s_cbranch_vccnz .LBB0_1634
	s_and_b64 s[6:7], s[18:19], exec
	s_waitcnt vmcnt(22)
	s_cselect_b32 s59, s56, s55
	s_cselect_b32 s60, s57, s54
	s_add_i32 s61, s55, 0x80
	s_add_i32 s62, s54, 0x100
	s_mov_b32 s63, 0
	v_add_u32_e32 v136, 0x10000, v161
	ds_read_b128 v[128:131], v136
	ds_read_b128 v[132:135], v136 offset:1024
	ds_read_b128 v[164:167], v136 offset:2048
	ds_read_b128 v[168:171], v136 offset:3072
	v_add_u32_e32 v136, 0x14000, v161
	ds_read_b128 v[172:175], v136
	ds_read_b128 v[176:179], v136 offset:1024
	ds_read_b128 v[180:183], v136 offset:2048
	ds_read_b128 v[184:187], v136 offset:3072
	s_add_i32 s6, s61, 0x80
	s_cmp_eq_u32 s46, s63
	s_cselect_b32 s65, s59, s6
	s_cselect_b32 s55, s60, s62
	s_or_b32 s54, s65, 0x80
	s_add_i32 s6, s22, s61
	s_mov_b32 m0, s47
	ds_read_b128 v[188:191], v162
	ds_read_b128 v[192:195], v162 offset:1024
	ds_read_b128 v[196:199], v162 offset:2048
	ds_read_b128 v[200:203], v162 offset:3072
	ds_read_b128 v[204:207], v162 offset:4096
	ds_read_b128 v[208:211], v162 offset:5120
	ds_read_b128 v[212:215], v162 offset:6144
	ds_read_b128 v[216:219], v162 offset:7168
	buffer_load_dwordx4 v137, s[36:39], s6 offen lds
	s_mov_b32 m0, s48
	s_nop 0
	buffer_load_dwordx4 v145, s[36:39], s6 offen lds
	s_waitcnt vmcnt(8)
	s_waitcnt lgkmcnt(0)
	s_barrier
	s_setprio 1
	v_mfma_f32_16x16x32_bf16 v[120:123], v[128:131], v[188:191], 0
	v_mfma_f32_16x16x32_bf16 v[124:127], v[164:167], v[188:191], 0
	v_mfma_f32_16x16x32_bf16 v[104:107], v[128:131], v[196:199], 0
	v_mfma_f32_16x16x32_bf16 v[108:111], v[164:167], v[196:199], 0
	v_mfma_f32_16x16x32_bf16 v[88:91], v[128:131], v[204:207], 0
	v_mfma_f32_16x16x32_bf16 v[92:95], v[164:167], v[204:207], 0
	v_mfma_f32_16x16x32_bf16 v[72:75], v[128:131], v[212:215], 0
	v_mfma_f32_16x16x32_bf16 v[76:79], v[164:167], v[212:215], 0
	v_mfma_f32_16x16x32_bf16 v[120:123], v[132:135], v[192:195], v[120:123]
	v_mfma_f32_16x16x32_bf16 v[124:127], v[168:171], v[192:195], v[124:127]
	v_mfma_f32_16x16x32_bf16 v[104:107], v[132:135], v[200:203], v[104:107]
	v_mfma_f32_16x16x32_bf16 v[108:111], v[168:171], v[200:203], v[108:111]
	v_mfma_f32_16x16x32_bf16 v[88:91], v[132:135], v[208:211], v[88:91]
	v_mfma_f32_16x16x32_bf16 v[92:95], v[168:171], v[208:211], v[92:95]
	v_mfma_f32_16x16x32_bf16 v[72:75], v[132:135], v[216:219], v[72:75]
	v_mfma_f32_16x16x32_bf16 v[76:79], v[168:171], v[216:219], v[76:79]
	v_mfma_f32_16x16x32_bf16 v[112:115], v[172:175], v[188:191], 0
	v_mfma_f32_16x16x32_bf16 v[116:119], v[180:183], v[188:191], 0
	v_mfma_f32_16x16x32_bf16 v[96:99], v[172:175], v[196:199], 0
	v_mfma_f32_16x16x32_bf16 v[100:103], v[180:183], v[196:199], 0
	v_mfma_f32_16x16x32_bf16 v[80:83], v[172:175], v[204:207], 0
	v_mfma_f32_16x16x32_bf16 v[84:87], v[180:183], v[204:207], 0
	v_mfma_f32_16x16x32_bf16 v[64:67], v[172:175], v[212:215], 0
	v_mfma_f32_16x16x32_bf16 v[68:71], v[180:183], v[212:215], 0
	v_mfma_f32_16x16x32_bf16 v[112:115], v[176:179], v[192:195], v[112:115]
	v_mfma_f32_16x16x32_bf16 v[116:119], v[184:187], v[192:195], v[116:119]
	v_mfma_f32_16x16x32_bf16 v[96:99], v[176:179], v[200:203], v[96:99]
	v_mfma_f32_16x16x32_bf16 v[100:103], v[184:187], v[200:203], v[100:103]
	v_mfma_f32_16x16x32_bf16 v[80:83], v[176:179], v[208:211], v[80:83]
	v_mfma_f32_16x16x32_bf16 v[84:87], v[184:187], v[208:211], v[84:87]
	v_mfma_f32_16x16x32_bf16 v[64:67], v[176:179], v[216:219], v[64:67]
	v_mfma_f32_16x16x32_bf16 v[68:71], v[184:187], v[216:219], v[68:71]
	s_setprio 0
	s_barrier
	s_mov_b32 m0, s24
	s_mov_b32 s6, s38
	s_mov_b32 s7, s39
	buffer_load_dwordx4 v141, s[4:7], s55 offen lds
	s_mov_b32 m0, s25
	ds_read_b128 v[188:191], v162 offset:16384
	s_add_i32 s66, s55, s22
	buffer_load_dwordx4 v149, s[4:7], s55 offen lds
	s_mov_b32 m0, s26
	ds_read_b128 v[192:195], v162 offset:17408
	buffer_load_dwordx4 v141, s[4:7], s66 offen lds
	s_mov_b32 m0, s23
	ds_read_b128 v[196:199], v162 offset:18432
	buffer_load_dwordx4 v137, s[36:39], s65 offen lds
	s_mov_b32 m0, s28
	ds_read_b128 v[200:203], v162 offset:19456
	buffer_load_dwordx4 v145, s[36:39], s65 offen lds
	ds_read_b128 v[204:207], v162 offset:20480
	ds_read_b128 v[208:211], v162 offset:21504
	ds_read_b128 v[212:215], v162 offset:22528
	ds_read_b128 v[216:219], v162 offset:23552
	s_waitcnt vmcnt(7)
	s_waitcnt lgkmcnt(0)
	s_barrier
	s_setprio 1
	v_mfma_f32_16x16x32_bf16 v[56:59], v[128:131], v[188:191], 0
	v_mfma_f32_16x16x32_bf16 v[60:63], v[164:167], v[188:191], 0
	v_mfma_f32_16x16x32_bf16 v[40:43], v[128:131], v[196:199], 0
	v_mfma_f32_16x16x32_bf16 v[44:47], v[164:167], v[196:199], 0
	v_mfma_f32_16x16x32_bf16 v[24:27], v[128:131], v[204:207], 0
	v_mfma_f32_16x16x32_bf16 v[28:31], v[164:167], v[204:207], 0
	v_mfma_f32_16x16x32_bf16 v[8:11], v[128:131], v[212:215], 0
	v_mfma_f32_16x16x32_bf16 v[12:15], v[164:167], v[212:215], 0
	v_mfma_f32_16x16x32_bf16 v[56:59], v[132:135], v[192:195], v[56:59]
	v_mfma_f32_16x16x32_bf16 v[60:63], v[168:171], v[192:195], v[60:63]
	v_mfma_f32_16x16x32_bf16 v[40:43], v[132:135], v[200:203], v[40:43]
	v_mfma_f32_16x16x32_bf16 v[44:47], v[168:171], v[200:203], v[44:47]
	v_mfma_f32_16x16x32_bf16 v[24:27], v[132:135], v[208:211], v[24:27]
	v_mfma_f32_16x16x32_bf16 v[28:31], v[168:171], v[208:211], v[28:31]
	v_mfma_f32_16x16x32_bf16 v[8:11], v[132:135], v[216:219], v[8:11]
	v_mfma_f32_16x16x32_bf16 v[12:15], v[168:171], v[216:219], v[12:15]
	v_mfma_f32_16x16x32_bf16 v[48:51], v[172:175], v[188:191], 0
	v_mfma_f32_16x16x32_bf16 v[52:55], v[180:183], v[188:191], 0
	v_mfma_f32_16x16x32_bf16 v[32:35], v[172:175], v[196:199], 0
	v_mfma_f32_16x16x32_bf16 v[36:39], v[180:183], v[196:199], 0
	v_mfma_f32_16x16x32_bf16 v[16:19], v[172:175], v[204:207], 0
	v_mfma_f32_16x16x32_bf16 v[20:23], v[180:183], v[204:207], 0
	v_mfma_f32_16x16x32_bf16 v[4:7], v[172:175], v[212:215], 0
	v_mfma_f32_16x16x32_bf16 v[0:3], v[180:183], v[212:215], 0
	v_mfma_f32_16x16x32_bf16 v[48:51], v[176:179], v[192:195], v[48:51]
	v_mfma_f32_16x16x32_bf16 v[52:55], v[184:187], v[192:195], v[52:55]
	v_mfma_f32_16x16x32_bf16 v[32:35], v[176:179], v[200:203], v[32:35]
	v_mfma_f32_16x16x32_bf16 v[36:39], v[184:187], v[200:203], v[36:39]
	v_mfma_f32_16x16x32_bf16 v[16:19], v[176:179], v[208:211], v[16:19]
	v_mfma_f32_16x16x32_bf16 v[20:23], v[184:187], v[208:211], v[20:23]
	v_mfma_f32_16x16x32_bf16 v[4:7], v[176:179], v[216:219], v[4:7]
	v_mfma_f32_16x16x32_bf16 v[0:3], v[184:187], v[216:219], v[0:3]
	s_setprio 0
	s_barrier
; #define PG8_STAGE(bufoff, rs_, soff_, voff) do { _Pragma("unroll") for (int _i = 0; _i < 2; ++_i) \
;         __builtin_amdgcn_raw_ptr_buffer_load_lds(rs_, (LAS void*)(lds + (bufoff) + ldsw + _i * 8192), 16, (int)(voff)[_i], (int)(soff_), 0, 0); } while (0)
; #define PG8_LDA(dst, b, h) do { _Pragma("unroll") for (int m = 0; m < 4; ++m) dst[m] = PG8_LD2(lds + PG8_SA(b, h) + aoff + m * 2048); } while (0)
; #define PG8_LDB(dst, b, h) do { _Pragma("unroll") for (int n = 0; n < 2; ++n) dst[n] = PG8_LD2(lds + PG8_SB(b, h) + boff + n * 2048); } while (0)
; #define PG8_WAIT_V(n) asm volatile("s_waitcnt vmcnt(" #n ")" ::: "memory")
; #define PG8_WAIT_L(n) asm volatile("s_waitcnt lgkmcnt(" #n ")" ::: "memory")
; #define PG8_BAR __builtin_amdgcn_s_barrier()
; #define PG8_SCHED __builtin_amdgcn_sched_barrier(0)
; template <class Epi, class Sched, bool ALIGN_EPI = false, bool SP2 = false, bool FP8 = false>
; __device__ __forceinline__ void gemm_phase(LAS unsigned char* lds, const Gemm g, const Sched& S, const Epi& E, int wbase) {
;     ...
;             PG8_LDB(B0, 1, 0); PG8_LDB(B1, 1, 1); PG8_SCHED; PG8_LDA(At, 1, 0); PG8_STAGE(PG8_SA(0, 1), rA2, a2 + hstep, voffA);
;             PG8_WAIT_V(8); PG8_WAIT_L(0); PG8_BAR; PG8_MMA(0, 0, At, B0); PG8_MMA(0, 1, At, B1); PG8_BAR; PG8_SCHED;
;             PG8_LDA(At, 1, 1); PG8_STAGE(PG8_SB(1, 0), rB2, b3, voffB); PG8_STAGE(PG8_SB(1, 1), rB2, b3 + hstep, voffB); PG8_STAGE(PG8_SA(1, 0), rA2, a3, voffA);
;             PG8_WAIT_V(8); PG8_WAIT_L(0); PG8_BAR; PG8_MMA(1, 0, At, B0); PG8_MMA(1, 1, At, B1); PG8_BAR; PG8_SCHED;
	s_mov_b32 m0, s27
	s_nop 0
	buffer_load_dwordx4 v149, s[4:7], s66 offen lds
	v_add_u32_e32 v136, 0x18000, v161
	ds_read_b128 v[128:131], v136
	ds_read_b128 v[132:135], v136 offset:1024
	ds_read_b128 v[164:167], v136 offset:2048
	ds_read_b128 v[168:171], v136 offset:3072
	v_add_u32_e32 v136, 0x1c000, v161
	ds_read_b128 v[172:175], v136
	ds_read_b128 v[176:179], v136 offset:1024
	ds_read_b128 v[180:183], v136 offset:2048
	ds_read_b128 v[184:187], v136 offset:3072
	s_add_i32 s65, s65, s22
	s_mov_b32 m0, s29
	ds_read_b128 v[188:191], v162 offset:32768
	ds_read_b128 v[192:195], v162 offset:33792
	ds_read_b128 v[196:199], v162 offset:34816
	ds_read_b128 v[200:203], v162 offset:35840
	ds_read_b128 v[204:207], v162 offset:36864
	ds_read_b128 v[208:211], v162 offset:37888
	ds_read_b128 v[212:215], v162 offset:38912
	ds_read_b128 v[216:219], v162 offset:39936
	buffer_load_dwordx4 v137, s[36:39], s65 offen lds
	s_mov_b32 m0, s30
	s_nop 0
	buffer_load_dwordx4 v145, s[36:39], s65 offen lds
	s_waitcnt vmcnt(8)
	s_waitcnt lgkmcnt(0)
	s_barrier
	s_setprio 1
	v_mfma_f32_16x16x32_bf16 v[120:123], v[128:131], v[188:191], v[120:123]
	v_mfma_f32_16x16x32_bf16 v[124:127], v[164:167], v[188:191], v[124:127]
	v_mfma_f32_16x16x32_bf16 v[104:107], v[128:131], v[196:199], v[104:107]
	v_mfma_f32_16x16x32_bf16 v[108:111], v[164:167], v[196:199], v[108:111]
	v_mfma_f32_16x16x32_bf16 v[88:91], v[128:131], v[204:207], v[88:91]
	v_mfma_f32_16x16x32_bf16 v[92:95], v[164:167], v[204:207], v[92:95]
	v_mfma_f32_16x16x32_bf16 v[72:75], v[128:131], v[212:215], v[72:75]
	v_mfma_f32_16x16x32_bf16 v[76:79], v[164:167], v[212:215], v[76:79]
	v_mfma_f32_16x16x32_bf16 v[120:123], v[132:135], v[192:195], v[120:123]
	v_mfma_f32_16x16x32_bf16 v[124:127], v[168:171], v[192:195], v[124:127]
	v_mfma_f32_16x16x32_bf16 v[104:107], v[132:135], v[200:203], v[104:107]
	v_mfma_f32_16x16x32_bf16 v[108:111], v[168:171], v[200:203], v[108:111]
	v_mfma_f32_16x16x32_bf16 v[88:91], v[132:135], v[208:211], v[88:91]
	v_mfma_f32_16x16x32_bf16 v[92:95], v[168:171], v[208:211], v[92:95]
	v_mfma_f32_16x16x32_bf16 v[72:75], v[132:135], v[216:219], v[72:75]
	v_mfma_f32_16x16x32_bf16 v[76:79], v[168:171], v[216:219], v[76:79]
	v_mfma_f32_16x16x32_bf16 v[112:115], v[172:175], v[188:191], v[112:115]
	v_mfma_f32_16x16x32_bf16 v[116:119], v[180:183], v[188:191], v[116:119]
	v_mfma_f32_16x16x32_bf16 v[96:99], v[172:175], v[196:199], v[96:99]
	v_mfma_f32_16x16x32_bf16 v[100:103], v[180:183], v[196:199], v[100:103]
	v_mfma_f32_16x16x32_bf16 v[80:83], v[172:175], v[204:207], v[80:83]
	v_mfma_f32_16x16x32_bf16 v[84:87], v[180:183], v[204:207], v[84:87]
	v_mfma_f32_16x16x32_bf16 v[64:67], v[172:175], v[212:215], v[64:67]
	v_mfma_f32_16x16x32_bf16 v[68:71], v[180:183], v[212:215], v[68:71]
	v_mfma_f32_16x16x32_bf16 v[112:115], v[176:179], v[192:195], v[112:115]
	v_mfma_f32_16x16x32_bf16 v[116:119], v[184:187], v[192:195], v[116:119]
	v_mfma_f32_16x16x32_bf16 v[96:99], v[176:179], v[200:203], v[96:99]
	v_mfma_f32_16x16x32_bf16 v[100:103], v[184:187], v[200:203], v[100:103]
	v_mfma_f32_16x16x32_bf16 v[80:83], v[176:179], v[208:211], v[80:83]
	v_mfma_f32_16x16x32_bf16 v[84:87], v[184:187], v[208:211], v[84:87]
	v_mfma_f32_16x16x32_bf16 v[64:67], v[176:179], v[216:219], v[64:67]
	v_mfma_f32_16x16x32_bf16 v[68:71], v[184:187], v[216:219], v[68:71]
	s_setprio 0
	s_barrier
	s_mov_b32 m0, s31
	s_bitset1_b32 s55, 7
	buffer_load_dwordx4 v141, s[4:7], s55 offen lds
	s_mov_b32 m0, s33
	ds_read_b128 v[188:191], v162 offset:49152
	buffer_load_dwordx4 v149, s[4:7], s55 offen lds
	s_add_i32 s55, s55, s22
	s_mov_b32 m0, s41
	ds_read_b128 v[192:195], v162 offset:50176
	buffer_load_dwordx4 v141, s[4:7], s55 offen lds
	s_mov_b32 m0, s42
	ds_read_b128 v[196:199], v162 offset:51200
	buffer_load_dwordx4 v149, s[4:7], s55 offen lds
	s_mov_b32 m0, s34
	ds_read_b128 v[200:203], v162 offset:52224
	buffer_load_dwordx4 v137, s[36:39], s54 offen lds
	s_mov_b32 m0, s35
	ds_read_b128 v[204:207], v162 offset:53248
	buffer_load_dwordx4 v145, s[36:39], s54 offen lds
	ds_read_b128 v[208:211], v162 offset:54272
	ds_read_b128 v[212:215], v162 offset:55296
	ds_read_b128 v[216:219], v162 offset:56320
	s_waitcnt vmcnt(8)
	s_waitcnt lgkmcnt(0)
	s_barrier
	s_setprio 1
	v_mfma_f32_16x16x32_bf16 v[56:59], v[128:131], v[188:191], v[56:59]
	v_mfma_f32_16x16x32_bf16 v[60:63], v[164:167], v[188:191], v[60:63]
	v_mfma_f32_16x16x32_bf16 v[40:43], v[128:131], v[196:199], v[40:43]
	v_mfma_f32_16x16x32_bf16 v[44:47], v[164:167], v[196:199], v[44:47]
	v_mfma_f32_16x16x32_bf16 v[24:27], v[128:131], v[204:207], v[24:27]
	v_mfma_f32_16x16x32_bf16 v[28:31], v[164:167], v[204:207], v[28:31]
	v_mfma_f32_16x16x32_bf16 v[8:11], v[128:131], v[212:215], v[8:11]
	v_mfma_f32_16x16x32_bf16 v[12:15], v[164:167], v[212:215], v[12:15]
	v_mfma_f32_16x16x32_bf16 v[56:59], v[132:135], v[192:195], v[56:59]
	v_mfma_f32_16x16x32_bf16 v[60:63], v[168:171], v[192:195], v[60:63]
	v_mfma_f32_16x16x32_bf16 v[40:43], v[132:135], v[200:203], v[40:43]
	v_mfma_f32_16x16x32_bf16 v[44:47], v[168:171], v[200:203], v[44:47]
	v_mfma_f32_16x16x32_bf16 v[24:27], v[132:135], v[208:211], v[24:27]
	v_mfma_f32_16x16x32_bf16 v[28:31], v[168:171], v[208:211], v[28:31]
	v_mfma_f32_16x16x32_bf16 v[8:11], v[132:135], v[216:219], v[8:11]
	v_mfma_f32_16x16x32_bf16 v[12:15], v[168:171], v[216:219], v[12:15]
	v_mfma_f32_16x16x32_bf16 v[48:51], v[172:175], v[188:191], v[48:51]
	v_mfma_f32_16x16x32_bf16 v[52:55], v[180:183], v[188:191], v[52:55]
	v_mfma_f32_16x16x32_bf16 v[32:35], v[172:175], v[196:199], v[32:35]
	v_mfma_f32_16x16x32_bf16 v[36:39], v[180:183], v[196:199], v[36:39]
	v_mfma_f32_16x16x32_bf16 v[16:19], v[172:175], v[204:207], v[16:19]
	v_mfma_f32_16x16x32_bf16 v[20:23], v[180:183], v[204:207], v[20:23]
	v_mfma_f32_16x16x32_bf16 v[4:7], v[172:175], v[212:215], v[4:7]
	v_mfma_f32_16x16x32_bf16 v[0:3], v[180:183], v[212:215], v[0:3]
	v_mfma_f32_16x16x32_bf16 v[48:51], v[176:179], v[192:195], v[48:51]
	v_mfma_f32_16x16x32_bf16 v[52:55], v[184:187], v[192:195], v[52:55]
	v_mfma_f32_16x16x32_bf16 v[32:35], v[176:179], v[200:203], v[32:35]
	v_mfma_f32_16x16x32_bf16 v[36:39], v[184:187], v[200:203], v[36:39]
	v_mfma_f32_16x16x32_bf16 v[16:19], v[176:179], v[208:211], v[16:19]
	v_mfma_f32_16x16x32_bf16 v[20:23], v[184:187], v[208:211], v[20:23]
	v_mfma_f32_16x16x32_bf16 v[4:7], v[176:179], v[216:219], v[4:7]
	v_mfma_f32_16x16x32_bf16 v[0:3], v[184:187], v[216:219], v[0:3]
	s_setprio 0
	s_barrier
	s_add_i32 s63, s63, 2
	s_addk_i32 s61, 0x100
	s_addk_i32 s62, 0x100
	s_cmp_ge_i32 s63, s44
	s_cbranch_scc0 .LBB0_1628
	s_branch .Lzp_after_1628

;     __device__ __forceinline__ unsigned a_off(const Unit& u, const Gemm& g) const { return (unsigned)u.pm * (unsigned)(BM * 2) * (unsigned)g.K; }
;     __device__ __forceinline__ unsigned b_off(const Unit& u, const Gemm& g) const { return (unsigned)u.pn * (unsigned)(BM * 2) * (unsigned)g.K; }
;     __device__ __forceinline__ bool next(int i, Unit& u) const { return so.next(i, u); }
;     __device__ __forceinline__ unsigned a_off(const Unit& u, const Gemm& g) const { return (unsigned)u.pm * (unsigned)(BM * 2) * (unsigned)g.K; }
;     __device__ __forceinline__ bool next(int i, Unit& u) const { const bool ok = so.next(i >> 1, u); u.part = i & 1; return ok; }
; template <class Epi, class Sched, bool ALIGN_EPI = false, bool SP2 = false, bool FP8 = false>
; __device__ __forceinline__ void gemm_phase(LAS unsigned char* lds, const Gemm g, const Sched& S, const Epi& E, int wbase) {
;     ...
;         const bool has_next = S.next(ui + 1, nxt);
;         const unsigned nA = has_next ? S.a_off(nxt, g) : cA, nB = has_next ? S.b_off(nxt, g) : cB;
;         const rsrc_t rAn = (Sched::TWO && has_next) ? (nxt.part ? rA1 : rA0) : rAc, rBn = (Sched::TWO && has_next) ? (nxt.part ? rB1 : rB0) : rBc;
;         float pre_[8] = {0.f, 0.f, 0.f, 0.f, 0.f, 0.f, 0.f, 0.f};
;         if constexpr (Epi::HAS_PRE) E.pre_load(pre_, cur, wr);
;         for (int t = 0; t < nt; t += 2) {
;             const bool last = (t == nt - 2);
;             const unsigned a1 = cA + (unsigned)(t + 1) * kstep;
;             const unsigned a2 = last ? nA : cA + (unsigned)(t + 2) * kstep, b2 = last ? nB : cB + (unsigned)(t + 2) * kstep; const rsrc_t rA2 = (Sched::TWO && last) ? rAn : rAc, rB2 = (Sched::TWO && last) ? rBn : rBc;
;             const unsigned a3 = a2 + kstep, b3 = b2 + kstep;
;             if (last && has_next) S.a_ready(nxt);
;             if constexpr (SP2) {
;             PG8_LDB(B0, 0, 0); PG8_LDB(B1, 0, 1); PG8_SCHED; PG8_LDA(At, 0, 0); PG8_STAGE(PG8_SA(1, 1), rAc, a1 + hstep, voffA);
;             PG8_WAIT_V(8); PG8_WAIT_L(0); PG8_BAR; PG8_MMA(0, 0, At, B0); PG8_MMA(0, 1, At, B1); PG8_BAR; PG8_SCHED;
;             PG8_LDA(At, 0, 1); PG8_STAGE(PG8_SB(0, 0), rB2, b2, voffB); PG8_STAGE(PG8_SB(0, 1), rB2, b2 + hstep, voffB); PG8_STAGE(PG8_SA(0, 0), rA2, a2, voffA);
;             PG8_WAIT_V(8); PG8_WAIT_L(0); PG8_BAR; PG8_MMA(1, 0, At, B0); PG8_MMA(1, 1, At, B1); PG8_BAR; PG8_SCHED;
.LBB0_1699:
	s_mul_i32 s61, s60, 0x1c0000
	s_andn2_b64 vcc, exec, s[14:15]
	s_mul_i32 s62, s59, 0x1c0000
	s_cbranch_vccnz .LBB0_1703
	s_and_b64 s[6:7], s[18:19], exec
	s_waitcnt vmcnt(22)
	s_cselect_b32 s21, s61, s55
	s_cselect_b32 s63, s62, s54
	s_add_i32 s65, s55, 0x80
	s_add_i32 s66, s54, 0x100
	s_mov_b32 s67, 0
	v_add_u32_e32 v140, 0x10000, v176
	v_add_u32_e32 v156, 0x14000, v176
	ds_read_b128 v[112:115], v140
	ds_read_b128 v[124:127], v140 offset:1024
	ds_read_b128 v[136:139], v140 offset:2048
	ds_read_b128 v[140:143], v140 offset:3072
	ds_read_b128 v[144:147], v156
	ds_read_b128 v[148:151], v156 offset:1024
	ds_read_b128 v[152:155], v156 offset:2048
	ds_read_b128 v[156:159], v156 offset:3072
	s_add_i32 s6, s65, 0x80
	s_cmp_eq_u32 s52, s67
	s_cselect_b32 s68, s21, s6
	s_cselect_b32 s55, s63, s66
	s_or_b32 s54, s68, 0x80
	s_add_i32 s6, s25, s65
	s_mov_b32 m0, s53
	ds_read_b128 v[160:163], v177
	ds_read_b128 v[164:167], v177 offset:1024
	ds_read_b128 v[178:181], v177 offset:2048
	ds_read_b128 v[182:185], v177 offset:3072
	ds_read_b128 v[186:189], v177 offset:4096
	ds_read_b128 v[190:193], v177 offset:5120
	ds_read_b128 v[194:197], v177 offset:6144
	ds_read_b128 v[198:201], v177 offset:7168
	buffer_load_dwordx4 v170, s[36:39], s6 offen lds
	s_mov_b32 m0, s56
	s_nop 0
	buffer_load_dwordx4 v172, s[36:39], s6 offen lds
	s_waitcnt vmcnt(8)
	s_waitcnt lgkmcnt(0)
	s_barrier
	s_setprio 1
	v_mfma_f32_16x16x32_bf16 v[132:135], v[112:115], v[160:163], 0
	v_mfma_f32_16x16x32_bf16 v[128:131], v[136:139], v[160:163], 0
	v_mfma_f32_16x16x32_bf16 v[108:111], v[112:115], v[178:181], 0
	v_mfma_f32_16x16x32_bf16 v[104:107], v[136:139], v[178:181], 0
	v_mfma_f32_16x16x32_bf16 v[92:95], v[112:115], v[186:189], 0
	v_mfma_f32_16x16x32_bf16 v[88:91], v[136:139], v[186:189], 0
	v_mfma_f32_16x16x32_bf16 v[76:79], v[112:115], v[194:197], 0
	v_mfma_f32_16x16x32_bf16 v[72:75], v[136:139], v[194:197], 0
	v_mfma_f32_16x16x32_bf16 v[132:135], v[124:127], v[164:167], v[132:135]
	v_mfma_f32_16x16x32_bf16 v[128:131], v[140:143], v[164:167], v[128:131]
	v_mfma_f32_16x16x32_bf16 v[108:111], v[124:127], v[182:185], v[108:111]
	v_mfma_f32_16x16x32_bf16 v[104:107], v[140:143], v[182:185], v[104:107]
	v_mfma_f32_16x16x32_bf16 v[92:95], v[124:127], v[190:193], v[92:95]
	v_mfma_f32_16x16x32_bf16 v[88:91], v[140:143], v[190:193], v[88:91]
	v_mfma_f32_16x16x32_bf16 v[76:79], v[124:127], v[198:201], v[76:79]
	v_mfma_f32_16x16x32_bf16 v[72:75], v[140:143], v[198:201], v[72:75]
	v_mfma_f32_16x16x32_bf16 v[120:123], v[144:147], v[160:163], 0
	v_mfma_f32_16x16x32_bf16 v[116:119], v[152:155], v[160:163], 0
	v_mfma_f32_16x16x32_bf16 v[100:103], v[144:147], v[178:181], 0
	v_mfma_f32_16x16x32_bf16 v[96:99], v[152:155], v[178:181], 0
	v_mfma_f32_16x16x32_bf16 v[84:87], v[144:147], v[186:189], 0
	v_mfma_f32_16x16x32_bf16 v[80:83], v[152:155], v[186:189], 0
	v_mfma_f32_16x16x32_bf16 v[68:71], v[144:147], v[194:197], 0
	v_mfma_f32_16x16x32_bf16 v[64:67], v[152:155], v[194:197], 0
	v_mfma_f32_16x16x32_bf16 v[120:123], v[148:151], v[164:167], v[120:123]
	v_mfma_f32_16x16x32_bf16 v[116:119], v[156:159], v[164:167], v[116:119]
	v_mfma_f32_16x16x32_bf16 v[100:103], v[148:151], v[182:185], v[100:103]
	v_mfma_f32_16x16x32_bf16 v[96:99], v[156:159], v[182:185], v[96:99]
	v_mfma_f32_16x16x32_bf16 v[84:87], v[148:151], v[190:193], v[84:87]
	v_mfma_f32_16x16x32_bf16 v[80:83], v[156:159], v[190:193], v[80:83]
	v_mfma_f32_16x16x32_bf16 v[68:71], v[148:151], v[198:201], v[68:71]
	v_mfma_f32_16x16x32_bf16 v[64:67], v[156:159], v[198:201], v[64:67]
	s_setprio 0
	s_barrier
	s_mov_b32 m0, s27
	s_mov_b32 s6, s38
	s_mov_b32 s7, s39
	buffer_load_dwordx4 v171, s[4:7], s55 offen lds
	s_mov_b32 m0, s28
	ds_read_b128 v[160:163], v177 offset:16384
	s_add_i32 s69, s55, s25
	buffer_load_dwordx4 v173, s[4:7], s55 offen lds
	s_mov_b32 m0, s29
	ds_read_b128 v[164:167], v177 offset:17408
	buffer_load_dwordx4 v171, s[4:7], s69 offen lds
	s_mov_b32 m0, s26
	ds_read_b128 v[178:181], v177 offset:18432
	buffer_load_dwordx4 v170, s[36:39], s68 offen lds
	s_mov_b32 m0, s31
	ds_read_b128 v[182:185], v177 offset:19456
	buffer_load_dwordx4 v172, s[36:39], s68 offen lds
	ds_read_b128 v[186:189], v177 offset:20480
	ds_read_b128 v[190:193], v177 offset:21504
	ds_read_b128 v[194:197], v177 offset:22528
	ds_read_b128 v[198:201], v177 offset:23552
	s_waitcnt vmcnt(7)
	s_waitcnt lgkmcnt(0)
	s_barrier
	s_setprio 1
	v_mfma_f32_16x16x32_bf16 v[60:63], v[112:115], v[160:163], 0
	v_mfma_f32_16x16x32_bf16 v[56:59], v[136:139], v[160:163], 0
	v_mfma_f32_16x16x32_bf16 v[44:47], v[112:115], v[178:181], 0
	v_mfma_f32_16x16x32_bf16 v[40:43], v[136:139], v[178:181], 0
	v_mfma_f32_16x16x32_bf16 v[28:31], v[112:115], v[186:189], 0
	v_mfma_f32_16x16x32_bf16 v[24:27], v[136:139], v[186:189], 0
	v_mfma_f32_16x16x32_bf16 v[12:15], v[112:115], v[194:197], 0
	v_mfma_f32_16x16x32_bf16 v[8:11], v[136:139], v[194:197], 0
	v_mfma_f32_16x16x32_bf16 v[60:63], v[124:127], v[164:167], v[60:63]
	v_mfma_f32_16x16x32_bf16 v[56:59], v[140:143], v[164:167], v[56:59]
	v_mfma_f32_16x16x32_bf16 v[44:47], v[124:127], v[182:185], v[44:47]
	v_mfma_f32_16x16x32_bf16 v[40:43], v[140:143], v[182:185], v[40:43]
	v_mfma_f32_16x16x32_bf16 v[28:31], v[124:127], v[190:193], v[28:31]
	v_mfma_f32_16x16x32_bf16 v[24:27], v[140:143], v[190:193], v[24:27]
	v_mfma_f32_16x16x32_bf16 v[12:15], v[124:127], v[198:201], v[12:15]
	v_mfma_f32_16x16x32_bf16 v[8:11], v[140:143], v[198:201], v[8:11]
	v_mfma_f32_16x16x32_bf16 v[52:55], v[144:147], v[160:163], 0
	v_mfma_f32_16x16x32_bf16 v[48:51], v[152:155], v[160:163], 0
	v_mfma_f32_16x16x32_bf16 v[36:39], v[144:147], v[178:181], 0
	v_mfma_f32_16x16x32_bf16 v[32:35], v[152:155], v[178:181], 0
	v_mfma_f32_16x16x32_bf16 v[20:23], v[144:147], v[186:189], 0
	v_mfma_f32_16x16x32_bf16 v[16:19], v[152:155], v[186:189], 0
	v_mfma_f32_16x16x32_bf16 v[4:7], v[144:147], v[194:197], 0
	v_mfma_f32_16x16x32_bf16 v[0:3], v[152:155], v[194:197], 0
	v_mfma_f32_16x16x32_bf16 v[52:55], v[148:151], v[164:167], v[52:55]
	v_mfma_f32_16x16x32_bf16 v[48:51], v[156:159], v[164:167], v[48:51]
	v_mfma_f32_16x16x32_bf16 v[36:39], v[148:151], v[182:185], v[36:39]
	v_mfma_f32_16x16x32_bf16 v[32:35], v[156:159], v[182:185], v[32:35]
	v_mfma_f32_16x16x32_bf16 v[20:23], v[148:151], v[190:193], v[20:23]
	v_mfma_f32_16x16x32_bf16 v[16:19], v[156:159], v[190:193], v[16:19]
	v_mfma_f32_16x16x32_bf16 v[4:7], v[148:151], v[198:201], v[4:7]
	v_mfma_f32_16x16x32_bf16 v[0:3], v[156:159], v[198:201], v[0:3]
	s_setprio 0
	s_barrier
; #define PG8_STAGE(bufoff, rs_, soff_, voff) do { _Pragma("unroll") for (int _i = 0; _i < 2; ++_i) \
;         __builtin_amdgcn_raw_ptr_buffer_load_lds(rs_, (LAS void*)(lds + (bufoff) + ldsw + _i * 8192), 16, (int)(voff)[_i], (int)(soff_), 0, 0); } while (0)
; #define PG8_LDA(dst, b, h) do { _Pragma("unroll") for (int m = 0; m < 4; ++m) dst[m] = PG8_LD2(lds + PG8_SA(b, h) + aoff + m * 2048); } while (0)
; #define PG8_LDB(dst, b, h) do { _Pragma("unroll") for (int n = 0; n < 2; ++n) dst[n] = PG8_LD2(lds + PG8_SB(b, h) + boff + n * 2048); } while (0)
; #define PG8_WAIT_V(n) asm volatile("s_waitcnt vmcnt(" #n ")" ::: "memory")
; #define PG8_WAIT_L(n) asm volatile("s_waitcnt lgkmcnt(" #n ")" ::: "memory")
; #define PG8_BAR __builtin_amdgcn_s_barrier()
; #define PG8_SCHED __builtin_amdgcn_sched_barrier(0)
; template <class Epi, class Sched, bool ALIGN_EPI = false, bool SP2 = false, bool FP8 = false>
; __device__ __forceinline__ void gemm_phase(LAS unsigned char* lds, const Gemm g, const Sched& S, const Epi& E, int wbase) {
;     ...
;             PG8_LDB(B0, 1, 0); PG8_LDB(B1, 1, 1); PG8_SCHED; PG8_LDA(At, 1, 0); PG8_STAGE(PG8_SA(0, 1), rA2, a2 + hstep, voffA);
;             PG8_WAIT_V(8); PG8_WAIT_L(0); PG8_BAR; PG8_MMA(0, 0, At, B0); PG8_MMA(0, 1, At, B1); PG8_BAR; PG8_SCHED;
;             PG8_LDA(At, 1, 1); PG8_STAGE(PG8_SB(1, 0), rB2, b3, voffB); PG8_STAGE(PG8_SB(1, 1), rB2, b3 + hstep, voffB); PG8_STAGE(PG8_SA(1, 0), rA2, a3, voffA);
;             PG8_WAIT_V(8); PG8_WAIT_L(0); PG8_BAR; PG8_MMA(1, 0, At, B0); PG8_MMA(1, 1, At, B1); PG8_BAR; PG8_SCHED;
	s_mov_b32 m0, s30
	s_nop 0
	buffer_load_dwordx4 v173, s[4:7], s69 offen lds
	v_add_u32_e32 v140, 0x18000, v176
	v_add_u32_e32 v156, 0x1c000, v176
	ds_read_b128 v[112:115], v140
	ds_read_b128 v[124:127], v140 offset:1024
	ds_read_b128 v[136:139], v140 offset:2048
	ds_read_b128 v[140:143], v140 offset:3072
	ds_read_b128 v[144:147], v156
	ds_read_b128 v[148:151], v156 offset:1024
	ds_read_b128 v[152:155], v156 offset:2048
	ds_read_b128 v[156:159], v156 offset:3072
	s_add_i32 s68, s68, s25
	s_mov_b32 m0, s33
	ds_read_b128 v[160:163], v177 offset:32768
	ds_read_b128 v[164:167], v177 offset:33792
	ds_read_b128 v[178:181], v177 offset:34816
	ds_read_b128 v[182:185], v177 offset:35840
	ds_read_b128 v[186:189], v177 offset:36864
	ds_read_b128 v[190:193], v177 offset:37888
	ds_read_b128 v[194:197], v177 offset:38912
	ds_read_b128 v[198:201], v177 offset:39936
	buffer_load_dwordx4 v170, s[36:39], s68 offen lds
	s_mov_b32 m0, s34
	s_nop 0
	buffer_load_dwordx4 v172, s[36:39], s68 offen lds
	s_waitcnt vmcnt(8)
	s_waitcnt lgkmcnt(0)
	s_barrier
	s_setprio 1
	v_mfma_f32_16x16x32_bf16 v[132:135], v[112:115], v[160:163], v[132:135]
	v_mfma_f32_16x16x32_bf16 v[128:131], v[136:139], v[160:163], v[128:131]
	v_mfma_f32_16x16x32_bf16 v[108:111], v[112:115], v[178:181], v[108:111]
	v_mfma_f32_16x16x32_bf16 v[104:107], v[136:139], v[178:181], v[104:107]
	v_mfma_f32_16x16x32_bf16 v[92:95], v[112:115], v[186:189], v[92:95]
	v_mfma_f32_16x16x32_bf16 v[88:91], v[136:139], v[186:189], v[88:91]
	v_mfma_f32_16x16x32_bf16 v[76:79], v[112:115], v[194:197], v[76:79]
	v_mfma_f32_16x16x32_bf16 v[72:75], v[136:139], v[194:197], v[72:75]
	v_mfma_f32_16x16x32_bf16 v[132:135], v[124:127], v[164:167], v[132:135]
	v_mfma_f32_16x16x32_bf16 v[128:131], v[140:143], v[164:167], v[128:131]
	v_mfma_f32_16x16x32_bf16 v[108:111], v[124:127], v[182:185], v[108:111]
	v_mfma_f32_16x16x32_bf16 v[104:107], v[140:143], v[182:185], v[104:107]
	v_mfma_f32_16x16x32_bf16 v[92:95], v[124:127], v[190:193], v[92:95]
	v_mfma_f32_16x16x32_bf16 v[88:91], v[140:143], v[190:193], v[88:91]
	v_mfma_f32_16x16x32_bf16 v[76:79], v[124:127], v[198:201], v[76:79]
	v_mfma_f32_16x16x32_bf16 v[72:75], v[140:143], v[198:201], v[72:75]
	v_mfma_f32_16x16x32_bf16 v[120:123], v[144:147], v[160:163], v[120:123]
	v_mfma_f32_16x16x32_bf16 v[116:119], v[152:155], v[160:163], v[116:119]
	v_mfma_f32_16x16x32_bf16 v[100:103], v[144:147], v[178:181], v[100:103]
	v_mfma_f32_16x16x32_bf16 v[96:99], v[152:155], v[178:181], v[96:99]
	v_mfma_f32_16x16x32_bf16 v[84:87], v[144:147], v[186:189], v[84:87]
	v_mfma_f32_16x16x32_bf16 v[80:83], v[152:155], v[186:189], v[80:83]
	v_mfma_f32_16x16x32_bf16 v[68:71], v[144:147], v[194:197], v[68:71]
	v_mfma_f32_16x16x32_bf16 v[64:67], v[152:155], v[194:197], v[64:67]
	v_mfma_f32_16x16x32_bf16 v[120:123], v[148:151], v[164:167], v[120:123]
	v_mfma_f32_16x16x32_bf16 v[116:119], v[156:159], v[164:167], v[116:119]
	v_mfma_f32_16x16x32_bf16 v[100:103], v[148:151], v[182:185], v[100:103]
	v_mfma_f32_16x16x32_bf16 v[96:99], v[156:159], v[182:185], v[96:99]
	v_mfma_f32_16x16x32_bf16 v[84:87], v[148:151], v[190:193], v[84:87]
	v_mfma_f32_16x16x32_bf16 v[80:83], v[156:159], v[190:193], v[80:83]
	v_mfma_f32_16x16x32_bf16 v[68:71], v[148:151], v[198:201], v[68:71]
	v_mfma_f32_16x16x32_bf16 v[64:67], v[156:159], v[198:201], v[64:67]
	s_setprio 0
	s_barrier
	s_mov_b32 m0, s1
	s_bitset1_b32 s55, 7
	buffer_load_dwordx4 v171, s[4:7], s55 offen lds
	s_mov_b32 m0, s35
	ds_read_b128 v[160:163], v177 offset:49152
	buffer_load_dwordx4 v173, s[4:7], s55 offen lds
	s_add_i32 s55, s55, s25
	s_mov_b32 m0, s43
	ds_read_b128 v[164:167], v177 offset:50176
	buffer_load_dwordx4 v171, s[4:7], s55 offen lds
	s_mov_b32 m0, s44
	ds_read_b128 v[178:181], v177 offset:51200
	buffer_load_dwordx4 v173, s[4:7], s55 offen lds
	s_mov_b32 m0, s41
	ds_read_b128 v[182:185], v177 offset:52224
	buffer_load_dwordx4 v170, s[36:39], s54 offen lds
	s_mov_b32 m0, s42
	ds_read_b128 v[186:189], v177 offset:53248
	buffer_load_dwordx4 v172, s[36:39], s54 offen lds
	ds_read_b128 v[190:193], v177 offset:54272
	ds_read_b128 v[194:197], v177 offset:55296
	ds_read_b128 v[198:201], v177 offset:56320
	s_waitcnt vmcnt(8)
	s_waitcnt lgkmcnt(0)
	s_barrier
	s_setprio 1
	v_mfma_f32_16x16x32_bf16 v[60:63], v[112:115], v[160:163], v[60:63]
	v_mfma_f32_16x16x32_bf16 v[56:59], v[136:139], v[160:163], v[56:59]
	v_mfma_f32_16x16x32_bf16 v[44:47], v[112:115], v[178:181], v[44:47]
	v_mfma_f32_16x16x32_bf16 v[40:43], v[136:139], v[178:181], v[40:43]
	v_mfma_f32_16x16x32_bf16 v[28:31], v[112:115], v[186:189], v[28:31]
	v_mfma_f32_16x16x32_bf16 v[24:27], v[136:139], v[186:189], v[24:27]
	v_mfma_f32_16x16x32_bf16 v[12:15], v[112:115], v[194:197], v[12:15]
	v_mfma_f32_16x16x32_bf16 v[8:11], v[136:139], v[194:197], v[8:11]
	v_mfma_f32_16x16x32_bf16 v[60:63], v[124:127], v[164:167], v[60:63]
	v_mfma_f32_16x16x32_bf16 v[56:59], v[140:143], v[164:167], v[56:59]
	v_mfma_f32_16x16x32_bf16 v[44:47], v[124:127], v[182:185], v[44:47]
	v_mfma_f32_16x16x32_bf16 v[40:43], v[140:143], v[182:185], v[40:43]
	v_mfma_f32_16x16x32_bf16 v[28:31], v[124:127], v[190:193], v[28:31]
	v_mfma_f32_16x16x32_bf16 v[24:27], v[140:143], v[190:193], v[24:27]
	v_mfma_f32_16x16x32_bf16 v[12:15], v[124:127], v[198:201], v[12:15]
	v_mfma_f32_16x16x32_bf16 v[8:11], v[140:143], v[198:201], v[8:11]
	v_mfma_f32_16x16x32_bf16 v[52:55], v[144:147], v[160:163], v[52:55]
	v_mfma_f32_16x16x32_bf16 v[48:51], v[152:155], v[160:163], v[48:51]
	v_mfma_f32_16x16x32_bf16 v[36:39], v[144:147], v[178:181], v[36:39]
	v_mfma_f32_16x16x32_bf16 v[32:35], v[152:155], v[178:181], v[32:35]
	v_mfma_f32_16x16x32_bf16 v[20:23], v[144:147], v[186:189], v[20:23]
	v_mfma_f32_16x16x32_bf16 v[16:19], v[152:155], v[186:189], v[16:19]
	v_mfma_f32_16x16x32_bf16 v[4:7], v[144:147], v[194:197], v[4:7]
	v_mfma_f32_16x16x32_bf16 v[0:3], v[152:155], v[194:197], v[0:3]
	v_mfma_f32_16x16x32_bf16 v[52:55], v[148:151], v[164:167], v[52:55]
	v_mfma_f32_16x16x32_bf16 v[48:51], v[156:159], v[164:167], v[48:51]
	v_mfma_f32_16x16x32_bf16 v[36:39], v[148:151], v[182:185], v[36:39]
	v_mfma_f32_16x16x32_bf16 v[32:35], v[156:159], v[182:185], v[32:35]
	v_mfma_f32_16x16x32_bf16 v[20:23], v[148:151], v[190:193], v[20:23]
	v_mfma_f32_16x16x32_bf16 v[16:19], v[156:159], v[190:193], v[16:19]
	v_mfma_f32_16x16x32_bf16 v[4:7], v[148:151], v[198:201], v[4:7]
	v_mfma_f32_16x16x32_bf16 v[0:3], v[156:159], v[198:201], v[0:3]
	s_setprio 0
	s_barrier
	s_add_i32 s67, s67, 2
	s_addk_i32 s65, 0x100
	s_addk_i32 s66, 0x100
	s_cmp_ge_i32 s67, s47
	s_cbranch_scc0 .LBB0_1701
	s_branch .Lzp_after_1701

;     __device__ __forceinline__ unsigned a_off(const Unit& u, const Gemm& g) const { return (unsigned)u.pm * (unsigned)(BM * 2) * (unsigned)g.K; }
;     __device__ __forceinline__ unsigned b_off(const Unit& u, const Gemm& g) const { return (unsigned)u.pn * (unsigned)(BM * 2) * (unsigned)g.K; }
;     __device__ __forceinline__ bool next(int i, Unit& u) const { return so.next(i, u); }
;     __device__ __forceinline__ unsigned a_off(const Unit& u, const Gemm& g) const { return (unsigned)u.pm * (unsigned)(BM * 2) * (unsigned)g.K; }
;     __device__ __forceinline__ bool next(int i, Unit& u) const { const bool ok = so.next(i >> 1, u); u.part = i & 1; return ok; }
; template <class Epi, class Sched, bool ALIGN_EPI = false, bool SP2 = false, bool FP8 = false>
; __device__ __forceinline__ void gemm_phase(LAS unsigned char* lds, const Gemm g, const Sched& S, const Epi& E, int wbase) {
;     ...
;         const bool has_next = S.next(ui + 1, nxt);
;         const unsigned nA = has_next ? S.a_off(nxt, g) : cA, nB = has_next ? S.b_off(nxt, g) : cB;
;         const rsrc_t rAn = (Sched::TWO && has_next) ? (nxt.part ? rA1 : rA0) : rAc, rBn = (Sched::TWO && has_next) ? (nxt.part ? rB1 : rB0) : rBc;
;         float pre_[8] = {0.f, 0.f, 0.f, 0.f, 0.f, 0.f, 0.f, 0.f};
;         if constexpr (Epi::HAS_PRE) E.pre_load(pre_, cur, wr);
;         for (int t = 0; t < nt; t += 2) {
;             const bool last = (t == nt - 2);
;             const unsigned a1 = cA + (unsigned)(t + 1) * kstep;
;             const unsigned a2 = last ? nA : cA + (unsigned)(t + 2) * kstep, b2 = last ? nB : cB + (unsigned)(t + 2) * kstep; const rsrc_t rA2 = (Sched::TWO && last) ? rAn : rAc, rB2 = (Sched::TWO && last) ? rBn : rBc;
;             const unsigned a3 = a2 + kstep, b3 = b2 + kstep;
;             if (last && has_next) S.a_ready(nxt);
;             if constexpr (SP2) {
;             PG8_LDB(B0, 0, 0); PG8_LDB(B1, 0, 1); PG8_SCHED; PG8_LDA(At, 0, 0); PG8_STAGE(PG8_SA(1, 1), rAc, a1 + hstep, voffA);
;             PG8_WAIT_V(8); PG8_WAIT_L(0); PG8_BAR; PG8_MMA(0, 0, At, B0); PG8_MMA(0, 1, At, B1); PG8_BAR; PG8_SCHED;
;             PG8_LDA(At, 0, 1); PG8_STAGE(PG8_SB(0, 0), rB2, b2, voffB); PG8_STAGE(PG8_SB(0, 1), rB2, b2 + hstep, voffB); PG8_STAGE(PG8_SA(0, 0), rA2, a2, voffA);
;             PG8_WAIT_V(8); PG8_WAIT_L(0); PG8_BAR; PG8_MMA(1, 0, At, B0); PG8_MMA(1, 1, At, B1); PG8_BAR; PG8_SCHED;
.LBB0_1779:
	s_lshl_b32 s53, s52, 18
	s_andn2_b64 vcc, exec, s[14:15]
	s_lshl_b32 s56, s48, 18
	s_cbranch_vccnz .LBB0_1783
	s_and_b64 s[6:7], s[18:19], exec
	s_waitcnt vmcnt(22)
	v_mov_b32_e32 v225, 1
	v_mov_b32_e32 v223, v233
	v_mov_b32_e32 v222, 0x358637bd
	s_cselect_b32 s59, s53, s55
	s_cselect_b32 s60, s56, s54
	s_add_i32 s61, s55, 0x80
	s_add_i32 s62, s54, 0x100
	s_mov_b32 s63, 0
	v_add_u32_e32 v140, 0x10000, v154
	v_add_u32_e32 v144, 0x14000, v154
	ds_read_b128 v[128:131], v140
	ds_read_b128 v[132:135], v140 offset:1024
	ds_read_b128 v[136:139], v140 offset:2048
	ds_read_b128 v[140:143], v140 offset:3072
	ds_read_b128 v[156:159], v144
	ds_read_b128 v[160:163], v144 offset:1024
	ds_read_b128 v[164:167], v144 offset:2048
	ds_read_b128 v[168:171], v144 offset:3072
	s_add_i32 s6, s61, 0x80
	s_cmp_eq_u32 s45, s63
	s_cselect_b32 s65, s59, s6
	s_cselect_b32 s55, s60, s62
	s_or_b32 s54, s65, 0x80
	s_add_i32 s6, s21, s61
	s_mov_b32 m0, s46
	ds_read_b128 v[172:175], v155
	ds_read_b128 v[176:179], v155 offset:1024
	ds_read_b128 v[180:183], v155 offset:2048
	ds_read_b128 v[184:187], v155 offset:3072
	ds_read_b128 v[194:197], v155 offset:4096
	ds_read_b128 v[198:201], v155 offset:5120
	ds_read_b128 v[202:205], v155 offset:6144
	ds_read_b128 v[206:209], v155 offset:7168
	buffer_load_dwordx4 v148, s[36:39], s6 offen lds
	s_mov_b32 m0, s47
	s_nop 0
	buffer_load_dwordx4 v150, s[36:39], s6 offen lds
	s_waitcnt vmcnt(8)
	s_waitcnt lgkmcnt(0)
	s_barrier
	s_setprio 1
	v_mfma_f32_16x16x128_f8f6f4 v[120:123], v[128:135], v[172:179], 0
	v_mfma_f32_16x16x128_f8f6f4 v[124:127], v[136:143], v[172:179], 0
	v_mfma_f32_16x16x128_f8f6f4 v[104:107], v[128:135], v[180:187], 0
	v_mfma_f32_16x16x128_f8f6f4 v[108:111], v[136:143], v[180:187], 0
	v_mfma_f32_16x16x128_f8f6f4 v[144:147], v[128:135], v[194:201], 0
	v_mfma_f32_16x16x128_f8f6f4 v[188:191], v[136:143], v[194:201], 0
	v_mfma_f32_16x16x128_f8f6f4 v[210:213], v[128:135], v[202:209], 0
	v_mfma_f32_16x16x128_f8f6f4 v[214:217], v[136:143], v[202:209], 0
	v_mfma_f32_16x16x128_f8f6f4 v[112:115], v[156:163], v[172:179], 0
	v_mfma_f32_16x16x128_f8f6f4 v[116:119], v[164:171], v[172:179], 0
	v_mfma_f32_16x16x128_f8f6f4 v[96:99], v[156:163], v[180:187], 0
	v_mfma_f32_16x16x128_f8f6f4 v[100:103], v[164:171], v[180:187], 0
	v_mfma_f32_16x16x128_f8f6f4 v[172:175], v[156:163], v[194:201], 0
	v_mfma_f32_16x16x128_f8f6f4 v[176:179], v[164:171], v[194:201], 0
	v_mfma_f32_16x16x128_f8f6f4 v[180:183], v[156:163], v[202:209], 0
	v_mfma_f32_16x16x128_f8f6f4 v[184:187], v[164:171], v[202:209], 0
	s_setprio 0
	s_barrier
	s_mov_b32 m0, s23
	s_mov_b32 s6, s38
	s_mov_b32 s7, s39
	s_nop 0
	buffer_load_dwordx4 v149, s[4:7], s55 offen lds
	s_mov_b32 m0, s24
	ds_read_b128 v[64:67], v155 offset:16384
	s_add_i32 s66, s55, s21
	buffer_load_dwordx4 v151, s[4:7], s55 offen lds
	s_mov_b32 m0, s25
	ds_read_b128 v[68:71], v155 offset:17408
	buffer_load_dwordx4 v149, s[4:7], s66 offen lds
	s_mov_b32 m0, s22
	ds_read_b128 v[72:75], v155 offset:18432
	buffer_load_dwordx4 v148, s[36:39], s65 offen lds
	s_mov_b32 m0, s27
	ds_read_b128 v[76:79], v155 offset:19456
	buffer_load_dwordx4 v150, s[36:39], s65 offen lds
	ds_read_b128 v[80:83], v155 offset:20480
	ds_read_b128 v[84:87], v155 offset:21504
	ds_read_b128 v[88:91], v155 offset:22528
	ds_read_b128 v[92:95], v155 offset:23552
	s_waitcnt vmcnt(7)
	s_waitcnt lgkmcnt(0)
	s_barrier
	s_setprio 1
	v_mfma_f32_16x16x128_f8f6f4 v[56:59], v[128:135], v[64:71], 0
	v_mfma_f32_16x16x128_f8f6f4 v[60:63], v[136:143], v[64:71], 0
	v_mfma_f32_16x16x128_f8f6f4 v[8:11], v[128:135], v[88:95], 0
	v_mfma_f32_16x16x128_f8f6f4 v[192:195], v[128:135], v[72:79], 0
	v_mfma_f32_16x16x128_f8f6f4 v[196:199], v[136:143], v[72:79], 0
	v_mfma_f32_16x16x128_f8f6f4 v[200:203], v[128:135], v[80:87], 0
	v_mfma_f32_16x16x128_f8f6f4 v[204:207], v[136:143], v[80:87], 0
	v_mfma_f32_16x16x128_f8f6f4 v[218:221], v[136:143], v[88:95], 0
	v_mfma_f32_16x16x128_f8f6f4 v[52:55], v[164:171], v[64:71], 0
	v_mfma_f32_16x16x128_f8f6f4 v[226:229], v[156:163], v[64:71], 0
	v_mfma_f32_16x16x128_f8f6f4 v[230:233], v[156:163], v[72:79], 0
	v_mfma_f32_16x16x128_f8f6f4 v[234:237], v[164:171], v[72:79], 0
	v_mfma_f32_16x16x128_f8f6f4 v[238:241], v[156:163], v[80:87], 0
	v_mfma_f32_16x16x128_f8f6f4 v[242:245], v[164:171], v[80:87], 0
	v_mfma_f32_16x16x128_f8f6f4 v[246:249], v[156:163], v[88:95], 0
	v_mfma_f32_16x16x128_f8f6f4 v[250:253], v[164:171], v[88:95], 0
	s_setprio 0
	s_barrier
; #define PG8_STAGE(bufoff, rs_, soff_, voff) do { _Pragma("unroll") for (int _i = 0; _i < 2; ++_i) \
;         __builtin_amdgcn_raw_ptr_buffer_load_lds(rs_, (LAS void*)(lds + (bufoff) + ldsw + _i * 8192), 16, (int)(voff)[_i], (int)(soff_), 0, 0); } while (0)
; #define PG8_LDA(dst, b, h) do { _Pragma("unroll") for (int m = 0; m < 4; ++m) dst[m] = PG8_LD2(lds + PG8_SA(b, h) + aoff + m * 2048); } while (0)
; #define PG8_LDB(dst, b, h) do { _Pragma("unroll") for (int n = 0; n < 2; ++n) dst[n] = PG8_LD2(lds + PG8_SB(b, h) + boff + n * 2048); } while (0)
; #define PG8_WAIT_V(n) asm volatile("s_waitcnt vmcnt(" #n ")" ::: "memory")
; #define PG8_WAIT_L(n) asm volatile("s_waitcnt lgkmcnt(" #n ")" ::: "memory")
; #define PG8_BAR __builtin_amdgcn_s_barrier()
; #define PG8_SCHED __builtin_amdgcn_sched_barrier(0)
; template <class Epi, class Sched, bool ALIGN_EPI = false, bool SP2 = false, bool FP8 = false>
; __device__ __forceinline__ void gemm_phase(LAS unsigned char* lds, const Gemm g, const Sched& S, const Epi& E, int wbase) {
;     ...
;             PG8_LDB(B0, 1, 0); PG8_LDB(B1, 1, 1); PG8_SCHED; PG8_LDA(At, 1, 0); PG8_STAGE(PG8_SA(0, 1), rA2, a2 + hstep, voffA);
;             PG8_WAIT_V(8); PG8_WAIT_L(0); PG8_BAR; PG8_MMA(0, 0, At, B0); PG8_MMA(0, 1, At, B1); PG8_BAR; PG8_SCHED;
;             PG8_LDA(At, 1, 1); PG8_STAGE(PG8_SB(1, 0), rB2, b3, voffB); PG8_STAGE(PG8_SB(1, 1), rB2, b3 + hstep, voffB); PG8_STAGE(PG8_SA(1, 0), rA2, a3, voffA);
;             PG8_WAIT_V(8); PG8_WAIT_L(0); PG8_BAR; PG8_MMA(1, 0, At, B0); PG8_MMA(1, 1, At, B1); PG8_BAR; PG8_SCHED;
	s_mov_b32 m0, s26
	s_nop 0
	buffer_load_dwordx4 v151, s[4:7], s66 offen lds
	s_nop 1
	v_add_u32_e32 v16, 0x18000, v154
	v_add_u32_e32 v20, 0x1c000, v154
	s_nop 0
	ds_read_b128 v[0:3], v16
	ds_read_b128 v[4:7], v16 offset:1024
	ds_read_b128 v[12:15], v16 offset:2048
	ds_read_b128 v[16:19], v16 offset:3072
	ds_read_b128 v[128:131], v20
	ds_read_b128 v[132:135], v20 offset:1024
	ds_read_b128 v[136:139], v20 offset:2048
	ds_read_b128 v[140:143], v20 offset:3072
	s_add_i32 s65, s65, s21
	s_mov_b32 m0, s28
	ds_read_b128 v[20:23], v155 offset:32768
	ds_read_b128 v[24:27], v155 offset:33792
	ds_read_b128 v[28:31], v155 offset:34816
	ds_read_b128 v[32:35], v155 offset:35840
	ds_read_b128 v[36:39], v155 offset:36864
	ds_read_b128 v[40:43], v155 offset:37888
	ds_read_b128 v[44:47], v155 offset:38912
	ds_read_b128 v[48:51], v155 offset:39936
	buffer_load_dwordx4 v148, s[36:39], s65 offen lds
	s_mov_b32 m0, s29
	s_nop 0
	buffer_load_dwordx4 v150, s[36:39], s65 offen lds
	s_waitcnt vmcnt(8)
	s_waitcnt lgkmcnt(0)
	s_barrier
	s_setprio 1
	v_mfma_f32_16x16x128_f8f6f4 v[120:123], v[0:7], v[20:27], v[120:123]
	v_mfma_f32_16x16x128_f8f6f4 v[124:127], v[12:19], v[20:27], v[124:127]
	v_mfma_f32_16x16x128_f8f6f4 v[104:107], v[0:7], v[28:35], v[104:107]
	v_mfma_f32_16x16x128_f8f6f4 v[108:111], v[12:19], v[28:35], v[108:111]
	v_mfma_f32_16x16x128_f8f6f4 v[88:91], v[0:7], v[36:43], v[144:147]
	v_mfma_f32_16x16x128_f8f6f4 v[92:95], v[12:19], v[36:43], v[188:191]
	v_mfma_f32_16x16x128_f8f6f4 v[72:75], v[0:7], v[44:51], v[210:213]
	v_mfma_f32_16x16x128_f8f6f4 v[76:79], v[12:19], v[44:51], v[214:217]
	v_mfma_f32_16x16x128_f8f6f4 v[112:115], v[128:135], v[20:27], v[112:115]
	v_mfma_f32_16x16x128_f8f6f4 v[116:119], v[136:143], v[20:27], v[116:119]
	v_mfma_f32_16x16x128_f8f6f4 v[96:99], v[128:135], v[28:35], v[96:99]
	v_mfma_f32_16x16x128_f8f6f4 v[100:103], v[136:143], v[28:35], v[100:103]
	v_mfma_f32_16x16x128_f8f6f4 v[80:83], v[128:135], v[36:43], v[172:175]
	v_mfma_f32_16x16x128_f8f6f4 v[84:87], v[136:143], v[36:43], v[176:179]
	v_mfma_f32_16x16x128_f8f6f4 v[64:67], v[128:135], v[44:51], v[180:183]
	v_mfma_f32_16x16x128_f8f6f4 v[68:71], v[136:143], v[44:51], v[184:187]
	s_setprio 0
	s_barrier
	s_mov_b32 m0, s30
	s_bitset1_b32 s55, 7
	buffer_load_dwordx4 v149, s[4:7], s55 offen lds
	s_mov_b32 m0, s31
	ds_read_b128 v[32:35], v155 offset:49152
	buffer_load_dwordx4 v151, s[4:7], s55 offen lds
	s_add_i32 s55, s55, s21
	s_mov_b32 m0, s35
	ds_read_b128 v[36:39], v155 offset:50176
	buffer_load_dwordx4 v149, s[4:7], s55 offen lds
	s_mov_b32 m0, s41
	ds_read_b128 v[156:159], v155 offset:51200
	buffer_load_dwordx4 v151, s[4:7], s55 offen lds
	s_mov_b32 m0, s33
	ds_read_b128 v[160:163], v155 offset:52224
	buffer_load_dwordx4 v148, s[36:39], s54 offen lds
	s_mov_b32 m0, s34
	ds_read_b128 v[164:167], v155 offset:53248
	buffer_load_dwordx4 v150, s[36:39], s54 offen lds
	ds_read_b128 v[168:171], v155 offset:54272
	ds_read_b128 v[172:175], v155 offset:55296
	ds_read_b128 v[176:179], v155 offset:56320
	s_waitcnt vmcnt(8)
	s_waitcnt lgkmcnt(0)
	s_barrier
	s_setprio 1
	v_mfma_f32_16x16x128_f8f6f4 v[56:59], v[0:7], v[32:39], v[56:59]
	v_mfma_f32_16x16x128_f8f6f4 v[60:63], v[12:19], v[32:39], v[60:63]
	v_mfma_f32_16x16x128_f8f6f4 v[40:43], v[0:7], v[156:163], v[192:195]
	v_mfma_f32_16x16x128_f8f6f4 v[44:47], v[12:19], v[156:163], v[196:199]
	v_mfma_f32_16x16x128_f8f6f4 v[24:27], v[0:7], v[164:171], v[200:203]
	v_mfma_f32_16x16x128_f8f6f4 v[28:31], v[12:19], v[164:171], v[204:207]
	v_mfma_f32_16x16x128_f8f6f4 v[8:11], v[0:7], v[172:179], v[8:11]
	v_mfma_f32_16x16x128_f8f6f4 v[12:15], v[12:19], v[172:179], v[218:221]
	v_mfma_f32_16x16x128_f8f6f4 v[48:51], v[128:135], v[32:39], v[226:229]
	v_mfma_f32_16x16x128_f8f6f4 v[52:55], v[136:143], v[32:39], v[52:55]
	v_mfma_f32_16x16x128_f8f6f4 v[32:35], v[128:135], v[156:163], v[230:233]
	v_mfma_f32_16x16x128_f8f6f4 v[36:39], v[136:143], v[156:163], v[234:237]
	v_mfma_f32_16x16x128_f8f6f4 v[16:19], v[128:135], v[164:171], v[238:241]
	v_mfma_f32_16x16x128_f8f6f4 v[20:23], v[136:143], v[164:171], v[242:245]
	v_mfma_f32_16x16x128_f8f6f4 v[4:7], v[128:135], v[172:179], v[246:249]
	v_mfma_f32_16x16x128_f8f6f4 v[0:3], v[136:143], v[172:179], v[250:253]
	s_setprio 0
	s_barrier
	s_add_i32 s63, s63, 2
	s_addk_i32 s61, 0x100
	s_addk_i32 s62, 0x100
	s_cmp_ge_i32 s63, s43
	s_cbranch_scc0 .LBB0_1781
	s_branch .Lzp_after_1781

;     __device__ __forceinline__ unsigned a_off(const Unit& u, const Gemm& g) const { return (unsigned)u.pm * (unsigned)(BM * 2) * (unsigned)g.K; }
;     __device__ __forceinline__ unsigned b_off(const Unit& u, const Gemm& g) const { return (unsigned)u.pn * (unsigned)(BM * 2) * (unsigned)g.K; }
;     __device__ __forceinline__ bool next(int i, Unit& u) const { return so.next(i, u); }
;     __device__ __forceinline__ unsigned a_off(const Unit& u, const Gemm& g) const { return (unsigned)u.pm * (unsigned)(BM * 2) * (unsigned)g.K; }
;     __device__ __forceinline__ bool next(int i, Unit& u) const { const bool ok = so.next(i >> 1, u); u.part = i & 1; return ok; }
; template <class Epi, class Sched, bool ALIGN_EPI = false, bool SP2 = false, bool FP8 = false>
; __device__ __forceinline__ void gemm_phase(LAS unsigned char* lds, const Gemm g, const Sched& S, const Epi& E, int wbase) {
;     ...
;         const bool has_next = S.next(ui + 1, nxt);
;         const unsigned nA = has_next ? S.a_off(nxt, g) : cA, nB = has_next ? S.b_off(nxt, g) : cB;
;         const rsrc_t rAn = (Sched::TWO && has_next) ? (nxt.part ? rA1 : rA0) : rAc, rBn = (Sched::TWO && has_next) ? (nxt.part ? rB1 : rB0) : rBc;
;         float pre_[8] = {0.f, 0.f, 0.f, 0.f, 0.f, 0.f, 0.f, 0.f};
;         if constexpr (Epi::HAS_PRE) E.pre_load(pre_, cur, wr);
;         for (int t = 0; t < nt; t += 2) {
;             const bool last = (t == nt - 2);
;             const unsigned a1 = cA + (unsigned)(t + 1) * kstep;
;             const unsigned a2 = last ? nA : cA + (unsigned)(t + 2) * kstep, b2 = last ? nB : cB + (unsigned)(t + 2) * kstep; const rsrc_t rA2 = (Sched::TWO && last) ? rAn : rAc, rB2 = (Sched::TWO && last) ? rBn : rBc;
;             const unsigned a3 = a2 + kstep, b3 = b2 + kstep;
;             if (last && has_next) S.a_ready(nxt);
;             if constexpr (SP2) {
;             PG8_LDB(B0, 0, 0); PG8_LDB(B1, 0, 1); PG8_SCHED; PG8_LDA(At, 0, 0); PG8_STAGE(PG8_SA(1, 1), rAc, a1 + hstep, voffA);
;             PG8_WAIT_V(8); PG8_WAIT_L(0); PG8_BAR; PG8_MMA(0, 0, At, B0); PG8_MMA(0, 1, At, B1); PG8_BAR; PG8_SCHED;
;             PG8_LDA(At, 0, 1); PG8_STAGE(PG8_SB(0, 0), rB2, b2, voffB); PG8_STAGE(PG8_SB(0, 1), rB2, b2 + hstep, voffB); PG8_STAGE(PG8_SA(0, 0), rA2, a2, voffA);
;             PG8_WAIT_V(8); PG8_WAIT_L(0); PG8_BAR; PG8_MMA(1, 0, At, B0); PG8_MMA(1, 1, At, B1); PG8_BAR; PG8_SCHED;
.LBB0_1852:
	s_mul_i32 s61, s60, 0xe0000
	s_andn2_b64 vcc, exec, s[14:15]
	s_mul_i32 s62, s59, 0xe0000
	s_cbranch_vccnz .LBB0_1856
	s_and_b64 s[6:7], s[18:19], exec
	s_waitcnt vmcnt(22)
	v_mov_b32_e32 v223, 0xff61b1e6
	v_mov_b32_e32 v222, 1
	v_mov_b32_e32 v169, v233
	v_mov_b32_e32 v168, 0x358637bd
	s_cselect_b32 s21, s61, s55
	s_cselect_b32 s63, s62, s54
	s_add_i32 s65, s55, 0x80
	s_add_i32 s66, s54, 0x100
	s_mov_b32 s67, 0
	v_add_u32_e32 v140, 0x10000, v176
	v_add_u32_e32 v156, 0x14000, v176
	ds_read_b128 v[128:131], v140
	ds_read_b128 v[132:135], v140 offset:1024
	ds_read_b128 v[136:139], v140 offset:2048
	ds_read_b128 v[140:143], v140 offset:3072
	ds_read_b128 v[144:147], v156
	ds_read_b128 v[148:151], v156 offset:1024
	ds_read_b128 v[152:155], v156 offset:2048
	ds_read_b128 v[156:159], v156 offset:3072
	s_add_i32 s6, s65, 0x80
	s_cmp_eq_u32 s52, s67
	s_cselect_b32 s68, s21, s6
	s_cselect_b32 s55, s63, s66
	s_or_b32 s54, s68, 0x80
	s_add_i32 s6, s24, s65
	s_mov_b32 m0, s53
	ds_read_b128 v[160:163], v177
	ds_read_b128 v[164:167], v177 offset:1024
	ds_read_b128 v[178:181], v177 offset:2048
	ds_read_b128 v[182:185], v177 offset:3072
	ds_read_b128 v[194:197], v177 offset:4096
	ds_read_b128 v[198:201], v177 offset:5120
	ds_read_b128 v[202:205], v177 offset:6144
	ds_read_b128 v[206:209], v177 offset:7168
	buffer_load_dwordx4 v170, s[36:39], s6 offen lds
	s_mov_b32 m0, s56
	s_nop 0
	buffer_load_dwordx4 v172, s[36:39], s6 offen lds
	s_waitcnt vmcnt(8)
	s_waitcnt lgkmcnt(0)
	s_barrier
	s_setprio 1
	v_mfma_f32_16x16x128_f8f6f4 v[124:127], v[128:135], v[160:167], 0
	v_mfma_f32_16x16x128_f8f6f4 v[120:123], v[136:143], v[160:167], 0
	v_mfma_f32_16x16x128_f8f6f4 v[108:111], v[128:135], v[178:185], 0
	v_mfma_f32_16x16x128_f8f6f4 v[104:107], v[136:143], v[178:185], 0
	v_mfma_f32_16x16x128_f8f6f4 v[186:189], v[128:135], v[194:201], 0
	v_mfma_f32_16x16x128_f8f6f4 v[190:193], v[136:143], v[194:201], 0
	v_mfma_f32_16x16x128_f8f6f4 v[210:213], v[128:135], v[202:209], 0
	v_mfma_f32_16x16x128_f8f6f4 v[214:217], v[136:143], v[202:209], 0
	v_mfma_f32_16x16x128_f8f6f4 v[116:119], v[144:151], v[160:167], 0
	v_mfma_f32_16x16x128_f8f6f4 v[112:115], v[152:159], v[160:167], 0
	v_mfma_f32_16x16x128_f8f6f4 v[100:103], v[144:151], v[178:185], 0
	v_mfma_f32_16x16x128_f8f6f4 v[96:99], v[152:159], v[178:185], 0
	v_mfma_f32_16x16x128_f8f6f4 v[160:163], v[144:151], v[194:201], 0
	v_mfma_f32_16x16x128_f8f6f4 v[164:167], v[152:159], v[194:201], 0
	v_mfma_f32_16x16x128_f8f6f4 v[178:181], v[144:151], v[202:209], 0
	v_mfma_f32_16x16x128_f8f6f4 v[182:185], v[152:159], v[202:209], 0
	s_setprio 0
	s_barrier
	s_mov_b32 m0, s26
	s_mov_b32 s6, s38
	s_mov_b32 s7, s39
	s_nop 1
	buffer_load_dwordx4 v171, s[4:7], s55 offen lds
	s_mov_b32 m0, s27
	ds_read_b128 v[64:67], v177 offset:16384
	s_add_i32 s69, s55, s24
	buffer_load_dwordx4 v173, s[4:7], s55 offen lds
	s_mov_b32 m0, s28
	ds_read_b128 v[68:71], v177 offset:17408
	buffer_load_dwordx4 v171, s[4:7], s69 offen lds
	s_mov_b32 m0, s25
	ds_read_b128 v[72:75], v177 offset:18432
	buffer_load_dwordx4 v170, s[36:39], s68 offen lds
	s_mov_b32 m0, s30
	ds_read_b128 v[76:79], v177 offset:19456
	buffer_load_dwordx4 v172, s[36:39], s68 offen lds
	ds_read_b128 v[80:83], v177 offset:20480
	ds_read_b128 v[84:87], v177 offset:21504
	ds_read_b128 v[88:91], v177 offset:22528
	ds_read_b128 v[92:95], v177 offset:23552
	s_waitcnt vmcnt(7)
	s_waitcnt lgkmcnt(0)
	s_barrier
	s_setprio 1
	v_mfma_f32_16x16x128_f8f6f4 v[60:63], v[128:135], v[64:71], 0
	v_mfma_f32_16x16x128_f8f6f4 v[56:59], v[136:143], v[64:71], 0
	v_mfma_f32_16x16x128_f8f6f4 v[194:197], v[128:135], v[72:79], 0
	v_mfma_f32_16x16x128_f8f6f4 v[198:201], v[136:143], v[72:79], 0
	v_mfma_f32_16x16x128_f8f6f4 v[202:205], v[128:135], v[80:87], 0
	v_mfma_f32_16x16x128_f8f6f4 v[206:209], v[136:143], v[80:87], 0
	v_mfma_f32_16x16x128_f8f6f4 v[218:221], v[128:135], v[88:95], 0
	v_mfma_f32_16x16x128_f8f6f4 v[226:229], v[136:143], v[88:95], 0
	v_mfma_f32_16x16x128_f8f6f4 v[52:55], v[144:151], v[64:71], 0
	v_mfma_f32_16x16x128_f8f6f4 v[48:51], v[152:159], v[64:71], 0
	v_mfma_f32_16x16x128_f8f6f4 v[230:233], v[144:151], v[72:79], 0
	v_mfma_f32_16x16x128_f8f6f4 v[234:237], v[152:159], v[72:79], 0
	v_mfma_f32_16x16x128_f8f6f4 v[238:241], v[144:151], v[80:87], 0
	v_mfma_f32_16x16x128_f8f6f4 v[242:245], v[152:159], v[80:87], 0
	v_mfma_f32_16x16x128_f8f6f4 v[246:249], v[144:151], v[88:95], 0
	v_mfma_f32_16x16x128_f8f6f4 v[250:253], v[152:159], v[88:95], 0
	s_setprio 0
	s_barrier
; #define PG8_STAGE(bufoff, rs_, soff_, voff) do { _Pragma("unroll") for (int _i = 0; _i < 2; ++_i) \
;         __builtin_amdgcn_raw_ptr_buffer_load_lds(rs_, (LAS void*)(lds + (bufoff) + ldsw + _i * 8192), 16, (int)(voff)[_i], (int)(soff_), 0, 0); } while (0)
; #define PG8_LDA(dst, b, h) do { _Pragma("unroll") for (int m = 0; m < 4; ++m) dst[m] = PG8_LD2(lds + PG8_SA(b, h) + aoff + m * 2048); } while (0)
; #define PG8_LDB(dst, b, h) do { _Pragma("unroll") for (int n = 0; n < 2; ++n) dst[n] = PG8_LD2(lds + PG8_SB(b, h) + boff + n * 2048); } while (0)
; #define PG8_WAIT_V(n) asm volatile("s_waitcnt vmcnt(" #n ")" ::: "memory")
; #define PG8_WAIT_L(n) asm volatile("s_waitcnt lgkmcnt(" #n ")" ::: "memory")
; #define PG8_BAR __builtin_amdgcn_s_barrier()
; #define PG8_SCHED __builtin_amdgcn_sched_barrier(0)
; template <class Epi, class Sched, bool ALIGN_EPI = false, bool SP2 = false, bool FP8 = false>
; __device__ __forceinline__ void gemm_phase(LAS unsigned char* lds, const Gemm g, const Sched& S, const Epi& E, int wbase) {
;     ...
;             PG8_LDB(B0, 1, 0); PG8_LDB(B1, 1, 1); PG8_SCHED; PG8_LDA(At, 1, 0); PG8_STAGE(PG8_SA(0, 1), rA2, a2 + hstep, voffA);
;             PG8_WAIT_V(8); PG8_WAIT_L(0); PG8_BAR; PG8_MMA(0, 0, At, B0); PG8_MMA(0, 1, At, B1); PG8_BAR; PG8_SCHED;
;             PG8_LDA(At, 1, 1); PG8_STAGE(PG8_SB(1, 0), rB2, b3, voffB); PG8_STAGE(PG8_SB(1, 1), rB2, b3 + hstep, voffB); PG8_STAGE(PG8_SA(1, 0), rA2, a3, voffA);
;             PG8_WAIT_V(8); PG8_WAIT_L(0); PG8_BAR; PG8_MMA(1, 0, At, B0); PG8_MMA(1, 1, At, B1); PG8_BAR; PG8_SCHED;
	s_mov_b32 m0, s29
	s_nop 0
	buffer_load_dwordx4 v173, s[4:7], s69 offen lds
	v_add_u32_e32 v8, 0x18000, v176
	s_nop 3
	ds_read_b128 v[0:3], v8
	ds_read_b128 v[4:7], v8 offset:1024
	ds_read_b128 v[16:19], v8 offset:2048
	ds_read_b128 v[20:23], v8 offset:3072
	v_add_u32_e32 v8, 0x1c000, v176
	ds_read_b128 v[128:131], v8
	ds_read_b128 v[132:135], v8 offset:1024
	ds_read_b128 v[136:139], v8 offset:2048
	ds_read_b128 v[140:143], v8 offset:3072
	s_add_i32 s68, s68, s24
	s_mov_b32 m0, s31
	ds_read_b128 v[8:11], v177 offset:32768
	ds_read_b128 v[12:15], v177 offset:33792
	ds_read_b128 v[24:27], v177 offset:34816
	ds_read_b128 v[28:31], v177 offset:35840
	ds_read_b128 v[32:35], v177 offset:36864
	ds_read_b128 v[36:39], v177 offset:37888
	ds_read_b128 v[40:43], v177 offset:38912
	ds_read_b128 v[44:47], v177 offset:39936
	buffer_load_dwordx4 v170, s[36:39], s68 offen lds
	s_mov_b32 m0, s33
	s_nop 0
	buffer_load_dwordx4 v172, s[36:39], s68 offen lds
	s_waitcnt vmcnt(8)
	s_waitcnt lgkmcnt(0)
	s_barrier
	s_setprio 1
	v_mfma_f32_16x16x128_f8f6f4 v[124:127], v[0:7], v[8:15], v[124:127]
	v_mfma_f32_16x16x128_f8f6f4 v[120:123], v[16:23], v[8:15], v[120:123]
	v_mfma_f32_16x16x128_f8f6f4 v[108:111], v[0:7], v[24:31], v[108:111]
	v_mfma_f32_16x16x128_f8f6f4 v[104:107], v[16:23], v[24:31], v[104:107]
	v_mfma_f32_16x16x128_f8f6f4 v[92:95], v[0:7], v[32:39], v[186:189]
	v_mfma_f32_16x16x128_f8f6f4 v[88:91], v[16:23], v[32:39], v[190:193]
	v_mfma_f32_16x16x128_f8f6f4 v[76:79], v[0:7], v[40:47], v[210:213]
	v_mfma_f32_16x16x128_f8f6f4 v[72:75], v[16:23], v[40:47], v[214:217]
	v_mfma_f32_16x16x128_f8f6f4 v[116:119], v[128:135], v[8:15], v[116:119]
	v_mfma_f32_16x16x128_f8f6f4 v[112:115], v[136:143], v[8:15], v[112:115]
	v_mfma_f32_16x16x128_f8f6f4 v[100:103], v[128:135], v[24:31], v[100:103]
	v_mfma_f32_16x16x128_f8f6f4 v[96:99], v[136:143], v[24:31], v[96:99]
	v_mfma_f32_16x16x128_f8f6f4 v[84:87], v[128:135], v[32:39], v[160:163]
	v_mfma_f32_16x16x128_f8f6f4 v[80:83], v[136:143], v[32:39], v[164:167]
	v_mfma_f32_16x16x128_f8f6f4 v[68:71], v[128:135], v[40:47], v[178:181]
	v_mfma_f32_16x16x128_f8f6f4 v[64:67], v[136:143], v[40:47], v[182:185]
	s_setprio 0
	s_barrier
	s_mov_b32 m0, s34
	s_bitset1_b32 s55, 7
	buffer_load_dwordx4 v171, s[4:7], s55 offen lds
	s_mov_b32 m0, s35
	ds_read_b128 v[32:35], v177 offset:49152
	buffer_load_dwordx4 v173, s[4:7], s55 offen lds
	s_add_i32 s55, s55, s24
	s_mov_b32 m0, s43
	ds_read_b128 v[36:39], v177 offset:50176
	buffer_load_dwordx4 v171, s[4:7], s55 offen lds
	s_mov_b32 m0, s44
	ds_read_b128 v[144:147], v177 offset:51200
	buffer_load_dwordx4 v173, s[4:7], s55 offen lds
	s_mov_b32 m0, s41
	ds_read_b128 v[148:151], v177 offset:52224
	buffer_load_dwordx4 v170, s[36:39], s54 offen lds
	s_mov_b32 m0, s42
	ds_read_b128 v[152:155], v177 offset:53248
	buffer_load_dwordx4 v172, s[36:39], s54 offen lds
	ds_read_b128 v[156:159], v177 offset:54272
	ds_read_b128 v[160:163], v177 offset:55296
	ds_read_b128 v[164:167], v177 offset:56320
	s_waitcnt vmcnt(8)
	s_waitcnt lgkmcnt(0)
	s_barrier
	s_setprio 1
	v_mfma_f32_16x16x128_f8f6f4 v[60:63], v[0:7], v[32:39], v[60:63]
	v_mfma_f32_16x16x128_f8f6f4 v[56:59], v[16:23], v[32:39], v[56:59]
	v_mfma_f32_16x16x128_f8f6f4 v[44:47], v[0:7], v[144:151], v[194:197]
	v_mfma_f32_16x16x128_f8f6f4 v[40:43], v[16:23], v[144:151], v[198:201]
	v_mfma_f32_16x16x128_f8f6f4 v[28:31], v[0:7], v[152:159], v[202:205]
	v_mfma_f32_16x16x128_f8f6f4 v[24:27], v[16:23], v[152:159], v[206:209]
	v_mfma_f32_16x16x128_f8f6f4 v[12:15], v[0:7], v[160:167], v[218:221]
	v_mfma_f32_16x16x128_f8f6f4 v[8:11], v[16:23], v[160:167], v[226:229]
	v_mfma_f32_16x16x128_f8f6f4 v[52:55], v[128:135], v[32:39], v[52:55]
	v_mfma_f32_16x16x128_f8f6f4 v[48:51], v[136:143], v[32:39], v[48:51]
	v_mfma_f32_16x16x128_f8f6f4 v[36:39], v[128:135], v[144:151], v[230:233]
	v_mfma_f32_16x16x128_f8f6f4 v[32:35], v[136:143], v[144:151], v[234:237]
	v_mfma_f32_16x16x128_f8f6f4 v[20:23], v[128:135], v[152:159], v[238:241]
	v_mfma_f32_16x16x128_f8f6f4 v[16:19], v[136:143], v[152:159], v[242:245]
	v_mfma_f32_16x16x128_f8f6f4 v[4:7], v[128:135], v[160:167], v[246:249]
	v_mfma_f32_16x16x128_f8f6f4 v[0:3], v[136:143], v[160:167], v[250:253]
	s_setprio 0
	s_barrier
	s_add_i32 s67, s67, 2
	s_addk_i32 s65, 0x100
	s_addk_i32 s66, 0x100
	s_cmp_ge_i32 s67, s47
	s_cbranch_scc0 .LBB0_1854
	s_branch .Lzp_after_1854

;     __device__ __forceinline__ unsigned a_off(const Unit& u, const Gemm& g) const { return (unsigned)u.pm * (unsigned)(BM * 2) * (unsigned)g.K; }
;     __device__ __forceinline__ unsigned b_off(const Unit& u, const Gemm& g) const { return (unsigned)u.pn * (unsigned)(BM * 2) * (unsigned)g.K; }
;     __device__ __forceinline__ bool next(int i, Unit& u) const { return so.next(i, u); }
;     __device__ __forceinline__ unsigned a_off(const Unit& u, const Gemm& g) const { return (unsigned)u.pm * (unsigned)(BM * 2) * (unsigned)g.K; }
;     __device__ __forceinline__ bool next(int i, Unit& u) const { const bool ok = so.next(i >> 1, u); u.part = i & 1; return ok; }
; template <class Epi, class Sched, bool ALIGN_EPI = false, bool SP2 = false, bool FP8 = false>
; __device__ __forceinline__ void gemm_phase(LAS unsigned char* lds, const Gemm g, const Sched& S, const Epi& E, int wbase) {
;     ...
;         const bool has_next = S.next(ui + 1, nxt);
;         const unsigned nA = has_next ? S.a_off(nxt, g) : cA, nB = has_next ? S.b_off(nxt, g) : cB;
;         const rsrc_t rAn = (Sched::TWO && has_next) ? (nxt.part ? rA1 : rA0) : rAc, rBn = (Sched::TWO && has_next) ? (nxt.part ? rB1 : rB0) : rBc;
;         float pre_[8] = {0.f, 0.f, 0.f, 0.f, 0.f, 0.f, 0.f, 0.f};
;         if constexpr (Epi::HAS_PRE) E.pre_load(pre_, cur, wr);
;         for (int t = 0; t < nt; t += 2) {
;             const bool last = (t == nt - 2);
;             const unsigned a1 = cA + (unsigned)(t + 1) * kstep;
;             const unsigned a2 = last ? nA : cA + (unsigned)(t + 2) * kstep, b2 = last ? nB : cB + (unsigned)(t + 2) * kstep; const rsrc_t rA2 = (Sched::TWO && last) ? rAn : rAc, rB2 = (Sched::TWO && last) ? rBn : rBc;
;             const unsigned a3 = a2 + kstep, b3 = b2 + kstep;
;             if (last && has_next) S.a_ready(nxt);
;             if constexpr (SP2) {
;             PG8_LDB(B0, 0, 0); PG8_LDB(B1, 0, 1); PG8_SCHED; PG8_LDA(At, 0, 0); PG8_STAGE(PG8_SA(1, 1), rAc, a1 + hstep, voffA);
;             PG8_WAIT_V(8); PG8_WAIT_L(0); PG8_BAR; PG8_MMA(0, 0, At, B0); PG8_MMA(0, 1, At, B1); PG8_BAR; PG8_SCHED;
;             PG8_LDA(At, 0, 1); PG8_STAGE(PG8_SB(0, 0), rB2, b2, voffB); PG8_STAGE(PG8_SB(0, 1), rB2, b2 + hstep, voffB); PG8_STAGE(PG8_SA(0, 0), rA2, a2, voffA);
;             PG8_WAIT_V(8); PG8_WAIT_L(0); PG8_BAR; PG8_MMA(1, 0, At, B0); PG8_MMA(1, 1, At, B1); PG8_BAR; PG8_SCHED;
.LBB0_1942:
	s_mov_b32 s68, s94
	s_lshl_b32 s85, s84, 19
	s_andn2_b64 vcc, exec, s[22:23]
	s_lshl_b32 s94, s83, 19
	s_cbranch_vccnz .LBB0_1966
	s_and_b64 s[6:7], s[26:27], exec
	s_waitcnt vmcnt(23)
	s_cselect_b32 s29, s85, s55
	s_cselect_b32 s60, s94, s54
	s_add_i32 s61, s55, 0x80
	s_add_i32 s62, s54, 0x100
	s_mov_b32 s63, 0
	s_waitcnt vmcnt(0)
	v_add_u32_e32 v136, 0x10000, v174
	v_add_u32_e32 v156, 0x14000, v174
	ds_read_b128 v[120:123], v136
	ds_read_b128 v[124:127], v136 offset:1024
	ds_read_b128 v[132:135], v136 offset:2048
	ds_read_b128 v[136:139], v136 offset:3072
	ds_read_b128 v[144:147], v156
	ds_read_b128 v[148:151], v156 offset:1024
	ds_read_b128 v[152:155], v156 offset:2048
	ds_read_b128 v[156:159], v156 offset:3072
	s_add_i32 s6, s61, 0x80
	s_cmp_eq_u32 s77, s63
	s_cselect_b32 s66, s29, s6
	s_cselect_b32 s55, s60, s62
	s_or_b32 s54, s66, 0x80
	s_add_i32 s6, s33, s61
	s_mov_b32 m0, s79
	ds_read_b128 v[160:163], v175
	ds_read_b128 v[164:167], v175 offset:1024
	ds_read_b128 v[176:179], v175 offset:2048
	ds_read_b128 v[180:183], v175 offset:3072
	ds_read_b128 v[184:187], v175 offset:4096
	ds_read_b128 v[188:191], v175 offset:5120
	ds_read_b128 v[192:195], v175 offset:6144
	ds_read_b128 v[196:199], v175 offset:7168
	buffer_load_dwordx4 v168, s[36:39], s6 offen lds
	s_mov_b32 m0, s82
	s_nop 0
	buffer_load_dwordx4 v170, s[36:39], s6 offen lds
	s_waitcnt vmcnt(8)
	s_waitcnt lgkmcnt(0)
	s_barrier
	s_setprio 1
	v_mfma_f32_16x16x32_bf16 v[140:143], v[120:123], v[160:163], 0
	v_mfma_f32_16x16x32_bf16 v[128:131], v[132:135], v[160:163], 0
	v_mfma_f32_16x16x32_bf16 v[108:111], v[120:123], v[176:179], 0
	v_mfma_f32_16x16x32_bf16 v[104:107], v[132:135], v[176:179], 0
	v_mfma_f32_16x16x32_bf16 v[92:95], v[120:123], v[184:187], 0
	v_mfma_f32_16x16x32_bf16 v[88:91], v[132:135], v[184:187], 0
	v_mfma_f32_16x16x32_bf16 v[76:79], v[120:123], v[192:195], 0
	v_mfma_f32_16x16x32_bf16 v[72:75], v[132:135], v[192:195], 0
	v_mfma_f32_16x16x32_bf16 v[140:143], v[124:127], v[164:167], v[140:143]
	v_mfma_f32_16x16x32_bf16 v[128:131], v[136:139], v[164:167], v[128:131]
	v_mfma_f32_16x16x32_bf16 v[108:111], v[124:127], v[180:183], v[108:111]
	v_mfma_f32_16x16x32_bf16 v[104:107], v[136:139], v[180:183], v[104:107]
	v_mfma_f32_16x16x32_bf16 v[92:95], v[124:127], v[188:191], v[92:95]
	v_mfma_f32_16x16x32_bf16 v[88:91], v[136:139], v[188:191], v[88:91]
	v_mfma_f32_16x16x32_bf16 v[76:79], v[124:127], v[196:199], v[76:79]
	v_mfma_f32_16x16x32_bf16 v[72:75], v[136:139], v[196:199], v[72:75]
	v_mfma_f32_16x16x32_bf16 v[116:119], v[144:147], v[160:163], 0
	v_mfma_f32_16x16x32_bf16 v[112:115], v[152:155], v[160:163], 0
	v_mfma_f32_16x16x32_bf16 v[100:103], v[144:147], v[176:179], 0
	v_mfma_f32_16x16x32_bf16 v[96:99], v[152:155], v[176:179], 0
	v_mfma_f32_16x16x32_bf16 v[84:87], v[144:147], v[184:187], 0
	v_mfma_f32_16x16x32_bf16 v[80:83], v[152:155], v[184:187], 0
	v_mfma_f32_16x16x32_bf16 v[68:71], v[144:147], v[192:195], 0
	v_mfma_f32_16x16x32_bf16 v[64:67], v[152:155], v[192:195], 0
	v_mfma_f32_16x16x32_bf16 v[116:119], v[148:151], v[164:167], v[116:119]
	v_mfma_f32_16x16x32_bf16 v[112:115], v[156:159], v[164:167], v[112:115]
	v_mfma_f32_16x16x32_bf16 v[100:103], v[148:151], v[180:183], v[100:103]
	v_mfma_f32_16x16x32_bf16 v[96:99], v[156:159], v[180:183], v[96:99]
	v_mfma_f32_16x16x32_bf16 v[84:87], v[148:151], v[188:191], v[84:87]
	v_mfma_f32_16x16x32_bf16 v[80:83], v[156:159], v[188:191], v[80:83]
	v_mfma_f32_16x16x32_bf16 v[68:71], v[148:151], v[196:199], v[68:71]
	v_mfma_f32_16x16x32_bf16 v[64:67], v[156:159], v[196:199], v[64:67]
	s_setprio 0
	s_barrier
	s_mov_b32 m0, s35
	s_mov_b32 s6, s38
	s_mov_b32 s7, s39
	buffer_load_dwordx4 v169, s[4:7], s55 offen lds
	s_mov_b32 m0, s41
	ds_read_b128 v[160:163], v175 offset:16384
	s_add_i32 s67, s55, s33
	buffer_load_dwordx4 v171, s[4:7], s55 offen lds
	s_mov_b32 m0, s42
	ds_read_b128 v[164:167], v175 offset:17408
	buffer_load_dwordx4 v169, s[4:7], s67 offen lds
	s_mov_b32 m0, s34
	ds_read_b128 v[176:179], v175 offset:18432
	buffer_load_dwordx4 v168, s[36:39], s66 offen lds
	s_mov_b32 m0, s44
	ds_read_b128 v[180:183], v175 offset:19456
	buffer_load_dwordx4 v170, s[36:39], s66 offen lds
	ds_read_b128 v[184:187], v175 offset:20480
	ds_read_b128 v[188:191], v175 offset:21504
	ds_read_b128 v[192:195], v175 offset:22528
	ds_read_b128 v[196:199], v175 offset:23552
	s_waitcnt vmcnt(7)
	s_waitcnt lgkmcnt(0)
	s_barrier
	s_setprio 1
	v_mfma_f32_16x16x32_bf16 v[60:63], v[120:123], v[160:163], 0
	v_mfma_f32_16x16x32_bf16 v[56:59], v[132:135], v[160:163], 0
	v_mfma_f32_16x16x32_bf16 v[44:47], v[120:123], v[176:179], 0
	v_mfma_f32_16x16x32_bf16 v[40:43], v[132:135], v[176:179], 0
	v_mfma_f32_16x16x32_bf16 v[28:31], v[120:123], v[184:187], 0
	v_mfma_f32_16x16x32_bf16 v[24:27], v[132:135], v[184:187], 0
	v_mfma_f32_16x16x32_bf16 v[12:15], v[120:123], v[192:195], 0
	v_mfma_f32_16x16x32_bf16 v[8:11], v[132:135], v[192:195], 0
	v_mfma_f32_16x16x32_bf16 v[60:63], v[124:127], v[164:167], v[60:63]
	v_mfma_f32_16x16x32_bf16 v[56:59], v[136:139], v[164:167], v[56:59]
	v_mfma_f32_16x16x32_bf16 v[44:47], v[124:127], v[180:183], v[44:47]
	v_mfma_f32_16x16x32_bf16 v[40:43], v[136:139], v[180:183], v[40:43]
	v_mfma_f32_16x16x32_bf16 v[28:31], v[124:127], v[188:191], v[28:31]
	v_mfma_f32_16x16x32_bf16 v[24:27], v[136:139], v[188:191], v[24:27]
	v_mfma_f32_16x16x32_bf16 v[12:15], v[124:127], v[196:199], v[12:15]
	v_mfma_f32_16x16x32_bf16 v[8:11], v[136:139], v[196:199], v[8:11]
	v_mfma_f32_16x16x32_bf16 v[52:55], v[144:147], v[160:163], 0
	v_mfma_f32_16x16x32_bf16 v[48:51], v[152:155], v[160:163], 0
	v_mfma_f32_16x16x32_bf16 v[36:39], v[144:147], v[176:179], 0
	v_mfma_f32_16x16x32_bf16 v[32:35], v[152:155], v[176:179], 0
	v_mfma_f32_16x16x32_bf16 v[20:23], v[144:147], v[184:187], 0
	v_mfma_f32_16x16x32_bf16 v[16:19], v[152:155], v[184:187], 0
	v_mfma_f32_16x16x32_bf16 v[4:7], v[144:147], v[192:195], 0
	v_mfma_f32_16x16x32_bf16 v[0:3], v[152:155], v[192:195], 0
	v_mfma_f32_16x16x32_bf16 v[52:55], v[148:151], v[164:167], v[52:55]
	v_mfma_f32_16x16x32_bf16 v[48:51], v[156:159], v[164:167], v[48:51]
	v_mfma_f32_16x16x32_bf16 v[36:39], v[148:151], v[180:183], v[36:39]
	v_mfma_f32_16x16x32_bf16 v[32:35], v[156:159], v[180:183], v[32:35]
	v_mfma_f32_16x16x32_bf16 v[20:23], v[148:151], v[188:191], v[20:23]
	v_mfma_f32_16x16x32_bf16 v[16:19], v[156:159], v[188:191], v[16:19]
	v_mfma_f32_16x16x32_bf16 v[4:7], v[148:151], v[196:199], v[4:7]
	v_mfma_f32_16x16x32_bf16 v[0:3], v[156:159], v[196:199], v[0:3]
	s_setprio 0
	s_barrier
; #define PG8_STAGE(bufoff, rs_, soff_, voff) do { _Pragma("unroll") for (int _i = 0; _i < 2; ++_i) \
;         __builtin_amdgcn_raw_ptr_buffer_load_lds(rs_, (LAS void*)(lds + (bufoff) + ldsw + _i * 8192), 16, (int)(voff)[_i], (int)(soff_), 0, 0); } while (0)
; #define PG8_LDA(dst, b, h) do { _Pragma("unroll") for (int m = 0; m < 4; ++m) dst[m] = PG8_LD2(lds + PG8_SA(b, h) + aoff + m * 2048); } while (0)
; #define PG8_LDB(dst, b, h) do { _Pragma("unroll") for (int n = 0; n < 2; ++n) dst[n] = PG8_LD2(lds + PG8_SB(b, h) + boff + n * 2048); } while (0)
; #define PG8_WAIT_V(n) asm volatile("s_waitcnt vmcnt(" #n ")" ::: "memory")
; #define PG8_WAIT_L(n) asm volatile("s_waitcnt lgkmcnt(" #n ")" ::: "memory")
; #define PG8_BAR __builtin_amdgcn_s_barrier()
; #define PG8_SCHED __builtin_amdgcn_sched_barrier(0)
; template <class Epi, class Sched, bool ALIGN_EPI = false, bool SP2 = false, bool FP8 = false>
; __device__ __forceinline__ void gemm_phase(LAS unsigned char* lds, const Gemm g, const Sched& S, const Epi& E, int wbase) {
;     ...
;             PG8_LDB(B0, 1, 0); PG8_LDB(B1, 1, 1); PG8_SCHED; PG8_LDA(At, 1, 0); PG8_STAGE(PG8_SA(0, 1), rA2, a2 + hstep, voffA);
;             PG8_WAIT_V(8); PG8_WAIT_L(0); PG8_BAR; PG8_MMA(0, 0, At, B0); PG8_MMA(0, 1, At, B1); PG8_BAR; PG8_SCHED;
;             PG8_LDA(At, 1, 1); PG8_STAGE(PG8_SB(1, 0), rB2, b3, voffB); PG8_STAGE(PG8_SB(1, 1), rB2, b3 + hstep, voffB); PG8_STAGE(PG8_SA(1, 0), rA2, a3, voffA);
;             PG8_WAIT_V(8); PG8_WAIT_L(0); PG8_BAR; PG8_MMA(1, 0, At, B0); PG8_MMA(1, 1, At, B1); PG8_BAR; PG8_SCHED;
	s_mov_b32 m0, s43
	s_nop 0
	buffer_load_dwordx4 v171, s[4:7], s67 offen lds
	v_add_u32_e32 v136, 0x18000, v174
	v_add_u32_e32 v156, 0x1c000, v174
	ds_read_b128 v[120:123], v136
	ds_read_b128 v[124:127], v136 offset:1024
	ds_read_b128 v[132:135], v136 offset:2048
	ds_read_b128 v[136:139], v136 offset:3072
	ds_read_b128 v[144:147], v156
	ds_read_b128 v[148:151], v156 offset:1024
	ds_read_b128 v[152:155], v156 offset:2048
	ds_read_b128 v[156:159], v156 offset:3072
	s_add_i32 s66, s66, s33
	s_mov_b32 m0, s45
	ds_read_b128 v[160:163], v175 offset:32768
	ds_read_b128 v[164:167], v175 offset:33792
	ds_read_b128 v[176:179], v175 offset:34816
	ds_read_b128 v[180:183], v175 offset:35840
	ds_read_b128 v[184:187], v175 offset:36864
	ds_read_b128 v[188:191], v175 offset:37888
	ds_read_b128 v[192:195], v175 offset:38912
	ds_read_b128 v[196:199], v175 offset:39936
	buffer_load_dwordx4 v168, s[36:39], s66 offen lds
	s_mov_b32 m0, s46
	s_nop 0
	buffer_load_dwordx4 v170, s[36:39], s66 offen lds
	s_waitcnt vmcnt(8)
	s_waitcnt lgkmcnt(0)
	s_barrier
	s_setprio 1
	v_mfma_f32_16x16x32_bf16 v[140:143], v[120:123], v[160:163], v[140:143]
	v_mfma_f32_16x16x32_bf16 v[128:131], v[132:135], v[160:163], v[128:131]
	v_mfma_f32_16x16x32_bf16 v[108:111], v[120:123], v[176:179], v[108:111]
	v_mfma_f32_16x16x32_bf16 v[104:107], v[132:135], v[176:179], v[104:107]
	v_mfma_f32_16x16x32_bf16 v[92:95], v[120:123], v[184:187], v[92:95]
	v_mfma_f32_16x16x32_bf16 v[88:91], v[132:135], v[184:187], v[88:91]
	v_mfma_f32_16x16x32_bf16 v[76:79], v[120:123], v[192:195], v[76:79]
	v_mfma_f32_16x16x32_bf16 v[72:75], v[132:135], v[192:195], v[72:75]
	v_mfma_f32_16x16x32_bf16 v[140:143], v[124:127], v[164:167], v[140:143]
	v_mfma_f32_16x16x32_bf16 v[128:131], v[136:139], v[164:167], v[128:131]
	v_mfma_f32_16x16x32_bf16 v[108:111], v[124:127], v[180:183], v[108:111]
	v_mfma_f32_16x16x32_bf16 v[104:107], v[136:139], v[180:183], v[104:107]
	v_mfma_f32_16x16x32_bf16 v[92:95], v[124:127], v[188:191], v[92:95]
	v_mfma_f32_16x16x32_bf16 v[88:91], v[136:139], v[188:191], v[88:91]
	v_mfma_f32_16x16x32_bf16 v[76:79], v[124:127], v[196:199], v[76:79]
	v_mfma_f32_16x16x32_bf16 v[72:75], v[136:139], v[196:199], v[72:75]
	v_mfma_f32_16x16x32_bf16 v[116:119], v[144:147], v[160:163], v[116:119]
	v_mfma_f32_16x16x32_bf16 v[112:115], v[152:155], v[160:163], v[112:115]
	v_mfma_f32_16x16x32_bf16 v[100:103], v[144:147], v[176:179], v[100:103]
	v_mfma_f32_16x16x32_bf16 v[96:99], v[152:155], v[176:179], v[96:99]
	v_mfma_f32_16x16x32_bf16 v[84:87], v[144:147], v[184:187], v[84:87]
	v_mfma_f32_16x16x32_bf16 v[80:83], v[152:155], v[184:187], v[80:83]
	v_mfma_f32_16x16x32_bf16 v[68:71], v[144:147], v[192:195], v[68:71]
	v_mfma_f32_16x16x32_bf16 v[64:67], v[152:155], v[192:195], v[64:67]
	v_mfma_f32_16x16x32_bf16 v[116:119], v[148:151], v[164:167], v[116:119]
	v_mfma_f32_16x16x32_bf16 v[112:115], v[156:159], v[164:167], v[112:115]
	v_mfma_f32_16x16x32_bf16 v[100:103], v[148:151], v[180:183], v[100:103]
	v_mfma_f32_16x16x32_bf16 v[96:99], v[156:159], v[180:183], v[96:99]
	v_mfma_f32_16x16x32_bf16 v[84:87], v[148:151], v[188:191], v[84:87]
	v_mfma_f32_16x16x32_bf16 v[80:83], v[156:159], v[188:191], v[80:83]
	v_mfma_f32_16x16x32_bf16 v[68:71], v[148:151], v[196:199], v[68:71]
	v_mfma_f32_16x16x32_bf16 v[64:67], v[156:159], v[196:199], v[64:67]
	s_setprio 0
	s_barrier
	s_mov_b32 m0, s47
	s_bitset1_b32 s55, 7
	buffer_load_dwordx4 v169, s[4:7], s55 offen lds
	s_mov_b32 m0, s48
	ds_read_b128 v[160:163], v175 offset:49152
	buffer_load_dwordx4 v171, s[4:7], s55 offen lds
	s_add_i32 s55, s55, s33
	s_mov_b32 m0, s56
	ds_read_b128 v[164:167], v175 offset:50176
	buffer_load_dwordx4 v169, s[4:7], s55 offen lds
	s_mov_b32 m0, s57
	ds_read_b128 v[176:179], v175 offset:51200
	buffer_load_dwordx4 v171, s[4:7], s55 offen lds
	s_mov_b32 m0, s52
	ds_read_b128 v[180:183], v175 offset:52224
	buffer_load_dwordx4 v168, s[36:39], s54 offen lds
	s_mov_b32 m0, s53
	ds_read_b128 v[184:187], v175 offset:53248
	buffer_load_dwordx4 v170, s[36:39], s54 offen lds
	ds_read_b128 v[188:191], v175 offset:54272
	ds_read_b128 v[192:195], v175 offset:55296
	ds_read_b128 v[196:199], v175 offset:56320
	s_waitcnt vmcnt(8)
	s_waitcnt lgkmcnt(0)
	s_barrier
	s_setprio 1
	v_mfma_f32_16x16x32_bf16 v[60:63], v[120:123], v[160:163], v[60:63]
	v_mfma_f32_16x16x32_bf16 v[56:59], v[132:135], v[160:163], v[56:59]
	v_mfma_f32_16x16x32_bf16 v[44:47], v[120:123], v[176:179], v[44:47]
	v_mfma_f32_16x16x32_bf16 v[40:43], v[132:135], v[176:179], v[40:43]
	v_mfma_f32_16x16x32_bf16 v[28:31], v[120:123], v[184:187], v[28:31]
	v_mfma_f32_16x16x32_bf16 v[24:27], v[132:135], v[184:187], v[24:27]
	v_mfma_f32_16x16x32_bf16 v[12:15], v[120:123], v[192:195], v[12:15]
	v_mfma_f32_16x16x32_bf16 v[8:11], v[132:135], v[192:195], v[8:11]
	v_mfma_f32_16x16x32_bf16 v[60:63], v[124:127], v[164:167], v[60:63]
	v_mfma_f32_16x16x32_bf16 v[56:59], v[136:139], v[164:167], v[56:59]
	v_mfma_f32_16x16x32_bf16 v[44:47], v[124:127], v[180:183], v[44:47]
	v_mfma_f32_16x16x32_bf16 v[40:43], v[136:139], v[180:183], v[40:43]
	v_mfma_f32_16x16x32_bf16 v[28:31], v[124:127], v[188:191], v[28:31]
	v_mfma_f32_16x16x32_bf16 v[24:27], v[136:139], v[188:191], v[24:27]
	v_mfma_f32_16x16x32_bf16 v[12:15], v[124:127], v[196:199], v[12:15]
	v_mfma_f32_16x16x32_bf16 v[8:11], v[136:139], v[196:199], v[8:11]
	v_mfma_f32_16x16x32_bf16 v[52:55], v[144:147], v[160:163], v[52:55]
	v_mfma_f32_16x16x32_bf16 v[48:51], v[152:155], v[160:163], v[48:51]
	v_mfma_f32_16x16x32_bf16 v[36:39], v[144:147], v[176:179], v[36:39]
	v_mfma_f32_16x16x32_bf16 v[32:35], v[152:155], v[176:179], v[32:35]
	v_mfma_f32_16x16x32_bf16 v[20:23], v[144:147], v[184:187], v[20:23]
	v_mfma_f32_16x16x32_bf16 v[16:19], v[152:155], v[184:187], v[16:19]
	v_mfma_f32_16x16x32_bf16 v[4:7], v[144:147], v[192:195], v[4:7]
	v_mfma_f32_16x16x32_bf16 v[0:3], v[152:155], v[192:195], v[0:3]
	v_mfma_f32_16x16x32_bf16 v[52:55], v[148:151], v[164:167], v[52:55]
	v_mfma_f32_16x16x32_bf16 v[48:51], v[156:159], v[164:167], v[48:51]
	v_mfma_f32_16x16x32_bf16 v[36:39], v[148:151], v[180:183], v[36:39]
	v_mfma_f32_16x16x32_bf16 v[32:35], v[156:159], v[180:183], v[32:35]
	v_mfma_f32_16x16x32_bf16 v[20:23], v[148:151], v[188:191], v[20:23]
	v_mfma_f32_16x16x32_bf16 v[16:19], v[156:159], v[188:191], v[16:19]
	v_mfma_f32_16x16x32_bf16 v[4:7], v[148:151], v[196:199], v[4:7]
	v_mfma_f32_16x16x32_bf16 v[0:3], v[156:159], v[196:199], v[0:3]
	s_setprio 0
	s_barrier
	s_add_i32 s63, s63, 2
	s_addk_i32 s61, 0x100
	s_addk_i32 s62, 0x100
	s_cmp_ge_i32 s63, s65
	s_cbranch_scc0 .LBB0_1944
	s_branch .Lzp_after_1944

;     __device__ __forceinline__ unsigned a_off(const Unit& u, const Gemm& g) const { return (unsigned)u.pm * (unsigned)(BM * 2) * (unsigned)g.K; }
;     __device__ __forceinline__ unsigned b_off(const Unit& u, const Gemm& g) const { return (unsigned)u.pn * (unsigned)(BM * 2) * (unsigned)g.K; }
;     __device__ __forceinline__ bool next(int i, Unit& u) const { return so.next(i, u); }
;     __device__ __forceinline__ unsigned a_off(const Unit& u, const Gemm& g) const { return (unsigned)u.pm * (unsigned)(BM * 2) * (unsigned)g.K; }
;     __device__ __forceinline__ bool next(int i, Unit& u) const { const bool ok = so.next(i >> 1, u); u.part = i & 1; return ok; }
; template <class Epi, class Sched, bool ALIGN_EPI = false, bool SP2 = false, bool FP8 = false>
; __device__ __forceinline__ void gemm_phase(LAS unsigned char* lds, const Gemm g, const Sched& S, const Epi& E, int wbase) {
;     ...
;         const bool has_next = S.next(ui + 1, nxt);
;         const unsigned nA = has_next ? S.a_off(nxt, g) : cA, nB = has_next ? S.b_off(nxt, g) : cB;
;         const rsrc_t rAn = (Sched::TWO && has_next) ? (nxt.part ? rA1 : rA0) : rAc, rBn = (Sched::TWO && has_next) ? (nxt.part ? rB1 : rB0) : rBc;
;         float pre_[8] = {0.f, 0.f, 0.f, 0.f, 0.f, 0.f, 0.f, 0.f};
;         if constexpr (Epi::HAS_PRE) E.pre_load(pre_, cur, wr);
;         for (int t = 0; t < nt; t += 2) {
;             const bool last = (t == nt - 2);
;             const unsigned a1 = cA + (unsigned)(t + 1) * kstep;
;             const unsigned a2 = last ? nA : cA + (unsigned)(t + 2) * kstep, b2 = last ? nB : cB + (unsigned)(t + 2) * kstep; const rsrc_t rA2 = (Sched::TWO && last) ? rAn : rAc, rB2 = (Sched::TWO && last) ? rBn : rBc;
;             const unsigned a3 = a2 + kstep, b3 = b2 + kstep;
;             if (last && has_next) S.a_ready(nxt);
;             if constexpr (SP2) {
;             PG8_LDB(B0, 0, 0); PG8_LDB(B1, 0, 1); PG8_SCHED; PG8_LDA(At, 0, 0); PG8_STAGE(PG8_SA(1, 1), rAc, a1 + hstep, voffA);
;             PG8_WAIT_V(8); PG8_WAIT_L(0); PG8_BAR; PG8_MMA(0, 0, At, B0); PG8_MMA(0, 1, At, B1); PG8_BAR; PG8_SCHED;
;             PG8_LDA(At, 0, 1); PG8_STAGE(PG8_SB(0, 0), rB2, b2, voffB); PG8_STAGE(PG8_SB(0, 1), rB2, b2 + hstep, voffB); PG8_STAGE(PG8_SA(0, 0), rA2, a2, voffA);
;             PG8_WAIT_V(8); PG8_WAIT_L(0); PG8_BAR; PG8_MMA(1, 0, At, B0); PG8_MMA(1, 1, At, B1); PG8_BAR; PG8_SCHED;
.LBB0_1988:
	s_lshl_b32 s95, s94, 18
	s_andn2_b64 vcc, exec, s[26:27]
	s_lshl_b32 s96, s9, 18
	s_cbranch_vccnz .LBB0_1992
	s_and_b64 s[2:3], s[34:35], exec
	s_waitcnt vmcnt(23)
	v_mov_b32_e32 v223, 0xff61b1e6
	v_mov_b32_e32 v222, 1
	v_mov_b32_e32 v173, v233
	v_mov_b32_e32 v172, 0x358637bd
	s_cselect_b32 s2, s95, s4
	s_cselect_b32 s3, s96, s5
	s_addk_i32 s4, 0x80
	s_addk_i32 s5, 0x100
	s_mov_b32 s61, 0
	s_waitcnt vmcnt(0)
	v_add_u32_e32 v136, 0x10000, v180
	v_add_u32_e32 v156, 0x14000, v180
	ds_read_b128 v[120:123], v136
	ds_read_b128 v[124:127], v136 offset:1024
	ds_read_b128 v[132:135], v136 offset:2048
	ds_read_b128 v[136:139], v136 offset:3072
	ds_read_b128 v[144:147], v156
	ds_read_b128 v[148:151], v156 offset:1024
	ds_read_b128 v[152:155], v156 offset:2048
	ds_read_b128 v[156:159], v156 offset:3072
	s_add_i32 s14, s4, 0x80
	s_cmp_eq_u32 s84, s61
	s_cselect_b32 s62, s2, s14
	s_cselect_b32 s55, s3, s5
	s_or_b32 s54, s62, 0x80
	s_add_i32 s14, s42, s4
	s_mov_b32 m0, s85
	ds_read_b128 v[160:163], v181
	ds_read_b128 v[164:167], v181 offset:1024
	ds_read_b128 v[182:185], v181 offset:2048
	ds_read_b128 v[186:189], v181 offset:3072
	ds_read_b128 v[194:197], v181 offset:4096
	ds_read_b128 v[198:201], v181 offset:5120
	ds_read_b128 v[202:205], v181 offset:6144
	ds_read_b128 v[206:209], v181 offset:7168
	buffer_load_dwordx4 v174, s[36:39], s14 offen lds
	s_mov_b32 m0, s8
	s_nop 0
	buffer_load_dwordx4 v176, s[36:39], s14 offen lds
	s_waitcnt vmcnt(8)
	s_waitcnt lgkmcnt(0)
	s_barrier
	s_setprio 1
	v_mfma_f32_16x16x128_f8f6f4 v[140:143], v[120:127], v[160:167], 0
	v_mfma_f32_16x16x128_f8f6f4 v[128:131], v[132:139], v[160:167], 0
	v_mfma_f32_16x16x128_f8f6f4 v[108:111], v[120:127], v[182:189], 0
	v_mfma_f32_16x16x128_f8f6f4 v[104:107], v[132:139], v[182:189], 0
	v_mfma_f32_16x16x128_f8f6f4 v[168:171], v[120:127], v[194:201], 0
	v_mfma_f32_16x16x128_f8f6f4 v[190:193], v[132:139], v[194:201], 0
	v_mfma_f32_16x16x128_f8f6f4 v[210:213], v[120:127], v[202:209], 0
	v_mfma_f32_16x16x128_f8f6f4 v[214:217], v[132:139], v[202:209], 0
	v_mfma_f32_16x16x128_f8f6f4 v[116:119], v[144:151], v[160:167], 0
	v_mfma_f32_16x16x128_f8f6f4 v[112:115], v[152:159], v[160:167], 0
	v_mfma_f32_16x16x128_f8f6f4 v[100:103], v[144:151], v[182:189], 0
	v_mfma_f32_16x16x128_f8f6f4 v[96:99], v[152:159], v[182:189], 0
	v_mfma_f32_16x16x128_f8f6f4 v[160:163], v[144:151], v[194:201], 0
	v_mfma_f32_16x16x128_f8f6f4 v[164:167], v[152:159], v[194:201], 0
	v_mfma_f32_16x16x128_f8f6f4 v[182:185], v[144:151], v[202:209], 0
	v_mfma_f32_16x16x128_f8f6f4 v[186:189], v[152:159], v[202:209], 0
	s_setprio 0
	s_barrier
	s_mov_b32 m0, s44
	s_mov_b32 s14, s38
	s_mov_b32 s15, s39
	s_nop 1
	buffer_load_dwordx4 v175, s[12:15], s55 offen lds
	s_mov_b32 m0, s45
	ds_read_b128 v[64:67], v181 offset:16384
	s_add_i32 s63, s55, s42
	buffer_load_dwordx4 v177, s[12:15], s55 offen lds
	s_mov_b32 m0, s46
	ds_read_b128 v[68:71], v181 offset:17408
	buffer_load_dwordx4 v175, s[12:15], s63 offen lds
	s_mov_b32 m0, s43
	ds_read_b128 v[72:75], v181 offset:18432
	buffer_load_dwordx4 v174, s[36:39], s62 offen lds
	s_mov_b32 m0, s48
	ds_read_b128 v[76:79], v181 offset:19456
	buffer_load_dwordx4 v176, s[36:39], s62 offen lds
	ds_read_b128 v[80:83], v181 offset:20480
	ds_read_b128 v[84:87], v181 offset:21504
	ds_read_b128 v[88:91], v181 offset:22528
	ds_read_b128 v[92:95], v181 offset:23552
	s_waitcnt vmcnt(7)
	s_waitcnt lgkmcnt(0)
	s_barrier
	s_setprio 1
	v_mfma_f32_16x16x128_f8f6f4 v[60:63], v[120:127], v[64:71], 0
	v_mfma_f32_16x16x128_f8f6f4 v[56:59], v[132:139], v[64:71], 0
	v_mfma_f32_16x16x128_f8f6f4 v[194:197], v[120:127], v[72:79], 0
	v_mfma_f32_16x16x128_f8f6f4 v[198:201], v[132:139], v[72:79], 0
	v_mfma_f32_16x16x128_f8f6f4 v[202:205], v[120:127], v[80:87], 0
	v_mfma_f32_16x16x128_f8f6f4 v[206:209], v[132:139], v[80:87], 0
	v_mfma_f32_16x16x128_f8f6f4 v[218:221], v[120:127], v[88:95], 0
	v_mfma_f32_16x16x128_f8f6f4 v[226:229], v[132:139], v[88:95], 0
	v_mfma_f32_16x16x128_f8f6f4 v[52:55], v[144:151], v[64:71], 0
	v_mfma_f32_16x16x128_f8f6f4 v[48:51], v[152:159], v[64:71], 0
	v_mfma_f32_16x16x128_f8f6f4 v[230:233], v[144:151], v[72:79], 0
	v_mfma_f32_16x16x128_f8f6f4 v[234:237], v[152:159], v[72:79], 0
	v_mfma_f32_16x16x128_f8f6f4 v[238:241], v[144:151], v[80:87], 0
	v_mfma_f32_16x16x128_f8f6f4 v[242:245], v[152:159], v[80:87], 0
	v_mfma_f32_16x16x128_f8f6f4 v[246:249], v[144:151], v[88:95], 0
	v_mfma_f32_16x16x128_f8f6f4 v[250:253], v[152:159], v[88:95], 0
	s_setprio 0
	s_barrier
; #define PG8_STAGE(bufoff, rs_, soff_, voff) do { _Pragma("unroll") for (int _i = 0; _i < 2; ++_i) \
;         __builtin_amdgcn_raw_ptr_buffer_load_lds(rs_, (LAS void*)(lds + (bufoff) + ldsw + _i * 8192), 16, (int)(voff)[_i], (int)(soff_), 0, 0); } while (0)
; #define PG8_LDA(dst, b, h) do { _Pragma("unroll") for (int m = 0; m < 4; ++m) dst[m] = PG8_LD2(lds + PG8_SA(b, h) + aoff + m * 2048); } while (0)
; #define PG8_LDB(dst, b, h) do { _Pragma("unroll") for (int n = 0; n < 2; ++n) dst[n] = PG8_LD2(lds + PG8_SB(b, h) + boff + n * 2048); } while (0)
; #define PG8_WAIT_V(n) asm volatile("s_waitcnt vmcnt(" #n ")" ::: "memory")
; #define PG8_WAIT_L(n) asm volatile("s_waitcnt lgkmcnt(" #n ")" ::: "memory")
; #define PG8_BAR __builtin_amdgcn_s_barrier()
; #define PG8_SCHED __builtin_amdgcn_sched_barrier(0)
; template <class Epi, class Sched, bool ALIGN_EPI = false, bool SP2 = false, bool FP8 = false>
; __device__ __forceinline__ void gemm_phase(LAS unsigned char* lds, const Gemm g, const Sched& S, const Epi& E, int wbase) {
;     ...
;             PG8_LDB(B0, 1, 0); PG8_LDB(B1, 1, 1); PG8_SCHED; PG8_LDA(At, 1, 0); PG8_STAGE(PG8_SA(0, 1), rA2, a2 + hstep, voffA);
;             PG8_WAIT_V(8); PG8_WAIT_L(0); PG8_BAR; PG8_MMA(0, 0, At, B0); PG8_MMA(0, 1, At, B1); PG8_BAR; PG8_SCHED;
;             PG8_LDA(At, 1, 1); PG8_STAGE(PG8_SB(1, 0), rB2, b3, voffB); PG8_STAGE(PG8_SB(1, 1), rB2, b3 + hstep, voffB); PG8_STAGE(PG8_SA(1, 0), rA2, a3, voffA);
;             PG8_WAIT_V(8); PG8_WAIT_L(0); PG8_BAR; PG8_MMA(1, 0, At, B0); PG8_MMA(1, 1, At, B1); PG8_BAR; PG8_SCHED;
	s_mov_b32 m0, s47
	s_nop 0
	buffer_load_dwordx4 v177, s[12:15], s63 offen lds
	v_add_u32_e32 v8, 0x18000, v180
	s_nop 3
	ds_read_b128 v[0:3], v8
	ds_read_b128 v[4:7], v8 offset:1024
	ds_read_b128 v[16:19], v8 offset:2048
	ds_read_b128 v[20:23], v8 offset:3072
	v_add_u32_e32 v8, 0x1c000, v180
	ds_read_b128 v[120:123], v8
	ds_read_b128 v[124:127], v8 offset:1024
	ds_read_b128 v[132:135], v8 offset:2048
	ds_read_b128 v[136:139], v8 offset:3072
	s_add_i32 s62, s62, s42
	s_mov_b32 m0, s52
	ds_read_b128 v[8:11], v181 offset:32768
	ds_read_b128 v[12:15], v181 offset:33792
	ds_read_b128 v[24:27], v181 offset:34816
	ds_read_b128 v[28:31], v181 offset:35840
	ds_read_b128 v[32:35], v181 offset:36864
	ds_read_b128 v[36:39], v181 offset:37888
	ds_read_b128 v[40:43], v181 offset:38912
	ds_read_b128 v[44:47], v181 offset:39936
	buffer_load_dwordx4 v174, s[36:39], s62 offen lds
	s_mov_b32 m0, s53
	s_nop 0
	buffer_load_dwordx4 v176, s[36:39], s62 offen lds
	s_waitcnt vmcnt(8)
	s_waitcnt lgkmcnt(0)
	s_barrier
	s_setprio 1
	v_mfma_f32_16x16x128_f8f6f4 v[140:143], v[0:7], v[8:15], v[140:143]
	v_mfma_f32_16x16x128_f8f6f4 v[128:131], v[16:23], v[8:15], v[128:131]
	v_mfma_f32_16x16x128_f8f6f4 v[108:111], v[0:7], v[24:31], v[108:111]
	v_mfma_f32_16x16x128_f8f6f4 v[104:107], v[16:23], v[24:31], v[104:107]
	v_mfma_f32_16x16x128_f8f6f4 v[92:95], v[0:7], v[32:39], v[168:171]
	v_mfma_f32_16x16x128_f8f6f4 v[88:91], v[16:23], v[32:39], v[190:193]
	v_mfma_f32_16x16x128_f8f6f4 v[76:79], v[0:7], v[40:47], v[210:213]
	v_mfma_f32_16x16x128_f8f6f4 v[72:75], v[16:23], v[40:47], v[214:217]
	v_mfma_f32_16x16x128_f8f6f4 v[116:119], v[120:127], v[8:15], v[116:119]
	v_mfma_f32_16x16x128_f8f6f4 v[112:115], v[132:139], v[8:15], v[112:115]
	v_mfma_f32_16x16x128_f8f6f4 v[100:103], v[120:127], v[24:31], v[100:103]
	v_mfma_f32_16x16x128_f8f6f4 v[96:99], v[132:139], v[24:31], v[96:99]
	v_mfma_f32_16x16x128_f8f6f4 v[84:87], v[120:127], v[32:39], v[160:163]
	v_mfma_f32_16x16x128_f8f6f4 v[80:83], v[132:139], v[32:39], v[164:167]
	v_mfma_f32_16x16x128_f8f6f4 v[68:71], v[120:127], v[40:47], v[182:185]
	v_mfma_f32_16x16x128_f8f6f4 v[64:67], v[132:139], v[40:47], v[186:189]
	s_setprio 0
	s_barrier
	s_mov_b32 m0, s56
	s_bitset1_b32 s55, 7
	buffer_load_dwordx4 v175, s[12:15], s55 offen lds
	s_mov_b32 m0, s57
	ds_read_b128 v[32:35], v181 offset:49152
	buffer_load_dwordx4 v177, s[12:15], s55 offen lds
	s_add_i32 s55, s55, s42
	s_mov_b32 m0, s65
	ds_read_b128 v[36:39], v181 offset:50176
	buffer_load_dwordx4 v175, s[12:15], s55 offen lds
	s_mov_b32 m0, s76
	ds_read_b128 v[144:147], v181 offset:51200
	buffer_load_dwordx4 v177, s[12:15], s55 offen lds
	s_mov_b32 m0, s58
	ds_read_b128 v[148:151], v181 offset:52224
	buffer_load_dwordx4 v174, s[36:39], s54 offen lds
	s_mov_b32 m0, s59
	ds_read_b128 v[152:155], v181 offset:53248
	buffer_load_dwordx4 v176, s[36:39], s54 offen lds
	ds_read_b128 v[156:159], v181 offset:54272
	ds_read_b128 v[160:163], v181 offset:55296
	ds_read_b128 v[164:167], v181 offset:56320
	s_waitcnt vmcnt(8)
	s_waitcnt lgkmcnt(0)
	s_barrier
	s_setprio 1
	v_mfma_f32_16x16x128_f8f6f4 v[60:63], v[0:7], v[32:39], v[60:63]
	v_mfma_f32_16x16x128_f8f6f4 v[56:59], v[16:23], v[32:39], v[56:59]
	v_mfma_f32_16x16x128_f8f6f4 v[44:47], v[0:7], v[144:151], v[194:197]
	v_mfma_f32_16x16x128_f8f6f4 v[40:43], v[16:23], v[144:151], v[198:201]
	v_mfma_f32_16x16x128_f8f6f4 v[28:31], v[0:7], v[152:159], v[202:205]
	v_mfma_f32_16x16x128_f8f6f4 v[24:27], v[16:23], v[152:159], v[206:209]
	v_mfma_f32_16x16x128_f8f6f4 v[12:15], v[0:7], v[160:167], v[218:221]
	v_mfma_f32_16x16x128_f8f6f4 v[8:11], v[16:23], v[160:167], v[226:229]
	v_mfma_f32_16x16x128_f8f6f4 v[52:55], v[120:127], v[32:39], v[52:55]
	v_mfma_f32_16x16x128_f8f6f4 v[48:51], v[132:139], v[32:39], v[48:51]
	v_mfma_f32_16x16x128_f8f6f4 v[36:39], v[120:127], v[144:151], v[230:233]
	v_mfma_f32_16x16x128_f8f6f4 v[32:35], v[132:139], v[144:151], v[234:237]
	v_mfma_f32_16x16x128_f8f6f4 v[20:23], v[120:127], v[152:159], v[238:241]
	v_mfma_f32_16x16x128_f8f6f4 v[16:19], v[132:139], v[152:159], v[242:245]
	v_mfma_f32_16x16x128_f8f6f4 v[4:7], v[120:127], v[160:167], v[246:249]
	v_mfma_f32_16x16x128_f8f6f4 v[0:3], v[132:139], v[160:167], v[250:253]
	s_setprio 0
	s_barrier
	s_add_i32 s61, s61, 2
	s_addk_i32 s4, 0x100
	s_addk_i32 s5, 0x100
	s_cmp_ge_i32 s61, s82
	s_cbranch_scc0 .LBB0_1990
	s_branch .Lzp_after_1990
